# fp8 GEMM K-loops: last two of the six LDS-DMA pieces of SP2/SP4 load parts moved into the following MFMA block, wait vmcnt(8)->vmcnt(6) (30 of 34 parts; gathered SP2 parts skipped)
# speedup vs baseline: 1.0038x; 1.0030x over previous
.LBB0_236:
	ds_read_b128 v[20:23], v188
	ds_read_b128 v[24:27], v189
	ds_read_b128 v[16:19], v183
	ds_read_b128 v[0:3], v184
	ds_read_b128 v[28:31], v190
	ds_read_b128 v[4:7], v191
	ds_read_b128 v[8:11], v192
	ds_read_b128 v[12:15], v193
	s_add_u32 s42, s40, 0xfffe0080
	s_addc_u32 s43, s41, -1
	s_cmp_eq_u32 s58, 4
	s_cselect_b32 s45, s15, s43
	s_cselect_b32 s44, s54, s42
	s_cselect_b32 s43, s13, s57
	s_cselect_b32 s42, s55, s56
	v_lshl_add_u64 v[232:233], s[40:41], 0, v[168:169]
	s_add_i32 m0, s20, 0xc000
	ds_read_b128 v[174:177], v200
	ds_read_b128 v[178:181], v200 offset:1024
	ds_read_b128 v[208:211], v200 offset:2048
	ds_read_b128 v[212:215], v200 offset:3072
	ds_read_b128 v[216:219], v200 offset:4096
	ds_read_b128 v[220:223], v200 offset:5120
	ds_read_b128 v[224:227], v200 offset:6144
	ds_read_b128 v[228:231], v200 offset:7168
	global_load_lds_dwordx4 v[232:233], off
	v_lshl_add_u64 v[232:233], s[40:41], 0, v[170:171]
	s_add_i32 m0, s20, 0xe000
	s_nop 0
	global_load_lds_dwordx4 v[232:233], off
	s_waitcnt vmcnt(8)
	s_waitcnt lgkmcnt(0)
	s_barrier
	s_setprio 1
	s_waitcnt lgkmcnt(0)
	v_mfma_f32_16x16x128_f8f6f4 v[156:159], v[16:23], v[174:181], v[156:159]
	v_mfma_f32_16x16x128_f8f6f4 v[124:127], v[24:31], v[174:181], v[124:127]
	v_mfma_f32_16x16x128_f8f6f4 v[144:147], v[16:23], v[208:215], v[144:147]
	v_mfma_f32_16x16x128_f8f6f4 v[112:115], v[24:31], v[208:215], v[112:115]
	v_mfma_f32_16x16x128_f8f6f4 v[140:143], v[16:23], v[216:223], v[140:143]
	v_mfma_f32_16x16x128_f8f6f4 v[108:111], v[24:31], v[216:223], v[108:111]
	v_mfma_f32_16x16x128_f8f6f4 v[136:139], v[16:23], v[224:231], v[136:139]
	v_mfma_f32_16x16x128_f8f6f4 v[96:99], v[24:31], v[224:231], v[96:99]
	s_setprio 0
	s_setprio 1
	v_mfma_f32_16x16x128_f8f6f4 v[72:75], v[0:7], v[174:181], v[72:75]
	v_mfma_f32_16x16x128_f8f6f4 v[44:47], v[8:15], v[174:181], v[44:47]
	v_mfma_f32_16x16x128_f8f6f4 v[56:59], v[0:7], v[208:215], v[56:59]
	v_mfma_f32_16x16x128_f8f6f4 v[40:43], v[8:15], v[208:215], v[40:43]
	v_mfma_f32_16x16x128_f8f6f4 v[52:55], v[0:7], v[216:223], v[52:55]
	v_mfma_f32_16x16x128_f8f6f4 v[36:39], v[8:15], v[216:223], v[36:39]
	v_mfma_f32_16x16x128_f8f6f4 v[48:51], v[0:7], v[224:231], v[48:51]
	v_mfma_f32_16x16x128_f8f6f4 v[32:35], v[8:15], v[224:231], v[32:35]
	s_setprio 0
	s_barrier
	s_mov_b32 m0, s21
	v_lshl_add_u64 v[174:175], s[42:43], 0, v[162:163]
	s_add_u32 s60, s42, 0x20000
	ds_read_b128 v[208:211], v200 offset:16384
	ds_read_b128 v[212:215], v200 offset:17408
	ds_read_b128 v[216:219], v200 offset:18432
	ds_read_b128 v[220:223], v200 offset:19456
	ds_read_b128 v[224:227], v200 offset:20480
	ds_read_b128 v[228:231], v200 offset:21504
	ds_read_b128 v[232:235], v200 offset:22528
	ds_read_b128 v[236:239], v200 offset:23552
	global_load_lds_dwordx4 v[174:175], off
	v_lshl_add_u64 v[176:177], s[42:43], 0, v[160:161]
	s_mov_b32 m0, s22
	s_addc_u32 s61, s43, 0
	global_load_lds_dwordx4 v[176:177], off
	v_lshl_add_u64 v[178:179], s[60:61], 0, v[162:163]
	s_mov_b32 m0, s23
	v_lshl_add_u64 v[180:181], s[44:45], 0, v[166:167]
	global_load_lds_dwordx4 v[178:179], off
	v_lshl_add_u64 v[178:179], s[60:61], 0, v[160:161]
	s_mov_b32 m0, s24
	s_nop 0
	global_load_lds_dwordx4 v[178:179], off
	s_waitcnt vmcnt(6)
	s_waitcnt lgkmcnt(0)
	s_barrier
	s_setprio 1
	s_waitcnt lgkmcnt(0)
	v_mfma_f32_16x16x128_f8f6f4 v[128:131], v[16:23], v[208:215], v[128:131]
	v_mfma_f32_16x16x128_f8f6f4 v[84:87], v[24:31], v[208:215], v[84:87]
	v_mfma_f32_16x16x128_f8f6f4 v[116:119], v[16:23], v[216:223], v[116:119]
	v_mfma_f32_16x16x128_f8f6f4 v[64:67], v[24:31], v[216:223], v[64:67]
	v_mfma_f32_16x16x128_f8f6f4 v[148:151], v[16:23], v[224:231], v[148:151]
	v_mfma_f32_16x16x128_f8f6f4 v[120:123], v[24:31], v[224:231], v[120:123]
	v_mfma_f32_16x16x128_f8f6f4 v[152:155], v[16:23], v[232:239], v[152:155]
	v_mfma_f32_16x16x128_f8f6f4 v[132:135], v[24:31], v[232:239], v[132:135]
	s_setprio 0
	v_lshl_add_u64 v[178:179], s[44:45], 0, v[164:165]
	s_mov_b32 m0, s20
	s_nop 0
	global_load_lds_dwordx4 v[178:179], off
	s_mov_b32 m0, s25
	s_nop 0
	global_load_lds_dwordx4 v[180:181], off
	s_setprio 1
	v_mfma_f32_16x16x128_f8f6f4 v[88:91], v[0:7], v[208:215], v[88:91]
	v_mfma_f32_16x16x128_f8f6f4 v[60:63], v[8:15], v[208:215], v[60:63]
	v_mfma_f32_16x16x128_f8f6f4 v[92:95], v[0:7], v[216:223], v[92:95]
	v_mfma_f32_16x16x128_f8f6f4 v[68:71], v[8:15], v[216:223], v[68:71]
	v_mfma_f32_16x16x128_f8f6f4 v[100:103], v[0:7], v[224:231], v[100:103]
	v_mfma_f32_16x16x128_f8f6f4 v[76:79], v[8:15], v[224:231], v[76:79]
	v_mfma_f32_16x16x128_f8f6f4 v[104:107], v[0:7], v[232:239], v[104:107]
	v_mfma_f32_16x16x128_f8f6f4 v[80:83], v[8:15], v[232:239], v[80:83]
	s_setprio 0
	s_barrier
	ds_read_b128 v[4:7], v194
	ds_read_b128 v[8:11], v195
	ds_read_b128 v[0:3], v185
	ds_read_b128 v[16:19], v186
	ds_read_b128 v[12:15], v196
	ds_read_b128 v[20:23], v197
	ds_read_b128 v[24:27], v198
	ds_read_b128 v[28:31], v199
	s_add_u32 s44, s44, 0x20000
	s_addc_u32 s45, s45, 0
	s_mov_b32 m0, s26
	v_lshl_add_u64 v[240:241], s[44:45], 0, v[164:165]
	ds_read_b128 v[208:211], v200 offset:32768
	ds_read_b128 v[212:215], v200 offset:33792
	ds_read_b128 v[216:219], v200 offset:34816
	ds_read_b128 v[220:223], v200 offset:35840
	ds_read_b128 v[224:227], v200 offset:36864
	ds_read_b128 v[228:231], v200 offset:37888
	ds_read_b128 v[232:235], v200 offset:38912
	ds_read_b128 v[236:239], v200 offset:39936
	global_load_lds_dwordx4 v[240:241], off
	v_lshl_add_u64 v[240:241], s[44:45], 0, v[166:167]
	s_mov_b32 m0, s27
	s_nop 0
	global_load_lds_dwordx4 v[240:241], off
	s_waitcnt vmcnt(8)
	s_waitcnt lgkmcnt(0)
	s_barrier
	s_setprio 1
	s_waitcnt lgkmcnt(0)
	v_mfma_f32_16x16x128_f8f6f4 v[156:159], v[0:7], v[208:215], v[156:159]
	v_mfma_f32_16x16x128_f8f6f4 v[124:127], v[8:15], v[208:215], v[124:127]
	v_mfma_f32_16x16x128_f8f6f4 v[144:147], v[0:7], v[216:223], v[144:147]
	v_mfma_f32_16x16x128_f8f6f4 v[112:115], v[8:15], v[216:223], v[112:115]
	v_mfma_f32_16x16x128_f8f6f4 v[140:143], v[0:7], v[224:231], v[140:143]
	v_mfma_f32_16x16x128_f8f6f4 v[108:111], v[8:15], v[224:231], v[108:111]
	v_mfma_f32_16x16x128_f8f6f4 v[136:139], v[0:7], v[232:239], v[136:139]
	v_mfma_f32_16x16x128_f8f6f4 v[96:99], v[8:15], v[232:239], v[96:99]
	s_setprio 0
	s_setprio 1
	v_mfma_f32_16x16x128_f8f6f4 v[72:75], v[16:23], v[208:215], v[72:75]
	v_mfma_f32_16x16x128_f8f6f4 v[44:47], v[24:31], v[208:215], v[44:47]
	v_mfma_f32_16x16x128_f8f6f4 v[56:59], v[16:23], v[216:223], v[56:59]
	v_mfma_f32_16x16x128_f8f6f4 v[40:43], v[24:31], v[216:223], v[40:43]
	v_mfma_f32_16x16x128_f8f6f4 v[52:55], v[16:23], v[224:231], v[52:55]
	v_mfma_f32_16x16x128_f8f6f4 v[36:39], v[24:31], v[224:231], v[36:39]
	v_mfma_f32_16x16x128_f8f6f4 v[48:51], v[16:23], v[232:239], v[48:51]
	v_mfma_f32_16x16x128_f8f6f4 v[32:35], v[24:31], v[232:239], v[32:35]
	s_setprio 0
	s_barrier
	s_mov_b32 m0, s29
	v_lshl_add_u64 v[174:175], v[174:175], 0, s[8:9]
	s_add_u32 s42, s42, 0x20080
	ds_read_b128 v[208:211], v200 offset:49152
	ds_read_b128 v[212:215], v200 offset:50176
	ds_read_b128 v[216:219], v200 offset:51200
	ds_read_b128 v[220:223], v200 offset:52224
	ds_read_b128 v[224:227], v200 offset:53248
	ds_read_b128 v[228:231], v200 offset:54272
	ds_read_b128 v[232:235], v200 offset:55296
	ds_read_b128 v[236:239], v200 offset:56320
	global_load_lds_dwordx4 v[174:175], off
	v_lshl_add_u64 v[174:175], v[176:177], 0, s[8:9]
	s_mov_b32 m0, s30
	s_addc_u32 s43, s43, 0
	global_load_lds_dwordx4 v[174:175], off
	v_lshl_add_u64 v[174:175], s[42:43], 0, v[162:163]
	s_mov_b32 m0, s46
	s_nop 0
	global_load_lds_dwordx4 v[174:175], off
	v_lshl_add_u64 v[174:175], s[42:43], 0, v[160:161]
	s_mov_b32 m0, s47
	s_nop 0
	global_load_lds_dwordx4 v[174:175], off
	s_waitcnt vmcnt(6)
	s_waitcnt lgkmcnt(0)
	s_barrier
	s_setprio 1
	s_waitcnt lgkmcnt(0)
	v_mfma_f32_16x16x128_f8f6f4 v[128:131], v[0:7], v[208:215], v[128:131]
	v_mfma_f32_16x16x128_f8f6f4 v[84:87], v[8:15], v[208:215], v[84:87]
	v_mfma_f32_16x16x128_f8f6f4 v[116:119], v[0:7], v[216:223], v[116:119]
	v_mfma_f32_16x16x128_f8f6f4 v[64:67], v[8:15], v[216:223], v[64:67]
	v_mfma_f32_16x16x128_f8f6f4 v[148:151], v[0:7], v[224:231], v[148:151]
	v_mfma_f32_16x16x128_f8f6f4 v[120:123], v[8:15], v[224:231], v[120:123]
	v_mfma_f32_16x16x128_f8f6f4 v[152:155], v[0:7], v[232:239], v[152:155]
	v_mfma_f32_16x16x128_f8f6f4 v[132:135], v[8:15], v[232:239], v[132:135]
	s_setprio 0
	v_lshl_add_u64 v[174:175], v[178:179], 0, s[8:9]
	s_mov_b32 m0, s31
	s_nop 0
	global_load_lds_dwordx4 v[174:175], off
	v_lshl_add_u64 v[174:175], v[180:181], 0, s[8:9]
	s_mov_b32 m0, s33
	s_nop 0
	global_load_lds_dwordx4 v[174:175], off
	s_setprio 1
	v_mfma_f32_16x16x128_f8f6f4 v[88:91], v[16:23], v[208:215], v[88:91]
	v_mfma_f32_16x16x128_f8f6f4 v[60:63], v[24:31], v[208:215], v[60:63]
	v_mfma_f32_16x16x128_f8f6f4 v[92:95], v[16:23], v[216:223], v[92:95]
	v_mfma_f32_16x16x128_f8f6f4 v[68:71], v[24:31], v[216:223], v[68:71]
	v_mfma_f32_16x16x128_f8f6f4 v[100:103], v[16:23], v[224:231], v[100:103]
	v_mfma_f32_16x16x128_f8f6f4 v[76:79], v[24:31], v[224:231], v[76:79]
	v_mfma_f32_16x16x128_f8f6f4 v[104:107], v[16:23], v[232:239], v[104:107]
	v_mfma_f32_16x16x128_f8f6f4 v[80:83], v[24:31], v[232:239], v[80:83]
	s_setprio 0
	s_barrier
	s_add_i32 s58, s58, 2
	s_add_u32 s40, s40, 0x100
	s_addc_u32 s41, s41, 0
	s_add_u32 s56, s56, 0x100
	s_addc_u32 s57, s57, 0
	s_cmp_gt_u32 s58, 5
	s_cbranch_scc0 .LBB0_236
	s_nop 15
	s_nop 7
	s_and_b64 vcc, exec, s[10:11]
	s_cbranch_vccz .LBB0_239
	s_barrier

.LBB0_577:
	ds_read_b128 v[20:23], v184
	ds_read_b128 v[24:27], v185
	ds_read_b128 v[16:19], v180
	ds_read_b128 v[0:3], v181
	ds_read_b128 v[28:31], v186
	ds_read_b128 v[4:7], v187
	ds_read_b128 v[8:11], v188
	ds_read_b128 v[12:15], v189
	s_add_u32 s34, s90, s48
	s_addc_u32 s35, s91, s49
	s_add_u32 s55, s90, s50
	s_addc_u32 s56, s91, s51
	s_cmp_eq_u32 s52, 4
	s_cselect_b32 s37, s15, s35
	s_cselect_b32 s36, s14, s34
	s_cselect_b32 s35, s7, s56
	s_cselect_b32 s34, s6, s55
	s_mov_b32 m0, s53
	v_lshl_add_u64 v[222:223], s[90:91], 0, v[168:169]
	ds_read_b128 v[172:175], v196
	ds_read_b128 v[176:179], v196 offset:1024
	ds_read_b128 v[198:201], v196 offset:2048
	ds_read_b128 v[202:205], v196 offset:3072
	ds_read_b128 v[206:209], v196 offset:4096
	ds_read_b128 v[210:213], v196 offset:5120
	ds_read_b128 v[214:217], v196 offset:6144
	ds_read_b128 v[218:221], v196 offset:7168
	global_load_lds_dwordx4 v[222:223], off
	v_lshl_add_u64 v[222:223], s[90:91], 0, v[170:171]
	s_mov_b32 m0, s54
	s_nop 0
	global_load_lds_dwordx4 v[222:223], off
	s_waitcnt vmcnt(8)
	s_waitcnt lgkmcnt(0)
	s_barrier
	s_setprio 1
	s_waitcnt lgkmcnt(0)
	v_mfma_f32_16x16x128_f8f6f4 v[116:119], v[16:23], v[172:179], v[116:119]
	v_mfma_f32_16x16x128_f8f6f4 v[112:115], v[24:31], v[172:179], v[112:115]
	v_mfma_f32_16x16x128_f8f6f4 v[100:103], v[16:23], v[198:205], v[100:103]
	v_mfma_f32_16x16x128_f8f6f4 v[96:99], v[24:31], v[198:205], v[96:99]
	v_mfma_f32_16x16x128_f8f6f4 v[84:87], v[16:23], v[206:213], v[84:87]
	v_mfma_f32_16x16x128_f8f6f4 v[80:83], v[24:31], v[206:213], v[80:83]
	v_mfma_f32_16x16x128_f8f6f4 v[68:71], v[16:23], v[214:221], v[68:71]
	v_mfma_f32_16x16x128_f8f6f4 v[64:67], v[24:31], v[214:221], v[64:67]
	s_setprio 0
	s_setprio 1
	v_mfma_f32_16x16x128_f8f6f4 v[108:111], v[0:7], v[172:179], v[108:111]
	v_mfma_f32_16x16x128_f8f6f4 v[104:107], v[8:15], v[172:179], v[104:107]
	v_mfma_f32_16x16x128_f8f6f4 v[92:95], v[0:7], v[198:205], v[92:95]
	v_mfma_f32_16x16x128_f8f6f4 v[88:91], v[8:15], v[198:205], v[88:91]
	v_mfma_f32_16x16x128_f8f6f4 v[76:79], v[0:7], v[206:213], v[76:79]
	v_mfma_f32_16x16x128_f8f6f4 v[72:75], v[8:15], v[206:213], v[72:75]
	v_mfma_f32_16x16x128_f8f6f4 v[60:63], v[0:7], v[214:221], v[60:63]
	v_mfma_f32_16x16x128_f8f6f4 v[56:59], v[8:15], v[214:221], v[56:59]
	s_setprio 0
	s_barrier
	s_mov_b32 m0, s28
	v_lshl_add_u64 v[172:173], s[34:35], 0, v[122:123]
	s_add_u32 s56, s34, 0x20000
	ds_read_b128 v[198:201], v196 offset:16384
	ds_read_b128 v[202:205], v196 offset:17408
	ds_read_b128 v[206:209], v196 offset:18432
	ds_read_b128 v[210:213], v196 offset:19456
	ds_read_b128 v[214:217], v196 offset:20480
	ds_read_b128 v[218:221], v196 offset:21504
	ds_read_b128 v[222:225], v196 offset:22528
	ds_read_b128 v[226:229], v196 offset:23552
	global_load_lds_dwordx4 v[172:173], off
	v_lshl_add_u64 v[174:175], s[34:35], 0, v[120:121]
	s_mov_b32 m0, s29
	s_addc_u32 s57, s35, 0
	global_load_lds_dwordx4 v[174:175], off
	v_lshl_add_u64 v[176:177], s[56:57], 0, v[122:123]
	s_mov_b32 m0, s30
	v_lshl_add_u64 v[178:179], s[36:37], 0, v[126:127]
	global_load_lds_dwordx4 v[176:177], off
	v_lshl_add_u64 v[176:177], s[56:57], 0, v[120:121]
	s_mov_b32 m0, s31
	s_nop 0
	global_load_lds_dwordx4 v[176:177], off
	s_waitcnt vmcnt(6)
	s_waitcnt lgkmcnt(0)
	s_barrier
	s_setprio 1
	s_waitcnt lgkmcnt(0)
	v_mfma_f32_16x16x128_f8f6f4 v[48:51], v[16:23], v[198:205], v[48:51]
	v_mfma_f32_16x16x128_f8f6f4 v[40:43], v[24:31], v[198:205], v[40:43]
	v_mfma_f32_16x16x128_f8f6f4 v[44:47], v[16:23], v[206:213], v[44:47]
	v_mfma_f32_16x16x128_f8f6f4 v[32:35], v[24:31], v[206:213], v[32:35]
	v_mfma_f32_16x16x128_f8f6f4 v[36:39], v[16:23], v[214:221], v[36:39]
	v_mfma_f32_16x16x128_f8f6f4 v[144:147], v[24:31], v[214:221], v[144:147]
	v_mfma_f32_16x16x128_f8f6f4 v[128:131], v[16:23], v[222:229], v[128:131]
	v_mfma_f32_16x16x128_f8f6f4 v[132:135], v[24:31], v[222:229], v[132:135]
	s_setprio 0
	v_lshl_add_u64 v[176:177], s[36:37], 0, v[124:125]
	s_mov_b32 m0, s3
	s_nop 0
	global_load_lds_dwordx4 v[176:177], off
	s_mov_b32 m0, s33
	s_nop 0
	global_load_lds_dwordx4 v[178:179], off
	s_setprio 1
	v_mfma_f32_16x16x128_f8f6f4 v[52:55], v[0:7], v[198:205], v[52:55]
	v_mfma_f32_16x16x128_f8f6f4 v[164:167], v[8:15], v[198:205], v[164:167]
	v_mfma_f32_16x16x128_f8f6f4 v[156:159], v[0:7], v[206:213], v[156:159]
	v_mfma_f32_16x16x128_f8f6f4 v[160:163], v[8:15], v[206:213], v[160:163]
	v_mfma_f32_16x16x128_f8f6f4 v[148:151], v[0:7], v[214:221], v[148:151]
	v_mfma_f32_16x16x128_f8f6f4 v[152:155], v[8:15], v[214:221], v[152:155]
	v_mfma_f32_16x16x128_f8f6f4 v[140:143], v[0:7], v[222:229], v[140:143]
	v_mfma_f32_16x16x128_f8f6f4 v[136:139], v[8:15], v[222:229], v[136:139]
	s_setprio 0
	s_barrier
	ds_read_b128 v[4:7], v190
	ds_read_b128 v[8:11], v191
	ds_read_b128 v[0:3], v182
	ds_read_b128 v[16:19], v183
	ds_read_b128 v[12:15], v192
	ds_read_b128 v[20:23], v193
	ds_read_b128 v[24:27], v194
	ds_read_b128 v[28:31], v195
	s_add_u32 s36, s36, 0x20000
	s_addc_u32 s37, s37, 0
	s_mov_b32 m0, s40
	v_lshl_add_u64 v[230:231], s[36:37], 0, v[124:125]
	ds_read_b128 v[198:201], v196 offset:32768
	ds_read_b128 v[202:205], v196 offset:33792
	ds_read_b128 v[206:209], v196 offset:34816
	ds_read_b128 v[210:213], v196 offset:35840
	ds_read_b128 v[214:217], v196 offset:36864
	ds_read_b128 v[218:221], v196 offset:37888
	ds_read_b128 v[222:225], v196 offset:38912
	ds_read_b128 v[226:229], v196 offset:39936
	global_load_lds_dwordx4 v[230:231], off
	v_lshl_add_u64 v[230:231], s[36:37], 0, v[126:127]
	s_mov_b32 m0, s41
	s_nop 0
	global_load_lds_dwordx4 v[230:231], off
	s_waitcnt vmcnt(8)
	s_waitcnt lgkmcnt(0)
	s_barrier
	s_setprio 1
	s_waitcnt lgkmcnt(0)
	v_mfma_f32_16x16x128_f8f6f4 v[116:119], v[0:7], v[198:205], v[116:119]
	v_mfma_f32_16x16x128_f8f6f4 v[112:115], v[8:15], v[198:205], v[112:115]
	v_mfma_f32_16x16x128_f8f6f4 v[100:103], v[0:7], v[206:213], v[100:103]
	v_mfma_f32_16x16x128_f8f6f4 v[96:99], v[8:15], v[206:213], v[96:99]
	v_mfma_f32_16x16x128_f8f6f4 v[84:87], v[0:7], v[214:221], v[84:87]
	v_mfma_f32_16x16x128_f8f6f4 v[80:83], v[8:15], v[214:221], v[80:83]
	v_mfma_f32_16x16x128_f8f6f4 v[68:71], v[0:7], v[222:229], v[68:71]
	v_mfma_f32_16x16x128_f8f6f4 v[64:67], v[8:15], v[222:229], v[64:67]
	s_setprio 0
	s_setprio 1
	v_mfma_f32_16x16x128_f8f6f4 v[108:111], v[16:23], v[198:205], v[108:111]
	v_mfma_f32_16x16x128_f8f6f4 v[104:107], v[24:31], v[198:205], v[104:107]
	v_mfma_f32_16x16x128_f8f6f4 v[92:95], v[16:23], v[206:213], v[92:95]
	v_mfma_f32_16x16x128_f8f6f4 v[88:91], v[24:31], v[206:213], v[88:91]
	v_mfma_f32_16x16x128_f8f6f4 v[76:79], v[16:23], v[214:221], v[76:79]
	v_mfma_f32_16x16x128_f8f6f4 v[72:75], v[24:31], v[214:221], v[72:75]
	v_mfma_f32_16x16x128_f8f6f4 v[60:63], v[16:23], v[222:229], v[60:63]
	v_mfma_f32_16x16x128_f8f6f4 v[56:59], v[24:31], v[222:229], v[56:59]
	s_setprio 0
	s_barrier
	s_mov_b32 m0, s42
	v_lshl_add_u64 v[172:173], v[172:173], 0, s[24:25]
	s_add_u32 s34, s34, 0x20080
	ds_read_b128 v[198:201], v196 offset:49152
	ds_read_b128 v[202:205], v196 offset:50176
	ds_read_b128 v[206:209], v196 offset:51200
	ds_read_b128 v[210:213], v196 offset:52224
	ds_read_b128 v[214:217], v196 offset:53248
	ds_read_b128 v[218:221], v196 offset:54272
	ds_read_b128 v[222:225], v196 offset:55296
	ds_read_b128 v[226:229], v196 offset:56320
	global_load_lds_dwordx4 v[172:173], off
	v_lshl_add_u64 v[172:173], v[174:175], 0, s[24:25]
	s_mov_b32 m0, s43
	s_addc_u32 s35, s35, 0
	global_load_lds_dwordx4 v[172:173], off
	v_lshl_add_u64 v[172:173], s[34:35], 0, v[122:123]
	s_mov_b32 m0, s46
	s_nop 0
	global_load_lds_dwordx4 v[172:173], off
	v_lshl_add_u64 v[172:173], s[34:35], 0, v[120:121]
	s_mov_b32 m0, s47
	s_nop 0
	global_load_lds_dwordx4 v[172:173], off
	s_waitcnt vmcnt(6)
	s_waitcnt lgkmcnt(0)
	s_barrier
	s_setprio 1
	s_waitcnt lgkmcnt(0)
	v_mfma_f32_16x16x128_f8f6f4 v[48:51], v[0:7], v[198:205], v[48:51]
	v_mfma_f32_16x16x128_f8f6f4 v[40:43], v[8:15], v[198:205], v[40:43]
	v_mfma_f32_16x16x128_f8f6f4 v[44:47], v[0:7], v[206:213], v[44:47]
	v_mfma_f32_16x16x128_f8f6f4 v[32:35], v[8:15], v[206:213], v[32:35]
	v_mfma_f32_16x16x128_f8f6f4 v[36:39], v[0:7], v[214:221], v[36:39]
	v_mfma_f32_16x16x128_f8f6f4 v[144:147], v[8:15], v[214:221], v[144:147]
	v_mfma_f32_16x16x128_f8f6f4 v[128:131], v[0:7], v[222:229], v[128:131]
	v_mfma_f32_16x16x128_f8f6f4 v[132:135], v[8:15], v[222:229], v[132:135]
	s_setprio 0
	v_lshl_add_u64 v[172:173], v[176:177], 0, s[24:25]
	s_mov_b32 m0, s44
	s_nop 0
	global_load_lds_dwordx4 v[172:173], off
	v_lshl_add_u64 v[172:173], v[178:179], 0, s[24:25]
	s_mov_b32 m0, s45
	s_nop 0
	global_load_lds_dwordx4 v[172:173], off
	s_setprio 1
	v_mfma_f32_16x16x128_f8f6f4 v[52:55], v[16:23], v[198:205], v[52:55]
	v_mfma_f32_16x16x128_f8f6f4 v[164:167], v[24:31], v[198:205], v[164:167]
	v_mfma_f32_16x16x128_f8f6f4 v[156:159], v[16:23], v[206:213], v[156:159]
	v_mfma_f32_16x16x128_f8f6f4 v[160:163], v[24:31], v[206:213], v[160:163]
	v_mfma_f32_16x16x128_f8f6f4 v[148:151], v[16:23], v[214:221], v[148:151]
	v_mfma_f32_16x16x128_f8f6f4 v[152:155], v[24:31], v[214:221], v[152:155]
	v_mfma_f32_16x16x128_f8f6f4 v[140:143], v[16:23], v[222:229], v[140:143]
	v_mfma_f32_16x16x128_f8f6f4 v[136:139], v[24:31], v[222:229], v[136:139]
	s_setprio 0
	s_barrier
	s_add_i32 s52, s52, 2
	s_add_u32 s48, s48, 0x100
	s_addc_u32 s49, s49, 0
	s_add_u32 s50, s50, 0x100
	s_addc_u32 s51, s51, 0
	v_lshl_add_u64 v[168:169], v[168:169], 0, s[26:27]
	s_cmp_gt_u32 s52, 5
	v_lshl_add_u64 v[170:171], v[170:171], 0, s[26:27]
	s_cbranch_scc0 .LBB0_577
	s_nop 15
	s_nop 7
	s_waitcnt vmcnt(0)
	s_cmpk_lt_u32 s21, 0x100
	s_cbranch_scc0 .LBB0_580
	s_barrier

.LBB0_626:
	ds_read_b128 v[20:23], v184
	ds_read_b128 v[24:27], v185
	ds_read_b128 v[16:19], v180
	ds_read_b128 v[0:3], v181
	ds_read_b128 v[28:31], v186
	ds_read_b128 v[4:7], v187
	ds_read_b128 v[8:11], v188
	ds_read_b128 v[12:15], v189
	s_add_u32 s34, s90, s44
	s_addc_u32 s35, s91, s45
	s_add_u32 s51, s90, s46
	s_addc_u32 s52, s91, s47
	s_cmp_eq_u32 s48, 4
	s_cselect_b32 s37, s15, s35
	s_cselect_b32 s36, s14, s34
	s_cselect_b32 s35, s7, s52
	s_cselect_b32 s34, s6, s51
	s_mov_b32 m0, s49
	v_lshl_add_u64 v[222:223], s[90:91], 0, v[168:169]
	ds_read_b128 v[172:175], v196
	ds_read_b128 v[176:179], v196 offset:1024
	ds_read_b128 v[198:201], v196 offset:2048
	ds_read_b128 v[202:205], v196 offset:3072
	ds_read_b128 v[206:209], v196 offset:4096
	ds_read_b128 v[210:213], v196 offset:5120
	ds_read_b128 v[214:217], v196 offset:6144
	ds_read_b128 v[218:221], v196 offset:7168
	global_load_lds_dwordx4 v[222:223], off
	v_lshl_add_u64 v[222:223], s[90:91], 0, v[170:171]
	s_mov_b32 m0, s50
	s_nop 0
	global_load_lds_dwordx4 v[222:223], off
	s_waitcnt vmcnt(8)
	s_waitcnt lgkmcnt(0)
	s_barrier
	s_setprio 1
	s_waitcnt lgkmcnt(0)
	v_mfma_f32_16x16x128_f8f6f4 v[116:119], v[16:23], v[172:179], v[116:119]
	v_mfma_f32_16x16x128_f8f6f4 v[112:115], v[24:31], v[172:179], v[112:115]
	v_mfma_f32_16x16x128_f8f6f4 v[100:103], v[16:23], v[198:205], v[100:103]
	v_mfma_f32_16x16x128_f8f6f4 v[96:99], v[24:31], v[198:205], v[96:99]
	v_mfma_f32_16x16x128_f8f6f4 v[84:87], v[16:23], v[206:213], v[84:87]
	v_mfma_f32_16x16x128_f8f6f4 v[80:83], v[24:31], v[206:213], v[80:83]
	v_mfma_f32_16x16x128_f8f6f4 v[68:71], v[16:23], v[214:221], v[68:71]
	v_mfma_f32_16x16x128_f8f6f4 v[64:67], v[24:31], v[214:221], v[64:67]
	s_setprio 0
	s_setprio 1
	v_mfma_f32_16x16x128_f8f6f4 v[108:111], v[0:7], v[172:179], v[108:111]
	v_mfma_f32_16x16x128_f8f6f4 v[104:107], v[8:15], v[172:179], v[104:107]
	v_mfma_f32_16x16x128_f8f6f4 v[92:95], v[0:7], v[198:205], v[92:95]
	v_mfma_f32_16x16x128_f8f6f4 v[88:91], v[8:15], v[198:205], v[88:91]
	v_mfma_f32_16x16x128_f8f6f4 v[76:79], v[0:7], v[206:213], v[76:79]
	v_mfma_f32_16x16x128_f8f6f4 v[72:75], v[8:15], v[206:213], v[72:75]
	v_mfma_f32_16x16x128_f8f6f4 v[60:63], v[0:7], v[214:221], v[60:63]
	v_mfma_f32_16x16x128_f8f6f4 v[56:59], v[8:15], v[214:221], v[56:59]
	s_setprio 0
	s_barrier
	s_mov_b32 m0, s16
	v_lshl_add_u64 v[172:173], s[34:35], 0, v[122:123]
	s_add_u32 s52, s34, 0x20000
	ds_read_b128 v[198:201], v196 offset:16384
	ds_read_b128 v[202:205], v196 offset:17408
	ds_read_b128 v[206:209], v196 offset:18432
	ds_read_b128 v[210:213], v196 offset:19456
	ds_read_b128 v[214:217], v196 offset:20480
	ds_read_b128 v[218:221], v196 offset:21504
	ds_read_b128 v[222:225], v196 offset:22528
	ds_read_b128 v[226:229], v196 offset:23552
	global_load_lds_dwordx4 v[172:173], off
	v_lshl_add_u64 v[174:175], s[34:35], 0, v[120:121]
	s_mov_b32 m0, s17
	s_addc_u32 s53, s35, 0
	global_load_lds_dwordx4 v[174:175], off
	v_lshl_add_u64 v[176:177], s[52:53], 0, v[122:123]
	s_mov_b32 m0, s22
	v_lshl_add_u64 v[178:179], s[36:37], 0, v[126:127]
	global_load_lds_dwordx4 v[176:177], off
	v_lshl_add_u64 v[176:177], s[52:53], 0, v[120:121]
	s_mov_b32 m0, s23
	s_nop 0
	global_load_lds_dwordx4 v[176:177], off
	s_waitcnt vmcnt(6)
	s_waitcnt lgkmcnt(0)
	s_barrier
	s_setprio 1
	s_waitcnt lgkmcnt(0)
	v_mfma_f32_16x16x128_f8f6f4 v[48:51], v[16:23], v[198:205], v[48:51]
	v_mfma_f32_16x16x128_f8f6f4 v[40:43], v[24:31], v[198:205], v[40:43]
	v_mfma_f32_16x16x128_f8f6f4 v[44:47], v[16:23], v[206:213], v[44:47]
	v_mfma_f32_16x16x128_f8f6f4 v[32:35], v[24:31], v[206:213], v[32:35]
	v_mfma_f32_16x16x128_f8f6f4 v[36:39], v[16:23], v[214:221], v[36:39]
	v_mfma_f32_16x16x128_f8f6f4 v[144:147], v[24:31], v[214:221], v[144:147]
	v_mfma_f32_16x16x128_f8f6f4 v[128:131], v[16:23], v[222:229], v[128:131]
	v_mfma_f32_16x16x128_f8f6f4 v[132:135], v[24:31], v[222:229], v[132:135]
	s_setprio 0
	v_lshl_add_u64 v[176:177], s[36:37], 0, v[124:125]
	s_mov_b32 m0, s3
	s_nop 0
	global_load_lds_dwordx4 v[176:177], off
	s_mov_b32 m0, s28
	s_nop 0
	global_load_lds_dwordx4 v[178:179], off
	s_setprio 1
	v_mfma_f32_16x16x128_f8f6f4 v[52:55], v[0:7], v[198:205], v[52:55]
	v_mfma_f32_16x16x128_f8f6f4 v[164:167], v[8:15], v[198:205], v[164:167]
	v_mfma_f32_16x16x128_f8f6f4 v[156:159], v[0:7], v[206:213], v[156:159]
	v_mfma_f32_16x16x128_f8f6f4 v[160:163], v[8:15], v[206:213], v[160:163]
	v_mfma_f32_16x16x128_f8f6f4 v[148:151], v[0:7], v[214:221], v[148:151]
	v_mfma_f32_16x16x128_f8f6f4 v[152:155], v[8:15], v[214:221], v[152:155]
	v_mfma_f32_16x16x128_f8f6f4 v[140:143], v[0:7], v[222:229], v[140:143]
	v_mfma_f32_16x16x128_f8f6f4 v[136:139], v[8:15], v[222:229], v[136:139]
	s_setprio 0
	s_barrier
	ds_read_b128 v[4:7], v190
	ds_read_b128 v[8:11], v191
	ds_read_b128 v[0:3], v182
	ds_read_b128 v[16:19], v183
	ds_read_b128 v[12:15], v192
	ds_read_b128 v[20:23], v193
	ds_read_b128 v[24:27], v194
	ds_read_b128 v[28:31], v195
	s_add_u32 s36, s36, 0x20000
	s_addc_u32 s37, s37, 0
	s_mov_b32 m0, s29
	v_lshl_add_u64 v[230:231], s[36:37], 0, v[124:125]
	ds_read_b128 v[198:201], v196 offset:32768
	ds_read_b128 v[202:205], v196 offset:33792
	ds_read_b128 v[206:209], v196 offset:34816
	ds_read_b128 v[210:213], v196 offset:35840
	ds_read_b128 v[214:217], v196 offset:36864
	ds_read_b128 v[218:221], v196 offset:37888
	ds_read_b128 v[222:225], v196 offset:38912
	ds_read_b128 v[226:229], v196 offset:39936
	global_load_lds_dwordx4 v[230:231], off
	v_lshl_add_u64 v[230:231], s[36:37], 0, v[126:127]
	s_mov_b32 m0, s30
	s_nop 0
	global_load_lds_dwordx4 v[230:231], off
	s_waitcnt vmcnt(8)
	s_waitcnt lgkmcnt(0)
	s_barrier
	s_setprio 1
	s_waitcnt lgkmcnt(0)
	v_mfma_f32_16x16x128_f8f6f4 v[116:119], v[0:7], v[198:205], v[116:119]
	v_mfma_f32_16x16x128_f8f6f4 v[112:115], v[8:15], v[198:205], v[112:115]
	v_mfma_f32_16x16x128_f8f6f4 v[100:103], v[0:7], v[206:213], v[100:103]
	v_mfma_f32_16x16x128_f8f6f4 v[96:99], v[8:15], v[206:213], v[96:99]
	v_mfma_f32_16x16x128_f8f6f4 v[84:87], v[0:7], v[214:221], v[84:87]
	v_mfma_f32_16x16x128_f8f6f4 v[80:83], v[8:15], v[214:221], v[80:83]
	v_mfma_f32_16x16x128_f8f6f4 v[68:71], v[0:7], v[222:229], v[68:71]
	v_mfma_f32_16x16x128_f8f6f4 v[64:67], v[8:15], v[222:229], v[64:67]
	s_setprio 0
	s_setprio 1
	v_mfma_f32_16x16x128_f8f6f4 v[108:111], v[16:23], v[198:205], v[108:111]
	v_mfma_f32_16x16x128_f8f6f4 v[104:107], v[24:31], v[198:205], v[104:107]
	v_mfma_f32_16x16x128_f8f6f4 v[92:95], v[16:23], v[206:213], v[92:95]
	v_mfma_f32_16x16x128_f8f6f4 v[88:91], v[24:31], v[206:213], v[88:91]
	v_mfma_f32_16x16x128_f8f6f4 v[76:79], v[16:23], v[214:221], v[76:79]
	v_mfma_f32_16x16x128_f8f6f4 v[72:75], v[24:31], v[214:221], v[72:75]
	v_mfma_f32_16x16x128_f8f6f4 v[60:63], v[16:23], v[222:229], v[60:63]
	v_mfma_f32_16x16x128_f8f6f4 v[56:59], v[24:31], v[222:229], v[56:59]
	s_setprio 0
	s_barrier
	s_mov_b32 m0, s31
	v_lshl_add_u64 v[172:173], v[172:173], 0, s[24:25]
	s_add_u32 s34, s34, 0x20080
	ds_read_b128 v[198:201], v196 offset:49152
	ds_read_b128 v[202:205], v196 offset:50176
	ds_read_b128 v[206:209], v196 offset:51200
	ds_read_b128 v[210:213], v196 offset:52224
	ds_read_b128 v[214:217], v196 offset:53248
	ds_read_b128 v[218:221], v196 offset:54272
	ds_read_b128 v[222:225], v196 offset:55296
	ds_read_b128 v[226:229], v196 offset:56320
	global_load_lds_dwordx4 v[172:173], off
	v_lshl_add_u64 v[172:173], v[174:175], 0, s[24:25]
	s_mov_b32 m0, s33
	s_addc_u32 s35, s35, 0
	global_load_lds_dwordx4 v[172:173], off
	v_lshl_add_u64 v[172:173], s[34:35], 0, v[122:123]
	s_mov_b32 m0, s42
	s_nop 0
	global_load_lds_dwordx4 v[172:173], off
	v_lshl_add_u64 v[172:173], s[34:35], 0, v[120:121]
	s_mov_b32 m0, s43
	s_nop 0
	global_load_lds_dwordx4 v[172:173], off
	s_waitcnt vmcnt(6)
	s_waitcnt lgkmcnt(0)
	s_barrier
	s_setprio 1
	s_waitcnt lgkmcnt(0)
	v_mfma_f32_16x16x128_f8f6f4 v[48:51], v[0:7], v[198:205], v[48:51]
	v_mfma_f32_16x16x128_f8f6f4 v[40:43], v[8:15], v[198:205], v[40:43]
	v_mfma_f32_16x16x128_f8f6f4 v[44:47], v[0:7], v[206:213], v[44:47]
	v_mfma_f32_16x16x128_f8f6f4 v[32:35], v[8:15], v[206:213], v[32:35]
	v_mfma_f32_16x16x128_f8f6f4 v[36:39], v[0:7], v[214:221], v[36:39]
	v_mfma_f32_16x16x128_f8f6f4 v[144:147], v[8:15], v[214:221], v[144:147]
	v_mfma_f32_16x16x128_f8f6f4 v[128:131], v[0:7], v[222:229], v[128:131]
	v_mfma_f32_16x16x128_f8f6f4 v[132:135], v[8:15], v[222:229], v[132:135]
	s_setprio 0
	v_lshl_add_u64 v[172:173], v[176:177], 0, s[24:25]
	s_mov_b32 m0, s40
	s_nop 0
	global_load_lds_dwordx4 v[172:173], off
	v_lshl_add_u64 v[172:173], v[178:179], 0, s[24:25]
	s_mov_b32 m0, s41
	s_nop 0
	global_load_lds_dwordx4 v[172:173], off
	s_setprio 1
	v_mfma_f32_16x16x128_f8f6f4 v[52:55], v[16:23], v[198:205], v[52:55]
	v_mfma_f32_16x16x128_f8f6f4 v[164:167], v[24:31], v[198:205], v[164:167]
	v_mfma_f32_16x16x128_f8f6f4 v[156:159], v[16:23], v[206:213], v[156:159]
	v_mfma_f32_16x16x128_f8f6f4 v[160:163], v[24:31], v[206:213], v[160:163]
	v_mfma_f32_16x16x128_f8f6f4 v[148:151], v[16:23], v[214:221], v[148:151]
	v_mfma_f32_16x16x128_f8f6f4 v[152:155], v[24:31], v[214:221], v[152:155]
	v_mfma_f32_16x16x128_f8f6f4 v[140:143], v[16:23], v[222:229], v[140:143]
	v_mfma_f32_16x16x128_f8f6f4 v[136:139], v[24:31], v[222:229], v[136:139]
	s_setprio 0
	s_barrier
	s_add_i32 s48, s48, 2
	s_add_u32 s44, s44, 0x100
	s_addc_u32 s45, s45, 0
	s_add_u32 s46, s46, 0x100
	s_addc_u32 s47, s47, 0
	v_lshl_add_u64 v[168:169], v[168:169], 0, s[26:27]
	s_cmp_gt_u32 s48, 5
	v_lshl_add_u64 v[170:171], v[170:171], 0, s[26:27]
	s_cbranch_scc0 .LBB0_626
	s_nop 15
	s_nop 7
	s_waitcnt vmcnt(0)
	s_cmpk_lt_u32 s19, 0x100
	s_cbranch_scc0 .LBB0_629
	s_barrier

.LBB0_815:
	s_add_u32 s44, s90, s4
	s_addc_u32 s45, s91, s5
	s_add_u32 s71, s44, 0x21c00100
	s_addc_u32 s72, s45, 0
	s_cmpk_eq_i32 s4, 0x300
	v_lshl_add_u64 v[0:1], v[180:181], 0, s[4:5]
	s_cselect_b64 vcc, -1, 0
	v_cndmask_b32_e32 v183, v1, v167, vcc
	v_cndmask_b32_e32 v182, v0, v220, vcc
	ds_read_b128 v[8:11], v194
	ds_read_b128 v[12:15], v198
	ds_read_b128 v[24:27], v199
	ds_read_b128 v[28:31], v200
	ds_read_b128 v[0:3], v195
	ds_read_b128 v[4:7], v201
	ds_read_b128 v[16:19], v202
	ds_read_b128 v[20:23], v203
	s_and_b64 s[44:45], vcc, exec
	s_cselect_b32 s45, s13, s72
	s_cselect_b32 s44, s12, s71
	v_cndmask_b32_e32 v160, v219, v215, vcc
	v_cndmask_b32_e32 v184, v170, v216, vcc
	v_cndmask_b32_e32 v175, v172, v217, vcc
	v_cndmask_b32_e32 v173, v174, v218, vcc
	v_lshl_add_u64 v[186:187], v[178:179], 0, s[4:5]
	s_add_i32 m0, s0, 0xc000
	ds_read_b128 v[222:225], v212
	ds_read_b128 v[226:229], v212 offset:1024
	ds_read_b128 v[230:233], v212 offset:2048
	ds_read_b128 v[234:237], v212 offset:3072
	ds_read_b128 v[238:241], v212 offset:4096
	ds_read_b128 v[242:245], v212 offset:5120
	ds_read_b128 v[246:249], v212 offset:6144
	ds_read_b128 v[250:253], v212 offset:7168
	global_load_lds_dwordx4 v[186:187], off
	v_lshl_add_u64 v[186:187], v[176:177], 0, s[4:5]
	s_add_i32 m0, s0, 0xe000
	s_nop 0
	global_load_lds_dwordx4 v[186:187], off
	s_waitcnt vmcnt(8)
	s_waitcnt lgkmcnt(0)
	s_barrier
	s_setprio 1
	s_waitcnt lgkmcnt(0)
	v_mfma_f32_16x16x128_f8f6f4 v[156:159], v[8:15], v[222:229], v[156:159]
	v_mfma_f32_16x16x128_f8f6f4 v[152:155], v[24:31], v[222:229], v[152:155]
	v_mfma_f32_16x16x128_f8f6f4 v[140:143], v[8:15], v[230:237], v[140:143]
	v_mfma_f32_16x16x128_f8f6f4 v[136:139], v[24:31], v[230:237], v[136:139]
	v_mfma_f32_16x16x128_f8f6f4 v[124:127], v[8:15], v[238:245], v[124:127]
	v_mfma_f32_16x16x128_f8f6f4 v[120:123], v[24:31], v[238:245], v[120:123]
	v_mfma_f32_16x16x128_f8f6f4 v[108:111], v[8:15], v[246:253], v[108:111]
	v_mfma_f32_16x16x128_f8f6f4 v[104:107], v[24:31], v[246:253], v[104:107]
	s_setprio 0
	s_setprio 1
	v_mfma_f32_16x16x128_f8f6f4 v[148:151], v[0:7], v[222:229], v[148:151]
	v_mfma_f32_16x16x128_f8f6f4 v[144:147], v[16:23], v[222:229], v[144:147]
	v_mfma_f32_16x16x128_f8f6f4 v[132:135], v[0:7], v[230:237], v[132:135]
	v_mfma_f32_16x16x128_f8f6f4 v[128:131], v[16:23], v[230:237], v[128:131]
	v_mfma_f32_16x16x128_f8f6f4 v[116:119], v[0:7], v[238:245], v[116:119]
	v_mfma_f32_16x16x128_f8f6f4 v[112:115], v[16:23], v[238:245], v[112:115]
	v_mfma_f32_16x16x128_f8f6f4 v[100:103], v[0:7], v[246:253], v[100:103]
	v_mfma_f32_16x16x128_f8f6f4 v[96:99], v[16:23], v[246:253], v[96:99]
	s_setprio 0
	s_barrier
	s_mov_b32 m0, s21
	v_lshl_add_u64 v[186:187], v[182:183], 0, v[164:165]
	ds_read_b128 v[222:225], v212 offset:16384
	ds_read_b128 v[226:229], v212 offset:17408
	ds_read_b128 v[230:233], v212 offset:18432
	ds_read_b128 v[234:237], v212 offset:19456
	ds_read_b128 v[238:241], v212 offset:20480
	ds_read_b128 v[242:245], v212 offset:21504
	ds_read_b128 v[246:249], v212 offset:22528
	ds_read_b128 v[250:253], v212 offset:23552
	global_load_lds_dwordx4 v[186:187], off
	v_lshl_add_u64 v[188:189], v[182:183], 0, v[162:163]
	s_mov_b32 m0, s22
	v_lshl_add_u64 v[190:191], v[182:183], 0, s[16:17]
	global_load_lds_dwordx4 v[188:189], off
	v_lshl_add_u64 v[192:193], v[190:191], 0, v[164:165]
	s_mov_b32 m0, s23
	v_lshl_add_u64 v[190:191], v[190:191], 0, v[162:163]
	global_load_lds_dwordx4 v[192:193], off
	s_mov_b32 m0, s28
	v_mov_b32_e32 v185, v161
	global_load_lds_dwordx4 v[190:191], off
	s_mov_b32 m0, s0
	v_lshl_add_u64 v[190:191], s[44:45], 0, v[160:161]
	global_load_lds_dwordx4 v160, s[44:45]
	s_mov_b32 m0, s29
	s_nop 0
	global_load_lds_dwordx4 v184, s[44:45]
	s_waitcnt vmcnt(8)
	s_waitcnt lgkmcnt(0)
	v_lshl_add_u64 v[184:185], s[44:45], 0, v[184:185]
	s_barrier
	s_setprio 1
	s_waitcnt lgkmcnt(0)
	v_mfma_f32_16x16x128_f8f6f4 v[84:87], v[8:15], v[222:229], v[84:87]
	v_mfma_f32_16x16x128_f8f6f4 v[80:83], v[24:31], v[222:229], v[80:83]
	v_mfma_f32_16x16x128_f8f6f4 v[68:71], v[8:15], v[230:237], v[68:71]
	v_mfma_f32_16x16x128_f8f6f4 v[64:67], v[24:31], v[230:237], v[64:67]
	v_mfma_f32_16x16x128_f8f6f4 v[52:55], v[8:15], v[238:245], v[52:55]
	v_mfma_f32_16x16x128_f8f6f4 v[48:51], v[24:31], v[238:245], v[48:51]
	v_mfma_f32_16x16x128_f8f6f4 v[36:39], v[8:15], v[246:253], v[36:39]
	v_mfma_f32_16x16x128_f8f6f4 v[32:35], v[24:31], v[246:253], v[32:35]
	s_setprio 0
	s_setprio 1
	v_mfma_f32_16x16x128_f8f6f4 v[92:95], v[0:7], v[222:229], v[92:95]
	v_mfma_f32_16x16x128_f8f6f4 v[88:91], v[16:23], v[222:229], v[88:91]
	v_mfma_f32_16x16x128_f8f6f4 v[76:79], v[0:7], v[230:237], v[76:79]
	v_mfma_f32_16x16x128_f8f6f4 v[72:75], v[16:23], v[230:237], v[72:75]
	v_mfma_f32_16x16x128_f8f6f4 v[60:63], v[0:7], v[238:245], v[60:63]
	v_mfma_f32_16x16x128_f8f6f4 v[56:59], v[16:23], v[238:245], v[56:59]
	v_mfma_f32_16x16x128_f8f6f4 v[44:47], v[0:7], v[246:253], v[44:47]
	v_mfma_f32_16x16x128_f8f6f4 v[40:43], v[16:23], v[246:253], v[40:43]
	s_setprio 0
	s_barrier
	ds_read_b128 v[4:7], v204
	ds_read_b128 v[8:11], v205
	ds_read_b128 v[0:3], v196
	ds_read_b128 v[16:19], v197
	ds_read_b128 v[12:15], v206
	ds_read_b128 v[20:23], v207
	ds_read_b128 v[24:27], v208
	ds_read_b128 v[28:31], v209
	s_mov_b32 m0, s30
	ds_read_b128 v[222:225], v212 offset:32768
	ds_read_b128 v[226:229], v212 offset:33792
	ds_read_b128 v[230:233], v212 offset:34816
	ds_read_b128 v[234:237], v212 offset:35840
	ds_read_b128 v[238:241], v212 offset:36864
	ds_read_b128 v[242:245], v212 offset:37888
	ds_read_b128 v[246:249], v212 offset:38912
	ds_read_b128 v[250:253], v212 offset:39936
	global_load_lds_dwordx4 v175, s[44:45]
	s_mov_b32 m0, s31
	s_nop 0
	global_load_lds_dwordx4 v173, s[44:45]
	s_waitcnt vmcnt(8)
	s_waitcnt lgkmcnt(0)
	s_barrier
	s_setprio 1
	s_waitcnt lgkmcnt(0)
	v_mfma_f32_16x16x128_f8f6f4 v[156:159], v[0:7], v[222:229], v[156:159]
	v_mfma_f32_16x16x128_f8f6f4 v[152:155], v[8:15], v[222:229], v[152:155]
	v_mfma_f32_16x16x128_f8f6f4 v[140:143], v[0:7], v[230:237], v[140:143]
	v_mfma_f32_16x16x128_f8f6f4 v[136:139], v[8:15], v[230:237], v[136:139]
	v_mfma_f32_16x16x128_f8f6f4 v[124:127], v[0:7], v[238:245], v[124:127]
	v_mfma_f32_16x16x128_f8f6f4 v[120:123], v[8:15], v[238:245], v[120:123]
	v_mfma_f32_16x16x128_f8f6f4 v[108:111], v[0:7], v[246:253], v[108:111]
	v_mfma_f32_16x16x128_f8f6f4 v[104:107], v[8:15], v[246:253], v[104:107]
	s_setprio 0
	s_setprio 1
	v_mfma_f32_16x16x128_f8f6f4 v[148:151], v[16:23], v[222:229], v[148:151]
	v_mfma_f32_16x16x128_f8f6f4 v[144:147], v[24:31], v[222:229], v[144:147]
	v_mfma_f32_16x16x128_f8f6f4 v[132:135], v[16:23], v[230:237], v[132:135]
	v_mfma_f32_16x16x128_f8f6f4 v[128:131], v[24:31], v[230:237], v[128:131]
	v_mfma_f32_16x16x128_f8f6f4 v[116:119], v[16:23], v[238:245], v[116:119]
	v_mfma_f32_16x16x128_f8f6f4 v[112:115], v[24:31], v[238:245], v[112:115]
	v_mfma_f32_16x16x128_f8f6f4 v[100:103], v[16:23], v[246:253], v[100:103]
	v_mfma_f32_16x16x128_f8f6f4 v[96:99], v[24:31], v[246:253], v[96:99]
	s_setprio 0
	s_barrier
	s_mov_b32 m0, s33
	v_lshl_add_u64 v[186:187], v[186:187], 0, s[26:27]
	ds_read_b128 v[222:225], v212 offset:49152
	ds_read_b128 v[226:229], v212 offset:50176
	ds_read_b128 v[230:233], v212 offset:51200
	ds_read_b128 v[234:237], v212 offset:52224
	ds_read_b128 v[238:241], v212 offset:53248
	ds_read_b128 v[242:245], v212 offset:54272
	ds_read_b128 v[246:249], v212 offset:55296
	ds_read_b128 v[250:253], v212 offset:56320
	global_load_lds_dwordx4 v[186:187], off
	v_lshl_add_u64 v[186:187], v[188:189], 0, s[26:27]
	s_mov_b32 m0, s46
	v_lshl_add_u64 v[182:183], v[182:183], 0, s[36:37]
	global_load_lds_dwordx4 v[186:187], off
	v_lshl_add_u64 v[186:187], v[182:183], 0, v[164:165]
	s_mov_b32 m0, s49
	v_lshl_add_u64 v[182:183], v[182:183], 0, v[162:163]
	global_load_lds_dwordx4 v[186:187], off
	s_mov_b32 m0, s50
	s_nop 0
	global_load_lds_dwordx4 v[182:183], off
	s_waitcnt vmcnt(6)
	s_waitcnt lgkmcnt(0)
	s_barrier
	s_setprio 1
	s_waitcnt lgkmcnt(0)
	v_mfma_f32_16x16x128_f8f6f4 v[84:87], v[0:7], v[222:229], v[84:87]
	v_mfma_f32_16x16x128_f8f6f4 v[80:83], v[8:15], v[222:229], v[80:83]
	v_mfma_f32_16x16x128_f8f6f4 v[68:71], v[0:7], v[230:237], v[68:71]
	v_mfma_f32_16x16x128_f8f6f4 v[64:67], v[8:15], v[230:237], v[64:67]
	v_mfma_f32_16x16x128_f8f6f4 v[52:55], v[0:7], v[238:245], v[52:55]
	v_mfma_f32_16x16x128_f8f6f4 v[48:51], v[8:15], v[238:245], v[48:51]
	v_mfma_f32_16x16x128_f8f6f4 v[36:39], v[0:7], v[246:253], v[36:39]
	v_mfma_f32_16x16x128_f8f6f4 v[32:35], v[8:15], v[246:253], v[32:35]
	s_setprio 0
	v_lshl_add_u64 v[182:183], v[190:191], 0, s[26:27]
	s_mov_b32 m0, s47
	s_nop 0
	global_load_lds_dwordx4 v[182:183], off
	v_lshl_add_u64 v[182:183], v[184:185], 0, s[26:27]
	s_mov_b32 m0, s48
	s_nop 0
	global_load_lds_dwordx4 v[182:183], off
	s_setprio 1
	v_mfma_f32_16x16x128_f8f6f4 v[92:95], v[16:23], v[222:229], v[92:95]
	v_mfma_f32_16x16x128_f8f6f4 v[88:91], v[24:31], v[222:229], v[88:91]
	v_mfma_f32_16x16x128_f8f6f4 v[76:79], v[16:23], v[230:237], v[76:79]
	v_mfma_f32_16x16x128_f8f6f4 v[72:75], v[24:31], v[230:237], v[72:75]
	v_mfma_f32_16x16x128_f8f6f4 v[60:63], v[16:23], v[238:245], v[60:63]
	v_mfma_f32_16x16x128_f8f6f4 v[56:59], v[24:31], v[238:245], v[56:59]
	v_mfma_f32_16x16x128_f8f6f4 v[44:47], v[16:23], v[246:253], v[44:47]
	v_mfma_f32_16x16x128_f8f6f4 v[40:43], v[24:31], v[246:253], v[40:43]
	s_setprio 0
	s_barrier
	s_add_i32 s43, s43, 2
	s_add_u32 s4, s4, 0x100
	s_addc_u32 s5, s5, 0
	s_cmp_gt_u32 s43, 5
	s_cbranch_scc0 .LBB0_815
	s_nop 15
	s_nop 7
	s_and_b64 vcc, exec, s[38:39]
	s_cbranch_vccz .LBB0_818
	s_barrier

.LBB0_913:
	v_lshl_add_u64 v[0:1], v[168:169], 0, s[44:45]
	v_lshl_add_u64 v[0:1], v[0:1], 0, s[92:93]
	v_cndmask_b32_e64 v179, v1, v171, s[42:43]
	v_cndmask_b32_e64 v178, v0, v205, s[42:43]
	ds_read_b128 v[8:11], v185
	ds_read_b128 v[12:15], v189
	ds_read_b128 v[24:27], v190
	ds_read_b128 v[28:31], v191
	ds_read_b128 v[0:3], v186
	ds_read_b128 v[4:7], v192
	ds_read_b128 v[16:19], v193
	ds_read_b128 v[20:23], v194
	s_add_u32 s25, s34, s44
	s_addc_u32 s75, s35, s45
	s_add_u32 s94, s25, 0x100
	s_addc_u32 s95, s75, 0
	s_and_b64 s[46:47], s[42:43], exec
	s_cselect_b32 s47, s37, s95
	s_cselect_b32 s46, s74, s94
	s_add_u32 s44, s25, 0x10080
	s_addc_u32 s45, s75, 0
	s_add_i32 m0, s23, 0xc000
	s_add_i32 s25, s23, 0xe000
	s_add_u32 s42, s46, 0x10000
	s_addc_u32 s43, s47, 0
	v_lshl_add_u64 v[180:181], v[178:179], 0, s[0:1]
	v_lshl_add_u64 v[174:175], v[178:179], 0, s[14:15]
	v_lshl_add_u64 v[176:177], s[44:45], 0, v[164:165]
	ds_read_b128 v[206:209], v203
	ds_read_b128 v[210:213], v203 offset:1024
	ds_read_b128 v[214:217], v203 offset:2048
	ds_read_b128 v[218:221], v203 offset:3072
	ds_read_b128 v[222:225], v203 offset:4096
	ds_read_b128 v[226:229], v203 offset:5120
	ds_read_b128 v[230:233], v203 offset:6144
	ds_read_b128 v[234:237], v203 offset:7168
	global_load_lds_dwordx4 v[176:177], off
	v_lshl_add_u64 v[176:177], s[44:45], 0, v[166:167]
	s_mov_b32 m0, s25
	s_nop 0
	global_load_lds_dwordx4 v[176:177], off
	s_waitcnt vmcnt(8)
	s_waitcnt lgkmcnt(0)
	s_barrier
	s_setprio 1
	s_waitcnt lgkmcnt(0)
	v_mfma_f32_16x16x128_f8f6f4 v[156:159], v[8:15], v[206:213], v[156:159]
	v_mfma_f32_16x16x128_f8f6f4 v[152:155], v[24:31], v[206:213], v[152:155]
	v_mfma_f32_16x16x128_f8f6f4 v[140:143], v[8:15], v[214:221], v[140:143]
	v_mfma_f32_16x16x128_f8f6f4 v[136:139], v[24:31], v[214:221], v[136:139]
	v_mfma_f32_16x16x128_f8f6f4 v[124:127], v[8:15], v[222:229], v[124:127]
	v_mfma_f32_16x16x128_f8f6f4 v[120:123], v[24:31], v[222:229], v[120:123]
	v_mfma_f32_16x16x128_f8f6f4 v[108:111], v[8:15], v[230:237], v[108:111]
	v_mfma_f32_16x16x128_f8f6f4 v[104:107], v[24:31], v[230:237], v[104:107]
	s_setprio 0
	s_setprio 1
	v_mfma_f32_16x16x128_f8f6f4 v[148:151], v[0:7], v[206:213], v[148:151]
	v_mfma_f32_16x16x128_f8f6f4 v[144:147], v[16:23], v[206:213], v[144:147]
	v_mfma_f32_16x16x128_f8f6f4 v[132:135], v[0:7], v[214:221], v[132:135]
	v_mfma_f32_16x16x128_f8f6f4 v[128:131], v[16:23], v[214:221], v[128:131]
	v_mfma_f32_16x16x128_f8f6f4 v[116:119], v[0:7], v[222:229], v[116:119]
	v_mfma_f32_16x16x128_f8f6f4 v[112:115], v[16:23], v[222:229], v[112:115]
	v_mfma_f32_16x16x128_f8f6f4 v[96:99], v[0:7], v[230:237], v[96:99]
	v_mfma_f32_16x16x128_f8f6f4 v[88:91], v[16:23], v[230:237], v[88:91]
	s_setprio 0
	s_barrier
	s_mov_b32 m0, s27
	v_lshl_add_u64 v[176:177], v[178:179], 0, v[162:163]
	ds_read_b128 v[206:209], v203 offset:16384
	ds_read_b128 v[210:213], v203 offset:17408
	ds_read_b128 v[214:217], v203 offset:18432
	ds_read_b128 v[218:221], v203 offset:19456
	ds_read_b128 v[222:225], v203 offset:20480
	ds_read_b128 v[226:229], v203 offset:21504
	ds_read_b128 v[230:233], v203 offset:22528
	ds_read_b128 v[234:237], v203 offset:23552
	global_load_lds_dwordx4 v[176:177], off
	v_lshl_add_u64 v[178:179], v[178:179], 0, v[160:161]
	s_mov_b32 m0, s28
	v_lshl_add_u64 v[182:183], v[180:181], 0, v[162:163]
	global_load_lds_dwordx4 v[178:179], off
	s_mov_b32 m0, s29
	v_lshl_add_u64 v[180:181], v[180:181], 0, v[160:161]
	global_load_lds_dwordx4 v[182:183], off
	s_mov_b32 m0, s30
	v_lshl_add_u64 v[182:183], s[46:47], 0, v[166:167]
	global_load_lds_dwordx4 v[180:181], off
	s_waitcnt vmcnt(6)
	s_waitcnt lgkmcnt(0)
	s_barrier
	s_setprio 1
	s_waitcnt lgkmcnt(0)
	v_mfma_f32_16x16x128_f8f6f4 v[84:87], v[8:15], v[206:213], v[84:87]
	v_mfma_f32_16x16x128_f8f6f4 v[76:79], v[24:31], v[206:213], v[76:79]
	v_mfma_f32_16x16x128_f8f6f4 v[60:63], v[8:15], v[214:221], v[60:63]
	v_mfma_f32_16x16x128_f8f6f4 v[48:51], v[24:31], v[214:221], v[48:51]
	v_mfma_f32_16x16x128_f8f6f4 v[68:71], v[8:15], v[222:229], v[68:71]
	v_mfma_f32_16x16x128_f8f6f4 v[56:59], v[24:31], v[222:229], v[56:59]
	v_mfma_f32_16x16x128_f8f6f4 v[44:47], v[8:15], v[230:237], v[44:47]
	v_mfma_f32_16x16x128_f8f6f4 v[36:39], v[24:31], v[230:237], v[36:39]
	s_setprio 0
	v_lshl_add_u64 v[180:181], s[46:47], 0, v[164:165]
	s_mov_b32 m0, s23
	s_nop 0
	global_load_lds_dwordx4 v[180:181], off
	s_mov_b32 m0, s31
	s_nop 0
	global_load_lds_dwordx4 v[182:183], off
	s_setprio 1
	v_mfma_f32_16x16x128_f8f6f4 v[100:103], v[0:7], v[206:213], v[100:103]
	v_mfma_f32_16x16x128_f8f6f4 v[92:95], v[16:23], v[206:213], v[92:95]
	v_mfma_f32_16x16x128_f8f6f4 v[80:83], v[0:7], v[214:221], v[80:83]
	v_mfma_f32_16x16x128_f8f6f4 v[72:75], v[16:23], v[214:221], v[72:75]
	v_mfma_f32_16x16x128_f8f6f4 v[64:67], v[0:7], v[222:229], v[64:67]
	v_mfma_f32_16x16x128_f8f6f4 v[52:55], v[16:23], v[222:229], v[52:55]
	v_mfma_f32_16x16x128_f8f6f4 v[40:43], v[0:7], v[230:237], v[40:43]
	v_mfma_f32_16x16x128_f8f6f4 v[32:35], v[16:23], v[230:237], v[32:35]
	s_setprio 0
	s_barrier
	ds_read_b128 v[4:7], v195
	ds_read_b128 v[8:11], v196
	ds_read_b128 v[0:3], v187
	ds_read_b128 v[16:19], v188
	ds_read_b128 v[12:15], v197
	ds_read_b128 v[20:23], v198
	ds_read_b128 v[24:27], v199
	ds_read_b128 v[28:31], v200
	s_mov_b32 m0, s33
	v_lshl_add_u64 v[238:239], s[42:43], 0, v[164:165]
	ds_read_b128 v[206:209], v203 offset:32768
	ds_read_b128 v[210:213], v203 offset:33792
	ds_read_b128 v[214:217], v203 offset:34816
	ds_read_b128 v[218:221], v203 offset:35840
	ds_read_b128 v[222:225], v203 offset:36864
	ds_read_b128 v[226:229], v203 offset:37888
	ds_read_b128 v[230:233], v203 offset:38912
	ds_read_b128 v[234:237], v203 offset:39936
	global_load_lds_dwordx4 v[238:239], off
	v_lshl_add_u64 v[238:239], s[42:43], 0, v[166:167]
	s_mov_b32 m0, s48
	s_nop 0
	global_load_lds_dwordx4 v[238:239], off
	s_waitcnt vmcnt(8)
	s_waitcnt lgkmcnt(0)
	s_barrier
	s_setprio 1
	s_waitcnt lgkmcnt(0)
	v_mfma_f32_16x16x128_f8f6f4 v[156:159], v[0:7], v[206:213], v[156:159]
	v_mfma_f32_16x16x128_f8f6f4 v[152:155], v[8:15], v[206:213], v[152:155]
	v_mfma_f32_16x16x128_f8f6f4 v[140:143], v[0:7], v[214:221], v[140:143]
	v_mfma_f32_16x16x128_f8f6f4 v[136:139], v[8:15], v[214:221], v[136:139]
	v_mfma_f32_16x16x128_f8f6f4 v[124:127], v[0:7], v[222:229], v[124:127]
	v_mfma_f32_16x16x128_f8f6f4 v[120:123], v[8:15], v[222:229], v[120:123]
	v_mfma_f32_16x16x128_f8f6f4 v[108:111], v[0:7], v[230:237], v[108:111]
	v_mfma_f32_16x16x128_f8f6f4 v[104:107], v[8:15], v[230:237], v[104:107]
	s_setprio 0
	s_setprio 1
	v_mfma_f32_16x16x128_f8f6f4 v[148:151], v[16:23], v[206:213], v[148:151]
	v_mfma_f32_16x16x128_f8f6f4 v[144:147], v[24:31], v[206:213], v[144:147]
	v_mfma_f32_16x16x128_f8f6f4 v[132:135], v[16:23], v[214:221], v[132:135]
	v_mfma_f32_16x16x128_f8f6f4 v[128:131], v[24:31], v[214:221], v[128:131]
	v_mfma_f32_16x16x128_f8f6f4 v[116:119], v[16:23], v[222:229], v[116:119]
	v_mfma_f32_16x16x128_f8f6f4 v[112:115], v[24:31], v[222:229], v[112:115]
	v_mfma_f32_16x16x128_f8f6f4 v[96:99], v[16:23], v[230:237], v[96:99]
	v_mfma_f32_16x16x128_f8f6f4 v[88:91], v[24:31], v[230:237], v[88:91]
	s_setprio 0
	s_barrier
	s_mov_b32 m0, s50
	v_lshl_add_u64 v[176:177], v[176:177], 0, s[12:13]
	ds_read_b128 v[206:209], v203 offset:49152
	ds_read_b128 v[210:213], v203 offset:50176
	ds_read_b128 v[214:217], v203 offset:51200
	ds_read_b128 v[218:221], v203 offset:52224
	ds_read_b128 v[222:225], v203 offset:53248
	ds_read_b128 v[226:229], v203 offset:54272
	ds_read_b128 v[230:233], v203 offset:55296
	ds_read_b128 v[234:237], v203 offset:56320
	global_load_lds_dwordx4 v[176:177], off
	v_lshl_add_u64 v[176:177], v[178:179], 0, s[12:13]
	s_mov_b32 m0, s51
	s_nop 0
	global_load_lds_dwordx4 v[176:177], off
	v_lshl_add_u64 v[176:177], v[174:175], 0, v[162:163]
	s_mov_b32 m0, s54
	v_lshl_add_u64 v[174:175], v[174:175], 0, v[160:161]
	global_load_lds_dwordx4 v[176:177], off
	s_mov_b32 m0, s55
	s_nop 0
	global_load_lds_dwordx4 v[174:175], off
	s_waitcnt vmcnt(6)
	s_waitcnt lgkmcnt(0)
	s_barrier
	s_setprio 1
	s_waitcnt lgkmcnt(0)
	v_mfma_f32_16x16x128_f8f6f4 v[84:87], v[0:7], v[206:213], v[84:87]
	v_mfma_f32_16x16x128_f8f6f4 v[76:79], v[8:15], v[206:213], v[76:79]
	v_mfma_f32_16x16x128_f8f6f4 v[60:63], v[0:7], v[214:221], v[60:63]
	v_mfma_f32_16x16x128_f8f6f4 v[48:51], v[8:15], v[214:221], v[48:51]
	v_mfma_f32_16x16x128_f8f6f4 v[68:71], v[0:7], v[222:229], v[68:71]
	v_mfma_f32_16x16x128_f8f6f4 v[56:59], v[8:15], v[222:229], v[56:59]
	v_mfma_f32_16x16x128_f8f6f4 v[44:47], v[0:7], v[230:237], v[44:47]
	v_mfma_f32_16x16x128_f8f6f4 v[36:39], v[8:15], v[230:237], v[36:39]
	s_setprio 0
	v_lshl_add_u64 v[174:175], v[180:181], 0, s[12:13]
	s_mov_b32 m0, s52
	s_nop 0
	global_load_lds_dwordx4 v[174:175], off
	v_lshl_add_u64 v[174:175], v[182:183], 0, s[12:13]
	s_mov_b32 m0, s53
	s_nop 0
	global_load_lds_dwordx4 v[174:175], off
	s_setprio 1
	v_mfma_f32_16x16x128_f8f6f4 v[100:103], v[16:23], v[206:213], v[100:103]
	v_mfma_f32_16x16x128_f8f6f4 v[92:95], v[24:31], v[206:213], v[92:95]
	v_mfma_f32_16x16x128_f8f6f4 v[80:83], v[16:23], v[214:221], v[80:83]
	v_mfma_f32_16x16x128_f8f6f4 v[72:75], v[24:31], v[214:221], v[72:75]
	v_mfma_f32_16x16x128_f8f6f4 v[64:67], v[16:23], v[222:229], v[64:67]
	v_mfma_f32_16x16x128_f8f6f4 v[52:55], v[24:31], v[222:229], v[52:55]
	v_mfma_f32_16x16x128_f8f6f4 v[40:43], v[16:23], v[230:237], v[40:43]
	v_mfma_f32_16x16x128_f8f6f4 v[32:35], v[24:31], v[230:237], v[32:35]
	s_setprio 0
	s_barrier
	s_andn2_b64 vcc, exec, s[40:41]
	s_mov_b64 s[42:43], -1
	s_mov_b64 s[40:41], 0
	s_mov_b64 s[44:45], 0x100
	s_cbranch_vccz .LBB0_913
	s_nop 15
	s_nop 7
	s_and_b64 vcc, exec, s[16:17]
	s_cbranch_vccz .LBB0_916
	s_barrier

.LBB0_1175:
	ds_read_b128 v[20:23], v188
	ds_read_b128 v[24:27], v189
	ds_read_b128 v[16:19], v183
	ds_read_b128 v[0:3], v184
	ds_read_b128 v[28:31], v190
	ds_read_b128 v[4:7], v191
	ds_read_b128 v[8:11], v192
	ds_read_b128 v[12:15], v193
	s_add_u32 s26, s24, 0xfffe0080
	s_addc_u32 s27, s25, -1
	s_cmp_eq_u32 s50, 4
	s_cselect_b32 s35, s9, s27
	s_cselect_b32 s34, s46, s26
	s_cselect_b32 s27, s7, s49
	s_cselect_b32 s26, s47, s48
	v_lshl_add_u64 v[228:229], s[24:25], 0, v[168:169]
	s_add_i32 m0, s17, 0xc000
	ds_read_b128 v[174:177], v200
	ds_read_b128 v[178:181], v200 offset:1024
	ds_read_b128 v[204:207], v200 offset:2048
	ds_read_b128 v[208:211], v200 offset:3072
	ds_read_b128 v[212:215], v200 offset:4096
	ds_read_b128 v[216:219], v200 offset:5120
	ds_read_b128 v[220:223], v200 offset:6144
	ds_read_b128 v[224:227], v200 offset:7168
	global_load_lds_dwordx4 v[228:229], off
	v_lshl_add_u64 v[228:229], s[24:25], 0, v[170:171]
	s_add_i32 m0, s17, 0xe000
	s_nop 0
	global_load_lds_dwordx4 v[228:229], off
	s_waitcnt vmcnt(8)
	s_waitcnt lgkmcnt(0)
	s_barrier
	s_setprio 1
	s_waitcnt lgkmcnt(0)
	v_mfma_f32_16x16x128_f8f6f4 v[156:159], v[16:23], v[174:181], v[156:159]
	v_mfma_f32_16x16x128_f8f6f4 v[152:155], v[24:31], v[174:181], v[152:155]
	v_mfma_f32_16x16x128_f8f6f4 v[144:147], v[16:23], v[204:211], v[144:147]
	v_mfma_f32_16x16x128_f8f6f4 v[136:139], v[24:31], v[204:211], v[136:139]
	v_mfma_f32_16x16x128_f8f6f4 v[128:131], v[16:23], v[212:219], v[128:131]
	v_mfma_f32_16x16x128_f8f6f4 v[120:123], v[24:31], v[212:219], v[120:123]
	v_mfma_f32_16x16x128_f8f6f4 v[112:115], v[16:23], v[220:227], v[112:115]
	v_mfma_f32_16x16x128_f8f6f4 v[104:107], v[24:31], v[220:227], v[104:107]
	s_setprio 0
	s_setprio 1
	v_mfma_f32_16x16x128_f8f6f4 v[148:151], v[0:7], v[174:181], v[148:151]
	v_mfma_f32_16x16x128_f8f6f4 v[140:143], v[8:15], v[174:181], v[140:143]
	v_mfma_f32_16x16x128_f8f6f4 v[132:135], v[0:7], v[204:211], v[132:135]
	v_mfma_f32_16x16x128_f8f6f4 v[124:127], v[8:15], v[204:211], v[124:127]
	v_mfma_f32_16x16x128_f8f6f4 v[116:119], v[0:7], v[212:219], v[116:119]
	v_mfma_f32_16x16x128_f8f6f4 v[108:111], v[8:15], v[212:219], v[108:111]
	v_mfma_f32_16x16x128_f8f6f4 v[92:95], v[0:7], v[220:227], v[92:95]
	v_mfma_f32_16x16x128_f8f6f4 v[88:91], v[8:15], v[220:227], v[88:91]
	s_setprio 0
	s_barrier
	s_mov_b32 m0, s22
	v_lshl_add_u64 v[174:175], s[26:27], 0, v[162:163]
	s_add_u32 s52, s26, 0x20000
	ds_read_b128 v[204:207], v200 offset:16384
	ds_read_b128 v[208:211], v200 offset:17408
	ds_read_b128 v[212:215], v200 offset:18432
	ds_read_b128 v[216:219], v200 offset:19456
	ds_read_b128 v[220:223], v200 offset:20480
	ds_read_b128 v[224:227], v200 offset:21504
	ds_read_b128 v[228:231], v200 offset:22528
	ds_read_b128 v[232:235], v200 offset:23552
	global_load_lds_dwordx4 v[174:175], off
	v_lshl_add_u64 v[176:177], s[26:27], 0, v[160:161]
	s_mov_b32 m0, s23
	s_addc_u32 s53, s27, 0
	global_load_lds_dwordx4 v[176:177], off
	v_lshl_add_u64 v[178:179], s[52:53], 0, v[162:163]
	s_mov_b32 m0, s28
	v_lshl_add_u64 v[180:181], s[34:35], 0, v[166:167]
	global_load_lds_dwordx4 v[178:179], off
	v_lshl_add_u64 v[178:179], s[52:53], 0, v[160:161]
	s_mov_b32 m0, s29
	s_nop 0
	global_load_lds_dwordx4 v[178:179], off
	s_waitcnt vmcnt(6)
	s_waitcnt lgkmcnt(0)
	s_barrier
	s_setprio 1
	s_waitcnt lgkmcnt(0)
	v_mfma_f32_16x16x128_f8f6f4 v[76:79], v[16:23], v[204:211], v[76:79]
	v_mfma_f32_16x16x128_f8f6f4 v[72:75], v[24:31], v[204:211], v[72:75]
	v_mfma_f32_16x16x128_f8f6f4 v[52:55], v[16:23], v[212:219], v[52:55]
	v_mfma_f32_16x16x128_f8f6f4 v[48:51], v[24:31], v[212:219], v[48:51]
	v_mfma_f32_16x16x128_f8f6f4 v[60:63], v[16:23], v[220:227], v[60:63]
	v_mfma_f32_16x16x128_f8f6f4 v[56:59], v[24:31], v[220:227], v[56:59]
	v_mfma_f32_16x16x128_f8f6f4 v[36:39], v[16:23], v[228:235], v[36:39]
	v_mfma_f32_16x16x128_f8f6f4 v[32:35], v[24:31], v[228:235], v[32:35]
	s_setprio 0
	v_lshl_add_u64 v[178:179], s[34:35], 0, v[164:165]
	s_mov_b32 m0, s17
	s_nop 0
	global_load_lds_dwordx4 v[178:179], off
	s_mov_b32 m0, s30
	s_nop 0
	global_load_lds_dwordx4 v[180:181], off
	s_setprio 1
	v_mfma_f32_16x16x128_f8f6f4 v[100:103], v[0:7], v[204:211], v[100:103]
	v_mfma_f32_16x16x128_f8f6f4 v[96:99], v[8:15], v[204:211], v[96:99]
	v_mfma_f32_16x16x128_f8f6f4 v[84:87], v[0:7], v[212:219], v[84:87]
	v_mfma_f32_16x16x128_f8f6f4 v[80:83], v[8:15], v[212:219], v[80:83]
	v_mfma_f32_16x16x128_f8f6f4 v[68:71], v[0:7], v[220:227], v[68:71]
	v_mfma_f32_16x16x128_f8f6f4 v[64:67], v[8:15], v[220:227], v[64:67]
	v_mfma_f32_16x16x128_f8f6f4 v[44:47], v[0:7], v[228:235], v[44:47]
	v_mfma_f32_16x16x128_f8f6f4 v[40:43], v[8:15], v[228:235], v[40:43]
	s_setprio 0
	s_barrier
	ds_read_b128 v[4:7], v194
	ds_read_b128 v[8:11], v195
	ds_read_b128 v[0:3], v185
	ds_read_b128 v[16:19], v186
	ds_read_b128 v[12:15], v196
	ds_read_b128 v[20:23], v197
	ds_read_b128 v[24:27], v198
	ds_read_b128 v[28:31], v199
	s_add_u32 s34, s34, 0x20000
	s_addc_u32 s35, s35, 0
	s_mov_b32 m0, s31
	v_lshl_add_u64 v[236:237], s[34:35], 0, v[164:165]
	ds_read_b128 v[204:207], v200 offset:32768
	ds_read_b128 v[208:211], v200 offset:33792
	ds_read_b128 v[212:215], v200 offset:34816
	ds_read_b128 v[216:219], v200 offset:35840
	ds_read_b128 v[220:223], v200 offset:36864
	ds_read_b128 v[224:227], v200 offset:37888
	ds_read_b128 v[228:231], v200 offset:38912
	ds_read_b128 v[232:235], v200 offset:39936
	global_load_lds_dwordx4 v[236:237], off
	v_lshl_add_u64 v[236:237], s[34:35], 0, v[166:167]
	s_mov_b32 m0, s33
	s_nop 0
	global_load_lds_dwordx4 v[236:237], off
	s_waitcnt vmcnt(8)
	s_waitcnt lgkmcnt(0)
	s_barrier
	s_setprio 1
	s_waitcnt lgkmcnt(0)
	v_mfma_f32_16x16x128_f8f6f4 v[156:159], v[0:7], v[204:211], v[156:159]
	v_mfma_f32_16x16x128_f8f6f4 v[152:155], v[8:15], v[204:211], v[152:155]
	v_mfma_f32_16x16x128_f8f6f4 v[144:147], v[0:7], v[212:219], v[144:147]
	v_mfma_f32_16x16x128_f8f6f4 v[136:139], v[8:15], v[212:219], v[136:139]
	v_mfma_f32_16x16x128_f8f6f4 v[128:131], v[0:7], v[220:227], v[128:131]
	v_mfma_f32_16x16x128_f8f6f4 v[120:123], v[8:15], v[220:227], v[120:123]
	v_mfma_f32_16x16x128_f8f6f4 v[112:115], v[0:7], v[228:235], v[112:115]
	v_mfma_f32_16x16x128_f8f6f4 v[104:107], v[8:15], v[228:235], v[104:107]
	s_setprio 0
	s_setprio 1
	v_mfma_f32_16x16x128_f8f6f4 v[148:151], v[16:23], v[204:211], v[148:151]
	v_mfma_f32_16x16x128_f8f6f4 v[140:143], v[24:31], v[204:211], v[140:143]
	v_mfma_f32_16x16x128_f8f6f4 v[132:135], v[16:23], v[212:219], v[132:135]
	v_mfma_f32_16x16x128_f8f6f4 v[124:127], v[24:31], v[212:219], v[124:127]
	v_mfma_f32_16x16x128_f8f6f4 v[116:119], v[16:23], v[220:227], v[116:119]
	v_mfma_f32_16x16x128_f8f6f4 v[108:111], v[24:31], v[220:227], v[108:111]
	v_mfma_f32_16x16x128_f8f6f4 v[92:95], v[16:23], v[228:235], v[92:95]
	v_mfma_f32_16x16x128_f8f6f4 v[88:91], v[24:31], v[228:235], v[88:91]
	s_setprio 0
	s_barrier
	s_mov_b32 m0, s37
	v_lshl_add_u64 v[174:175], v[174:175], 0, s[2:3]
	s_add_u32 s26, s26, 0x20080
	ds_read_b128 v[204:207], v200 offset:49152
	ds_read_b128 v[208:211], v200 offset:50176
	ds_read_b128 v[212:215], v200 offset:51200
	ds_read_b128 v[216:219], v200 offset:52224
	ds_read_b128 v[220:223], v200 offset:53248
	ds_read_b128 v[224:227], v200 offset:54272
	ds_read_b128 v[228:231], v200 offset:55296
	ds_read_b128 v[232:235], v200 offset:56320
	global_load_lds_dwordx4 v[174:175], off
	v_lshl_add_u64 v[174:175], v[176:177], 0, s[2:3]
	s_mov_b32 m0, s38
	s_addc_u32 s27, s27, 0
	global_load_lds_dwordx4 v[174:175], off
	v_lshl_add_u64 v[174:175], s[26:27], 0, v[162:163]
	s_mov_b32 m0, s41
	s_nop 0
	global_load_lds_dwordx4 v[174:175], off
	v_lshl_add_u64 v[174:175], s[26:27], 0, v[160:161]
	s_mov_b32 m0, s42
	s_nop 0
	global_load_lds_dwordx4 v[174:175], off
	s_waitcnt vmcnt(6)
	s_waitcnt lgkmcnt(0)
	s_barrier
	s_setprio 1
	s_waitcnt lgkmcnt(0)
	v_mfma_f32_16x16x128_f8f6f4 v[76:79], v[0:7], v[204:211], v[76:79]
	v_mfma_f32_16x16x128_f8f6f4 v[72:75], v[8:15], v[204:211], v[72:75]
	v_mfma_f32_16x16x128_f8f6f4 v[52:55], v[0:7], v[212:219], v[52:55]
	v_mfma_f32_16x16x128_f8f6f4 v[48:51], v[8:15], v[212:219], v[48:51]
	v_mfma_f32_16x16x128_f8f6f4 v[60:63], v[0:7], v[220:227], v[60:63]
	v_mfma_f32_16x16x128_f8f6f4 v[56:59], v[8:15], v[220:227], v[56:59]
	v_mfma_f32_16x16x128_f8f6f4 v[36:39], v[0:7], v[228:235], v[36:39]
	v_mfma_f32_16x16x128_f8f6f4 v[32:35], v[8:15], v[228:235], v[32:35]
	s_setprio 0
	v_lshl_add_u64 v[174:175], v[178:179], 0, s[2:3]
	s_mov_b32 m0, s39
	s_nop 0
	global_load_lds_dwordx4 v[174:175], off
	v_lshl_add_u64 v[174:175], v[180:181], 0, s[2:3]
	s_mov_b32 m0, s40
	s_nop 0
	global_load_lds_dwordx4 v[174:175], off
	s_setprio 1
	v_mfma_f32_16x16x128_f8f6f4 v[100:103], v[16:23], v[204:211], v[100:103]
	v_mfma_f32_16x16x128_f8f6f4 v[96:99], v[24:31], v[204:211], v[96:99]
	v_mfma_f32_16x16x128_f8f6f4 v[84:87], v[16:23], v[212:219], v[84:87]
	v_mfma_f32_16x16x128_f8f6f4 v[80:83], v[24:31], v[212:219], v[80:83]
	v_mfma_f32_16x16x128_f8f6f4 v[68:71], v[16:23], v[220:227], v[68:71]
	v_mfma_f32_16x16x128_f8f6f4 v[64:67], v[24:31], v[220:227], v[64:67]
	v_mfma_f32_16x16x128_f8f6f4 v[44:47], v[16:23], v[228:235], v[44:47]
	v_mfma_f32_16x16x128_f8f6f4 v[40:43], v[24:31], v[228:235], v[40:43]
	s_setprio 0
	s_barrier
	s_add_i32 s50, s50, 2
	s_add_u32 s24, s24, 0x100
	s_addc_u32 s25, s25, 0
	s_add_u32 s48, s48, 0x100
	s_addc_u32 s49, s49, 0
	s_cmp_gt_u32 s50, 5
	s_cbranch_scc0 .LBB0_1175
	s_nop 15
	s_nop 7
	s_and_b64 vcc, exec, s[4:5]
	s_cbranch_vccz .LBB0_1178
	s_barrier

.LBB0_1501:
	ds_read_b128 v[20:23], v217
	ds_read_b128 v[24:27], v218
	ds_read_b128 v[16:19], v213
	ds_read_b128 v[0:3], v214
	ds_read_b128 v[28:31], v219
	ds_read_b128 v[4:7], v220
	ds_read_b128 v[8:11], v221
	ds_read_b128 v[12:15], v222
	s_add_u32 s6, s2, 0xfffe0080
	s_addc_u32 s7, s3, -1
	s_cmp_eq_u32 s55, 4
	s_cselect_b32 s53, s1, s7
	s_cselect_b32 s52, s5, s6
	s_cselect_b32 s7, s33, s54
	s_cselect_b32 s6, s43, s45
	v_lshl_add_u64 v[210:211], s[2:3], 0, v[194:195]
	s_add_i32 m0, s61, 0xc000
	ds_read_b128 v[160:163], v229
	ds_read_b128 v[164:167], v229 offset:1024
	ds_read_b128 v[168:171], v229 offset:2048
	ds_read_b128 v[172:175], v229 offset:3072
	ds_read_b128 v[176:179], v229 offset:4096
	ds_read_b128 v[180:183], v229 offset:5120
	ds_read_b128 v[202:205], v229 offset:6144
	ds_read_b128 v[206:209], v229 offset:7168
	global_load_lds_dwordx4 v[210:211], off
	v_lshl_add_u64 v[210:211], s[2:3], 0, v[196:197]
	s_add_i32 m0, s61, 0xe000
	s_nop 0
	global_load_lds_dwordx4 v[210:211], off
	s_waitcnt vmcnt(8)
	s_waitcnt lgkmcnt(0)
	s_barrier
	s_setprio 1
	s_waitcnt lgkmcnt(0)
	v_mfma_f32_16x16x128_f8f6f4 v[156:159], v[16:23], v[160:167], v[156:159]
	v_mfma_f32_16x16x128_f8f6f4 v[152:155], v[24:31], v[160:167], v[152:155]
	v_mfma_f32_16x16x128_f8f6f4 v[140:143], v[16:23], v[168:175], v[140:143]
	v_mfma_f32_16x16x128_f8f6f4 v[136:139], v[24:31], v[168:175], v[136:139]
	v_mfma_f32_16x16x128_f8f6f4 v[124:127], v[16:23], v[176:183], v[124:127]
	v_mfma_f32_16x16x128_f8f6f4 v[120:123], v[24:31], v[176:183], v[120:123]
	v_mfma_f32_16x16x128_f8f6f4 v[108:111], v[16:23], v[202:209], v[108:111]
	v_mfma_f32_16x16x128_f8f6f4 v[104:107], v[24:31], v[202:209], v[104:107]
	s_setprio 0
	s_setprio 1
	v_mfma_f32_16x16x128_f8f6f4 v[148:151], v[0:7], v[160:167], v[148:151]
	v_mfma_f32_16x16x128_f8f6f4 v[144:147], v[8:15], v[160:167], v[144:147]
	v_mfma_f32_16x16x128_f8f6f4 v[132:135], v[0:7], v[168:175], v[132:135]
	v_mfma_f32_16x16x128_f8f6f4 v[128:131], v[8:15], v[168:175], v[128:131]
	v_mfma_f32_16x16x128_f8f6f4 v[116:119], v[0:7], v[176:183], v[116:119]
	v_mfma_f32_16x16x128_f8f6f4 v[112:115], v[8:15], v[176:183], v[112:115]
	v_mfma_f32_16x16x128_f8f6f4 v[100:103], v[0:7], v[202:209], v[100:103]
	v_mfma_f32_16x16x128_f8f6f4 v[96:99], v[8:15], v[202:209], v[96:99]
	s_setprio 0
	s_barrier
	s_mov_b32 m0, s62
	v_lshl_add_u64 v[160:161], s[6:7], 0, v[184:185]
	s_add_u32 s56, s6, 0x20000
	ds_read_b128 v[168:171], v229 offset:16384
	ds_read_b128 v[172:175], v229 offset:17408
	ds_read_b128 v[176:179], v229 offset:18432
	ds_read_b128 v[180:183], v229 offset:19456
	ds_read_b128 v[202:205], v229 offset:20480
	ds_read_b128 v[206:209], v229 offset:21504
	ds_read_b128 v[236:239], v229 offset:22528
	ds_read_b128 v[240:243], v229 offset:23552
	global_load_lds_dwordx4 v[160:161], off
	v_lshl_add_u64 v[162:163], s[6:7], 0, v[186:187]
	s_mov_b32 m0, s63
	s_addc_u32 s57, s7, 0
	global_load_lds_dwordx4 v[162:163], off
	v_lshl_add_u64 v[164:165], s[56:57], 0, v[184:185]
	s_mov_b32 m0, s64
	v_lshl_add_u64 v[166:167], s[52:53], 0, v[190:191]
	global_load_lds_dwordx4 v[164:165], off
	v_lshl_add_u64 v[164:165], s[56:57], 0, v[186:187]
	s_mov_b32 m0, s65
	s_nop 0
	global_load_lds_dwordx4 v[164:165], off
	s_waitcnt vmcnt(6)
	s_waitcnt lgkmcnt(0)
	s_barrier
	s_setprio 1
	s_waitcnt lgkmcnt(0)
	v_mfma_f32_16x16x128_f8f6f4 v[84:87], v[16:23], v[168:175], v[84:87]
	v_mfma_f32_16x16x128_f8f6f4 v[80:83], v[24:31], v[168:175], v[80:83]
	v_mfma_f32_16x16x128_f8f6f4 v[68:71], v[16:23], v[176:183], v[68:71]
	v_mfma_f32_16x16x128_f8f6f4 v[64:67], v[24:31], v[176:183], v[64:67]
	v_mfma_f32_16x16x128_f8f6f4 v[56:59], v[16:23], v[202:209], v[56:59]
	v_mfma_f32_16x16x128_f8f6f4 v[48:51], v[24:31], v[202:209], v[48:51]
	v_mfma_f32_16x16x128_f8f6f4 v[40:43], v[16:23], v[236:243], v[40:43]
	v_mfma_f32_16x16x128_f8f6f4 v[32:35], v[24:31], v[236:243], v[32:35]
	s_setprio 0
	v_lshl_add_u64 v[164:165], s[52:53], 0, v[188:189]
	s_mov_b32 m0, s61
	s_nop 0
	global_load_lds_dwordx4 v[164:165], off
	s_mov_b32 m0, s66
	s_nop 0
	global_load_lds_dwordx4 v[166:167], off
	s_setprio 1
	v_mfma_f32_16x16x128_f8f6f4 v[92:95], v[0:7], v[168:175], v[92:95]
	v_mfma_f32_16x16x128_f8f6f4 v[88:91], v[8:15], v[168:175], v[88:91]
	v_mfma_f32_16x16x128_f8f6f4 v[76:79], v[0:7], v[176:183], v[76:79]
	v_mfma_f32_16x16x128_f8f6f4 v[72:75], v[8:15], v[176:183], v[72:75]
	v_mfma_f32_16x16x128_f8f6f4 v[60:63], v[0:7], v[202:209], v[60:63]
	v_mfma_f32_16x16x128_f8f6f4 v[52:55], v[8:15], v[202:209], v[52:55]
	v_mfma_f32_16x16x128_f8f6f4 v[44:47], v[0:7], v[236:243], v[44:47]
	v_mfma_f32_16x16x128_f8f6f4 v[36:39], v[8:15], v[236:243], v[36:39]
	s_setprio 0
	s_barrier
	ds_read_b128 v[4:7], v223
	ds_read_b128 v[8:11], v224
	ds_read_b128 v[0:3], v215
	ds_read_b128 v[16:19], v216
	ds_read_b128 v[12:15], v225
	ds_read_b128 v[20:23], v226
	ds_read_b128 v[24:27], v227
	ds_read_b128 v[28:31], v228
	s_add_u32 s52, s52, 0x20000
	s_addc_u32 s53, s53, 0
	s_mov_b32 m0, s67
	v_lshl_add_u64 v[210:211], s[52:53], 0, v[188:189]
	ds_read_b128 v[168:171], v229 offset:32768
	ds_read_b128 v[172:175], v229 offset:33792
	ds_read_b128 v[176:179], v229 offset:34816
	ds_read_b128 v[180:183], v229 offset:35840
	ds_read_b128 v[202:205], v229 offset:36864
	ds_read_b128 v[206:209], v229 offset:37888
	ds_read_b128 v[236:239], v229 offset:38912
	ds_read_b128 v[240:243], v229 offset:39936
	global_load_lds_dwordx4 v[210:211], off
	v_lshl_add_u64 v[210:211], s[52:53], 0, v[190:191]
	s_mov_b32 m0, s68
	s_nop 0
	global_load_lds_dwordx4 v[210:211], off
	s_waitcnt vmcnt(8)
	s_waitcnt lgkmcnt(0)
	s_barrier
	s_setprio 1
	s_waitcnt lgkmcnt(0)
	v_mfma_f32_16x16x128_f8f6f4 v[156:159], v[0:7], v[168:175], v[156:159]
	v_mfma_f32_16x16x128_f8f6f4 v[152:155], v[8:15], v[168:175], v[152:155]
	v_mfma_f32_16x16x128_f8f6f4 v[140:143], v[0:7], v[176:183], v[140:143]
	v_mfma_f32_16x16x128_f8f6f4 v[136:139], v[8:15], v[176:183], v[136:139]
	v_mfma_f32_16x16x128_f8f6f4 v[124:127], v[0:7], v[202:209], v[124:127]
	v_mfma_f32_16x16x128_f8f6f4 v[120:123], v[8:15], v[202:209], v[120:123]
	v_mfma_f32_16x16x128_f8f6f4 v[108:111], v[0:7], v[236:243], v[108:111]
	v_mfma_f32_16x16x128_f8f6f4 v[104:107], v[8:15], v[236:243], v[104:107]
	s_setprio 0
	s_setprio 1
	v_mfma_f32_16x16x128_f8f6f4 v[148:151], v[16:23], v[168:175], v[148:151]
	v_mfma_f32_16x16x128_f8f6f4 v[144:147], v[24:31], v[168:175], v[144:147]
	v_mfma_f32_16x16x128_f8f6f4 v[132:135], v[16:23], v[176:183], v[132:135]
	v_mfma_f32_16x16x128_f8f6f4 v[128:131], v[24:31], v[176:183], v[128:131]
	v_mfma_f32_16x16x128_f8f6f4 v[116:119], v[16:23], v[202:209], v[116:119]
	v_mfma_f32_16x16x128_f8f6f4 v[112:115], v[24:31], v[202:209], v[112:115]
	v_mfma_f32_16x16x128_f8f6f4 v[100:103], v[16:23], v[236:243], v[100:103]
	v_mfma_f32_16x16x128_f8f6f4 v[96:99], v[24:31], v[236:243], v[96:99]
	s_setprio 0
	s_barrier
	s_mov_b32 m0, s11
	v_lshl_add_u64 v[160:161], v[160:161], 0, s[30:31]
	s_add_u32 s6, s6, 0x20080
	ds_read_b128 v[168:171], v229 offset:49152
	ds_read_b128 v[172:175], v229 offset:50176
	ds_read_b128 v[176:179], v229 offset:51200
	ds_read_b128 v[180:183], v229 offset:52224
	ds_read_b128 v[202:205], v229 offset:53248
	ds_read_b128 v[206:209], v229 offset:54272
	ds_read_b128 v[236:239], v229 offset:55296
	ds_read_b128 v[240:243], v229 offset:56320
	global_load_lds_dwordx4 v[160:161], off
	v_lshl_add_u64 v[160:161], v[162:163], 0, s[30:31]
	s_mov_b32 m0, s39
	s_addc_u32 s7, s7, 0
	global_load_lds_dwordx4 v[160:161], off
	v_lshl_add_u64 v[160:161], s[6:7], 0, v[184:185]
	s_mov_b32 m0, s20
	s_nop 0
	global_load_lds_dwordx4 v[160:161], off
	v_lshl_add_u64 v[160:161], s[6:7], 0, v[186:187]
	s_mov_b32 m0, s21
	s_nop 0
	global_load_lds_dwordx4 v[160:161], off
	s_waitcnt vmcnt(6)
	s_waitcnt lgkmcnt(0)
	s_barrier
	s_setprio 1
	s_waitcnt lgkmcnt(0)
	v_mfma_f32_16x16x128_f8f6f4 v[84:87], v[0:7], v[168:175], v[84:87]
	v_mfma_f32_16x16x128_f8f6f4 v[80:83], v[8:15], v[168:175], v[80:83]
	v_mfma_f32_16x16x128_f8f6f4 v[68:71], v[0:7], v[176:183], v[68:71]
	v_mfma_f32_16x16x128_f8f6f4 v[64:67], v[8:15], v[176:183], v[64:67]
	v_mfma_f32_16x16x128_f8f6f4 v[56:59], v[0:7], v[202:209], v[56:59]
	v_mfma_f32_16x16x128_f8f6f4 v[48:51], v[8:15], v[202:209], v[48:51]
	v_mfma_f32_16x16x128_f8f6f4 v[40:43], v[0:7], v[236:243], v[40:43]
	v_mfma_f32_16x16x128_f8f6f4 v[32:35], v[8:15], v[236:243], v[32:35]
	s_setprio 0
	v_lshl_add_u64 v[160:161], v[164:165], 0, s[30:31]
	s_mov_b32 m0, s18
	s_nop 0
	global_load_lds_dwordx4 v[160:161], off
	v_lshl_add_u64 v[160:161], v[166:167], 0, s[30:31]
	s_mov_b32 m0, s19
	s_nop 0
	global_load_lds_dwordx4 v[160:161], off
	s_setprio 1
	v_mfma_f32_16x16x128_f8f6f4 v[92:95], v[16:23], v[168:175], v[92:95]
	v_mfma_f32_16x16x128_f8f6f4 v[88:91], v[24:31], v[168:175], v[88:91]
	v_mfma_f32_16x16x128_f8f6f4 v[76:79], v[16:23], v[176:183], v[76:79]
	v_mfma_f32_16x16x128_f8f6f4 v[72:75], v[24:31], v[176:183], v[72:75]
	v_mfma_f32_16x16x128_f8f6f4 v[60:63], v[16:23], v[202:209], v[60:63]
	v_mfma_f32_16x16x128_f8f6f4 v[52:55], v[24:31], v[202:209], v[52:55]
	v_mfma_f32_16x16x128_f8f6f4 v[44:47], v[16:23], v[236:243], v[44:47]
	v_mfma_f32_16x16x128_f8f6f4 v[36:39], v[24:31], v[236:243], v[36:39]
	s_setprio 0
	s_barrier
	s_add_i32 s55, s55, 2
	s_add_u32 s2, s2, 0x100
	s_addc_u32 s3, s3, 0
	s_add_u32 s45, s45, 0x100
	s_addc_u32 s54, s54, 0
	s_cmp_gt_u32 s55, 5
	s_cbranch_scc0 .LBB0_1501
	s_nop 15
	s_nop 7
	s_and_b64 vcc, exec, s[34:35]
	s_cbranch_vccz .LBB0_1504
	s_barrier

.LBB0_1692:
	s_add_u32 s42, s90, s4
	s_addc_u32 s43, s91, s5
	s_add_u32 s73, s42, 0x21c00100
	s_addc_u32 s74, s43, 0
	s_cmpk_eq_i32 s4, 0x300
	v_lshl_add_u64 v[0:1], v[180:181], 0, s[4:5]
	s_cselect_b64 vcc, -1, 0
	v_cndmask_b32_e32 v183, v1, v167, vcc
	v_cndmask_b32_e32 v182, v0, v220, vcc
	ds_read_b128 v[8:11], v194
	ds_read_b128 v[12:15], v198
	ds_read_b128 v[24:27], v199
	ds_read_b128 v[28:31], v200
	ds_read_b128 v[0:3], v195
	ds_read_b128 v[4:7], v201
	ds_read_b128 v[16:19], v202
	ds_read_b128 v[20:23], v203
	s_and_b64 s[42:43], vcc, exec
	s_cselect_b32 s43, s9, s74
	s_cselect_b32 s42, s8, s73
	v_cndmask_b32_e32 v160, v219, v215, vcc
	v_cndmask_b32_e32 v184, v170, v216, vcc
	v_cndmask_b32_e32 v175, v172, v217, vcc
	v_cndmask_b32_e32 v173, v174, v218, vcc
	v_lshl_add_u64 v[186:187], v[178:179], 0, s[4:5]
	s_add_i32 m0, s0, 0xc000
	ds_read_b128 v[222:225], v212
	ds_read_b128 v[226:229], v212 offset:1024
	ds_read_b128 v[230:233], v212 offset:2048
	ds_read_b128 v[234:237], v212 offset:3072
	ds_read_b128 v[238:241], v212 offset:4096
	ds_read_b128 v[242:245], v212 offset:5120
	ds_read_b128 v[246:249], v212 offset:6144
	ds_read_b128 v[250:253], v212 offset:7168
	global_load_lds_dwordx4 v[186:187], off
	v_lshl_add_u64 v[186:187], v[176:177], 0, s[4:5]
	s_add_i32 m0, s0, 0xe000
	s_nop 0
	global_load_lds_dwordx4 v[186:187], off
	s_waitcnt vmcnt(8)
	s_waitcnt lgkmcnt(0)
	s_barrier
	s_setprio 1
	s_waitcnt lgkmcnt(0)
	v_mfma_f32_16x16x128_f8f6f4 v[156:159], v[8:15], v[222:229], v[156:159]
	v_mfma_f32_16x16x128_f8f6f4 v[152:155], v[24:31], v[222:229], v[152:155]
	v_mfma_f32_16x16x128_f8f6f4 v[140:143], v[8:15], v[230:237], v[140:143]
	v_mfma_f32_16x16x128_f8f6f4 v[136:139], v[24:31], v[230:237], v[136:139]
	v_mfma_f32_16x16x128_f8f6f4 v[124:127], v[8:15], v[238:245], v[124:127]
	v_mfma_f32_16x16x128_f8f6f4 v[120:123], v[24:31], v[238:245], v[120:123]
	v_mfma_f32_16x16x128_f8f6f4 v[108:111], v[8:15], v[246:253], v[108:111]
	v_mfma_f32_16x16x128_f8f6f4 v[104:107], v[24:31], v[246:253], v[104:107]
	s_setprio 0
	s_setprio 1
	v_mfma_f32_16x16x128_f8f6f4 v[148:151], v[0:7], v[222:229], v[148:151]
	v_mfma_f32_16x16x128_f8f6f4 v[144:147], v[16:23], v[222:229], v[144:147]
	v_mfma_f32_16x16x128_f8f6f4 v[132:135], v[0:7], v[230:237], v[132:135]
	v_mfma_f32_16x16x128_f8f6f4 v[128:131], v[16:23], v[230:237], v[128:131]
	v_mfma_f32_16x16x128_f8f6f4 v[116:119], v[0:7], v[238:245], v[116:119]
	v_mfma_f32_16x16x128_f8f6f4 v[112:115], v[16:23], v[238:245], v[112:115]
	v_mfma_f32_16x16x128_f8f6f4 v[100:103], v[0:7], v[246:253], v[100:103]
	v_mfma_f32_16x16x128_f8f6f4 v[96:99], v[16:23], v[246:253], v[96:99]
	s_setprio 0
	s_barrier
	s_mov_b32 m0, s21
	v_lshl_add_u64 v[186:187], v[182:183], 0, v[164:165]
	ds_read_b128 v[222:225], v212 offset:16384
	ds_read_b128 v[226:229], v212 offset:17408
	ds_read_b128 v[230:233], v212 offset:18432
	ds_read_b128 v[234:237], v212 offset:19456
	ds_read_b128 v[238:241], v212 offset:20480
	ds_read_b128 v[242:245], v212 offset:21504
	ds_read_b128 v[246:249], v212 offset:22528
	ds_read_b128 v[250:253], v212 offset:23552
	global_load_lds_dwordx4 v[186:187], off
	v_lshl_add_u64 v[188:189], v[182:183], 0, v[162:163]
	s_mov_b32 m0, s22
	v_lshl_add_u64 v[190:191], v[182:183], 0, s[12:13]
	global_load_lds_dwordx4 v[188:189], off
	v_lshl_add_u64 v[192:193], v[190:191], 0, v[164:165]
	s_mov_b32 m0, s23
	v_lshl_add_u64 v[190:191], v[190:191], 0, v[162:163]
	global_load_lds_dwordx4 v[192:193], off
	s_mov_b32 m0, s33
	v_mov_b32_e32 v185, v161
	global_load_lds_dwordx4 v[190:191], off
	s_mov_b32 m0, s0
	v_lshl_add_u64 v[190:191], s[42:43], 0, v[160:161]
	global_load_lds_dwordx4 v160, s[42:43]
	s_mov_b32 m0, s44
	s_nop 0
	global_load_lds_dwordx4 v184, s[42:43]
	s_waitcnt vmcnt(8)
	s_waitcnt lgkmcnt(0)
	v_lshl_add_u64 v[184:185], s[42:43], 0, v[184:185]
	s_barrier
	s_setprio 1
	s_waitcnt lgkmcnt(0)
	v_mfma_f32_16x16x128_f8f6f4 v[84:87], v[8:15], v[222:229], v[84:87]
	v_mfma_f32_16x16x128_f8f6f4 v[80:83], v[24:31], v[222:229], v[80:83]
	v_mfma_f32_16x16x128_f8f6f4 v[68:71], v[8:15], v[230:237], v[68:71]
	v_mfma_f32_16x16x128_f8f6f4 v[64:67], v[24:31], v[230:237], v[64:67]
	v_mfma_f32_16x16x128_f8f6f4 v[52:55], v[8:15], v[238:245], v[52:55]
	v_mfma_f32_16x16x128_f8f6f4 v[48:51], v[24:31], v[238:245], v[48:51]
	v_mfma_f32_16x16x128_f8f6f4 v[36:39], v[8:15], v[246:253], v[36:39]
	v_mfma_f32_16x16x128_f8f6f4 v[32:35], v[24:31], v[246:253], v[32:35]
	s_setprio 0
	s_setprio 1
	v_mfma_f32_16x16x128_f8f6f4 v[92:95], v[0:7], v[222:229], v[92:95]
	v_mfma_f32_16x16x128_f8f6f4 v[88:91], v[16:23], v[222:229], v[88:91]
	v_mfma_f32_16x16x128_f8f6f4 v[76:79], v[0:7], v[230:237], v[76:79]
	v_mfma_f32_16x16x128_f8f6f4 v[72:75], v[16:23], v[230:237], v[72:75]
	v_mfma_f32_16x16x128_f8f6f4 v[60:63], v[0:7], v[238:245], v[60:63]
	v_mfma_f32_16x16x128_f8f6f4 v[56:59], v[16:23], v[238:245], v[56:59]
	v_mfma_f32_16x16x128_f8f6f4 v[44:47], v[0:7], v[246:253], v[44:47]
	v_mfma_f32_16x16x128_f8f6f4 v[40:43], v[16:23], v[246:253], v[40:43]
	s_setprio 0
	s_barrier
	ds_read_b128 v[4:7], v204
	ds_read_b128 v[8:11], v205
	ds_read_b128 v[0:3], v196
	ds_read_b128 v[16:19], v197
	ds_read_b128 v[12:15], v206
	ds_read_b128 v[20:23], v207
	ds_read_b128 v[24:27], v208
	ds_read_b128 v[28:31], v209
	s_mov_b32 m0, s45
	ds_read_b128 v[222:225], v212 offset:32768
	ds_read_b128 v[226:229], v212 offset:33792
	ds_read_b128 v[230:233], v212 offset:34816
	ds_read_b128 v[234:237], v212 offset:35840
	ds_read_b128 v[238:241], v212 offset:36864
	ds_read_b128 v[242:245], v212 offset:37888
	ds_read_b128 v[246:249], v212 offset:38912
	ds_read_b128 v[250:253], v212 offset:39936
	global_load_lds_dwordx4 v175, s[42:43]
	s_mov_b32 m0, s46
	s_nop 0
	global_load_lds_dwordx4 v173, s[42:43]
	s_waitcnt vmcnt(8)
	s_waitcnt lgkmcnt(0)
	s_barrier
	s_setprio 1
	s_waitcnt lgkmcnt(0)
	v_mfma_f32_16x16x128_f8f6f4 v[156:159], v[0:7], v[222:229], v[156:159]
	v_mfma_f32_16x16x128_f8f6f4 v[152:155], v[8:15], v[222:229], v[152:155]
	v_mfma_f32_16x16x128_f8f6f4 v[140:143], v[0:7], v[230:237], v[140:143]
	v_mfma_f32_16x16x128_f8f6f4 v[136:139], v[8:15], v[230:237], v[136:139]
	v_mfma_f32_16x16x128_f8f6f4 v[124:127], v[0:7], v[238:245], v[124:127]
	v_mfma_f32_16x16x128_f8f6f4 v[120:123], v[8:15], v[238:245], v[120:123]
	v_mfma_f32_16x16x128_f8f6f4 v[108:111], v[0:7], v[246:253], v[108:111]
	v_mfma_f32_16x16x128_f8f6f4 v[104:107], v[8:15], v[246:253], v[104:107]
	s_setprio 0
	s_setprio 1
	v_mfma_f32_16x16x128_f8f6f4 v[148:151], v[16:23], v[222:229], v[148:151]
	v_mfma_f32_16x16x128_f8f6f4 v[144:147], v[24:31], v[222:229], v[144:147]
	v_mfma_f32_16x16x128_f8f6f4 v[132:135], v[16:23], v[230:237], v[132:135]
	v_mfma_f32_16x16x128_f8f6f4 v[128:131], v[24:31], v[230:237], v[128:131]
	v_mfma_f32_16x16x128_f8f6f4 v[116:119], v[16:23], v[238:245], v[116:119]
	v_mfma_f32_16x16x128_f8f6f4 v[112:115], v[24:31], v[238:245], v[112:115]
	v_mfma_f32_16x16x128_f8f6f4 v[100:103], v[16:23], v[246:253], v[100:103]
	v_mfma_f32_16x16x128_f8f6f4 v[96:99], v[24:31], v[246:253], v[96:99]
	s_setprio 0
	s_barrier
	s_mov_b32 m0, s47
	v_lshl_add_u64 v[186:187], v[186:187], 0, s[16:17]
	ds_read_b128 v[222:225], v212 offset:49152
	ds_read_b128 v[226:229], v212 offset:50176
	ds_read_b128 v[230:233], v212 offset:51200
	ds_read_b128 v[234:237], v212 offset:52224
	ds_read_b128 v[238:241], v212 offset:53248
	ds_read_b128 v[242:245], v212 offset:54272
	ds_read_b128 v[246:249], v212 offset:55296
	ds_read_b128 v[250:253], v212 offset:56320
	global_load_lds_dwordx4 v[186:187], off
	v_lshl_add_u64 v[186:187], v[188:189], 0, s[16:17]
	s_mov_b32 m0, s48
	v_lshl_add_u64 v[182:183], v[182:183], 0, s[34:35]
	global_load_lds_dwordx4 v[186:187], off
	v_lshl_add_u64 v[186:187], v[182:183], 0, v[164:165]
	s_mov_b32 m0, s51
	v_lshl_add_u64 v[182:183], v[182:183], 0, v[162:163]
	global_load_lds_dwordx4 v[186:187], off
	s_mov_b32 m0, s52
	s_nop 0
	global_load_lds_dwordx4 v[182:183], off
	s_waitcnt vmcnt(6)
	s_waitcnt lgkmcnt(0)
	s_barrier
	s_setprio 1
	s_waitcnt lgkmcnt(0)
	v_mfma_f32_16x16x128_f8f6f4 v[84:87], v[0:7], v[222:229], v[84:87]
	v_mfma_f32_16x16x128_f8f6f4 v[80:83], v[8:15], v[222:229], v[80:83]
	v_mfma_f32_16x16x128_f8f6f4 v[68:71], v[0:7], v[230:237], v[68:71]
	v_mfma_f32_16x16x128_f8f6f4 v[64:67], v[8:15], v[230:237], v[64:67]
	v_mfma_f32_16x16x128_f8f6f4 v[52:55], v[0:7], v[238:245], v[52:55]
	v_mfma_f32_16x16x128_f8f6f4 v[48:51], v[8:15], v[238:245], v[48:51]
	v_mfma_f32_16x16x128_f8f6f4 v[36:39], v[0:7], v[246:253], v[36:39]
	v_mfma_f32_16x16x128_f8f6f4 v[32:35], v[8:15], v[246:253], v[32:35]
	s_setprio 0
	v_lshl_add_u64 v[182:183], v[190:191], 0, s[16:17]
	s_mov_b32 m0, s49
	s_nop 0
	global_load_lds_dwordx4 v[182:183], off
	v_lshl_add_u64 v[182:183], v[184:185], 0, s[16:17]
	s_mov_b32 m0, s50
	s_nop 0
	global_load_lds_dwordx4 v[182:183], off
	s_setprio 1
	v_mfma_f32_16x16x128_f8f6f4 v[92:95], v[16:23], v[222:229], v[92:95]
	v_mfma_f32_16x16x128_f8f6f4 v[88:91], v[24:31], v[222:229], v[88:91]
	v_mfma_f32_16x16x128_f8f6f4 v[76:79], v[16:23], v[230:237], v[76:79]
	v_mfma_f32_16x16x128_f8f6f4 v[72:75], v[24:31], v[230:237], v[72:75]
	v_mfma_f32_16x16x128_f8f6f4 v[60:63], v[16:23], v[238:245], v[60:63]
	v_mfma_f32_16x16x128_f8f6f4 v[56:59], v[24:31], v[238:245], v[56:59]
	v_mfma_f32_16x16x128_f8f6f4 v[44:47], v[16:23], v[246:253], v[44:47]
	v_mfma_f32_16x16x128_f8f6f4 v[40:43], v[24:31], v[246:253], v[40:43]
	s_setprio 0
	s_barrier
	s_add_i32 s41, s41, 2
	s_add_u32 s4, s4, 0x100
	s_addc_u32 s5, s5, 0
	s_cmp_gt_u32 s41, 5
	s_cbranch_scc0 .LBB0_1692
	s_nop 15
	s_nop 7
	s_and_b64 vcc, exec, s[36:37]
	s_cbranch_vccz .LBB0_1695
	s_barrier

.LBB0_1790:
	v_lshl_add_u64 v[0:1], v[168:169], 0, s[42:43]
	v_lshl_add_u64 v[0:1], v[0:1], 0, s[94:95]
	v_cndmask_b32_e64 v179, v1, v171, s[40:41]
	v_cndmask_b32_e64 v178, v0, v205, s[40:41]
	ds_read_b128 v[8:11], v185
	ds_read_b128 v[12:15], v189
	ds_read_b128 v[24:27], v190
	ds_read_b128 v[28:31], v191
	ds_read_b128 v[0:3], v186
	ds_read_b128 v[4:7], v192
	ds_read_b128 v[16:19], v193
	ds_read_b128 v[20:23], v194
	s_add_u32 s15, s30, s42
	s_addc_u32 s93, s31, s43
	s_add_u32 vcc_lo, s15, 0x100
	s_addc_u32 vcc_hi, s93, 0
	s_and_b64 s[44:45], s[40:41], exec
	s_cselect_b32 s45, s35, vcc_hi
	s_cselect_b32 s44, s92, vcc_lo
	s_add_u32 s42, s15, 0x10080
	s_addc_u32 s43, s93, 0
	s_add_i32 m0, s22, 0xc000
	s_add_i32 s15, s22, 0xe000
	s_add_u32 s40, s44, 0x10000
	s_addc_u32 s41, s45, 0
	v_lshl_add_u64 v[180:181], v[178:179], 0, s[0:1]
	v_lshl_add_u64 v[174:175], v[178:179], 0, s[10:11]
	v_lshl_add_u64 v[176:177], s[42:43], 0, v[164:165]
	ds_read_b128 v[206:209], v203
	ds_read_b128 v[210:213], v203 offset:1024
	ds_read_b128 v[214:217], v203 offset:2048
	ds_read_b128 v[218:221], v203 offset:3072
	ds_read_b128 v[222:225], v203 offset:4096
	ds_read_b128 v[226:229], v203 offset:5120
	ds_read_b128 v[230:233], v203 offset:6144
	ds_read_b128 v[234:237], v203 offset:7168
	global_load_lds_dwordx4 v[176:177], off
	v_lshl_add_u64 v[176:177], s[42:43], 0, v[166:167]
	s_mov_b32 m0, s15
	s_nop 0
	global_load_lds_dwordx4 v[176:177], off
	s_waitcnt vmcnt(8)
	s_waitcnt lgkmcnt(0)
	s_barrier
	s_setprio 1
	s_waitcnt lgkmcnt(0)
	v_mfma_f32_16x16x128_f8f6f4 v[156:159], v[8:15], v[206:213], v[156:159]
	v_mfma_f32_16x16x128_f8f6f4 v[152:155], v[24:31], v[206:213], v[152:155]
	v_mfma_f32_16x16x128_f8f6f4 v[140:143], v[8:15], v[214:221], v[140:143]
	v_mfma_f32_16x16x128_f8f6f4 v[136:139], v[24:31], v[214:221], v[136:139]
	v_mfma_f32_16x16x128_f8f6f4 v[124:127], v[8:15], v[222:229], v[124:127]
	v_mfma_f32_16x16x128_f8f6f4 v[120:123], v[24:31], v[222:229], v[120:123]
	v_mfma_f32_16x16x128_f8f6f4 v[108:111], v[8:15], v[230:237], v[108:111]
	v_mfma_f32_16x16x128_f8f6f4 v[104:107], v[24:31], v[230:237], v[104:107]
	s_setprio 0
	s_setprio 1
	v_mfma_f32_16x16x128_f8f6f4 v[148:151], v[0:7], v[206:213], v[148:151]
	v_mfma_f32_16x16x128_f8f6f4 v[144:147], v[16:23], v[206:213], v[144:147]
	v_mfma_f32_16x16x128_f8f6f4 v[132:135], v[0:7], v[214:221], v[132:135]
	v_mfma_f32_16x16x128_f8f6f4 v[128:131], v[16:23], v[214:221], v[128:131]
	v_mfma_f32_16x16x128_f8f6f4 v[116:119], v[0:7], v[222:229], v[116:119]
	v_mfma_f32_16x16x128_f8f6f4 v[112:115], v[16:23], v[222:229], v[112:115]
	v_mfma_f32_16x16x128_f8f6f4 v[96:99], v[0:7], v[230:237], v[96:99]
	v_mfma_f32_16x16x128_f8f6f4 v[88:91], v[16:23], v[230:237], v[88:91]
	s_setprio 0
	s_barrier
	s_mov_b32 m0, s23
	v_lshl_add_u64 v[176:177], v[178:179], 0, v[162:163]
	ds_read_b128 v[206:209], v203 offset:16384
	ds_read_b128 v[210:213], v203 offset:17408
	ds_read_b128 v[214:217], v203 offset:18432
	ds_read_b128 v[218:221], v203 offset:19456
	ds_read_b128 v[222:225], v203 offset:20480
	ds_read_b128 v[226:229], v203 offset:21504
	ds_read_b128 v[230:233], v203 offset:22528
	ds_read_b128 v[234:237], v203 offset:23552
	global_load_lds_dwordx4 v[176:177], off
	v_lshl_add_u64 v[178:179], v[178:179], 0, v[160:161]
	s_mov_b32 m0, s33
	v_lshl_add_u64 v[182:183], v[180:181], 0, v[162:163]
	global_load_lds_dwordx4 v[178:179], off
	s_mov_b32 m0, s46
	v_lshl_add_u64 v[180:181], v[180:181], 0, v[160:161]
	global_load_lds_dwordx4 v[182:183], off
	s_mov_b32 m0, s47
	v_lshl_add_u64 v[182:183], s[44:45], 0, v[166:167]
	global_load_lds_dwordx4 v[180:181], off
	s_waitcnt vmcnt(6)
	s_waitcnt lgkmcnt(0)
	s_barrier
	s_setprio 1
	s_waitcnt lgkmcnt(0)
	v_mfma_f32_16x16x128_f8f6f4 v[84:87], v[8:15], v[206:213], v[84:87]
	v_mfma_f32_16x16x128_f8f6f4 v[76:79], v[24:31], v[206:213], v[76:79]
	v_mfma_f32_16x16x128_f8f6f4 v[60:63], v[8:15], v[214:221], v[60:63]
	v_mfma_f32_16x16x128_f8f6f4 v[48:51], v[24:31], v[214:221], v[48:51]
	v_mfma_f32_16x16x128_f8f6f4 v[68:71], v[8:15], v[222:229], v[68:71]
	v_mfma_f32_16x16x128_f8f6f4 v[56:59], v[24:31], v[222:229], v[56:59]
	v_mfma_f32_16x16x128_f8f6f4 v[44:47], v[8:15], v[230:237], v[44:47]
	v_mfma_f32_16x16x128_f8f6f4 v[36:39], v[24:31], v[230:237], v[36:39]
	s_setprio 0
	v_lshl_add_u64 v[180:181], s[44:45], 0, v[164:165]
	s_mov_b32 m0, s22
	s_nop 0
	global_load_lds_dwordx4 v[180:181], off
	s_mov_b32 m0, s48
	s_nop 0
	global_load_lds_dwordx4 v[182:183], off
	s_setprio 1
	v_mfma_f32_16x16x128_f8f6f4 v[100:103], v[0:7], v[206:213], v[100:103]
	v_mfma_f32_16x16x128_f8f6f4 v[92:95], v[16:23], v[206:213], v[92:95]
	v_mfma_f32_16x16x128_f8f6f4 v[80:83], v[0:7], v[214:221], v[80:83]
	v_mfma_f32_16x16x128_f8f6f4 v[72:75], v[16:23], v[214:221], v[72:75]
	v_mfma_f32_16x16x128_f8f6f4 v[64:67], v[0:7], v[222:229], v[64:67]
	v_mfma_f32_16x16x128_f8f6f4 v[52:55], v[16:23], v[222:229], v[52:55]
	v_mfma_f32_16x16x128_f8f6f4 v[40:43], v[0:7], v[230:237], v[40:43]
	v_mfma_f32_16x16x128_f8f6f4 v[32:35], v[16:23], v[230:237], v[32:35]
	s_setprio 0
	s_barrier
	ds_read_b128 v[4:7], v195
	ds_read_b128 v[8:11], v196
	ds_read_b128 v[0:3], v187
	ds_read_b128 v[16:19], v188
	ds_read_b128 v[12:15], v197
	ds_read_b128 v[20:23], v198
	ds_read_b128 v[24:27], v199
	ds_read_b128 v[28:31], v200
	s_mov_b32 m0, s49
	v_lshl_add_u64 v[238:239], s[40:41], 0, v[164:165]
	ds_read_b128 v[206:209], v203 offset:32768
	ds_read_b128 v[210:213], v203 offset:33792
	ds_read_b128 v[214:217], v203 offset:34816
	ds_read_b128 v[218:221], v203 offset:35840
	ds_read_b128 v[222:225], v203 offset:36864
	ds_read_b128 v[226:229], v203 offset:37888
	ds_read_b128 v[230:233], v203 offset:38912
	ds_read_b128 v[234:237], v203 offset:39936
	global_load_lds_dwordx4 v[238:239], off
	v_lshl_add_u64 v[238:239], s[40:41], 0, v[166:167]
	s_mov_b32 m0, s50
	s_nop 0
	global_load_lds_dwordx4 v[238:239], off
	s_waitcnt vmcnt(8)
	s_waitcnt lgkmcnt(0)
	s_barrier
	s_setprio 1
	s_waitcnt lgkmcnt(0)
	v_mfma_f32_16x16x128_f8f6f4 v[156:159], v[0:7], v[206:213], v[156:159]
	v_mfma_f32_16x16x128_f8f6f4 v[152:155], v[8:15], v[206:213], v[152:155]
	v_mfma_f32_16x16x128_f8f6f4 v[140:143], v[0:7], v[214:221], v[140:143]
	v_mfma_f32_16x16x128_f8f6f4 v[136:139], v[8:15], v[214:221], v[136:139]
	v_mfma_f32_16x16x128_f8f6f4 v[124:127], v[0:7], v[222:229], v[124:127]
	v_mfma_f32_16x16x128_f8f6f4 v[120:123], v[8:15], v[222:229], v[120:123]
	v_mfma_f32_16x16x128_f8f6f4 v[108:111], v[0:7], v[230:237], v[108:111]
	v_mfma_f32_16x16x128_f8f6f4 v[104:107], v[8:15], v[230:237], v[104:107]
	s_setprio 0
	s_setprio 1
	v_mfma_f32_16x16x128_f8f6f4 v[148:151], v[16:23], v[206:213], v[148:151]
	v_mfma_f32_16x16x128_f8f6f4 v[144:147], v[24:31], v[206:213], v[144:147]
	v_mfma_f32_16x16x128_f8f6f4 v[132:135], v[16:23], v[214:221], v[132:135]
	v_mfma_f32_16x16x128_f8f6f4 v[128:131], v[24:31], v[214:221], v[128:131]
	v_mfma_f32_16x16x128_f8f6f4 v[116:119], v[16:23], v[222:229], v[116:119]
	v_mfma_f32_16x16x128_f8f6f4 v[112:115], v[24:31], v[222:229], v[112:115]
	v_mfma_f32_16x16x128_f8f6f4 v[96:99], v[16:23], v[230:237], v[96:99]
	v_mfma_f32_16x16x128_f8f6f4 v[88:91], v[24:31], v[230:237], v[88:91]
	s_setprio 0
	s_barrier
	s_mov_b32 m0, s52
	v_lshl_add_u64 v[176:177], v[176:177], 0, s[8:9]
	ds_read_b128 v[206:209], v203 offset:49152
	ds_read_b128 v[210:213], v203 offset:50176
	ds_read_b128 v[214:217], v203 offset:51200
	ds_read_b128 v[218:221], v203 offset:52224
	ds_read_b128 v[222:225], v203 offset:53248
	ds_read_b128 v[226:229], v203 offset:54272
	ds_read_b128 v[230:233], v203 offset:55296
	ds_read_b128 v[234:237], v203 offset:56320
	global_load_lds_dwordx4 v[176:177], off
	v_lshl_add_u64 v[176:177], v[178:179], 0, s[8:9]
	s_mov_b32 m0, s53
	s_nop 0
	global_load_lds_dwordx4 v[176:177], off
	v_lshl_add_u64 v[176:177], v[174:175], 0, v[162:163]
	s_mov_b32 m0, s56
	v_lshl_add_u64 v[174:175], v[174:175], 0, v[160:161]
	global_load_lds_dwordx4 v[176:177], off
	s_mov_b32 m0, s57
	s_nop 0
	global_load_lds_dwordx4 v[174:175], off
	s_waitcnt vmcnt(6)
	s_waitcnt lgkmcnt(0)
	s_barrier
	s_setprio 1
	s_waitcnt lgkmcnt(0)
	v_mfma_f32_16x16x128_f8f6f4 v[84:87], v[0:7], v[206:213], v[84:87]
	v_mfma_f32_16x16x128_f8f6f4 v[76:79], v[8:15], v[206:213], v[76:79]
	v_mfma_f32_16x16x128_f8f6f4 v[60:63], v[0:7], v[214:221], v[60:63]
	v_mfma_f32_16x16x128_f8f6f4 v[48:51], v[8:15], v[214:221], v[48:51]
	v_mfma_f32_16x16x128_f8f6f4 v[68:71], v[0:7], v[222:229], v[68:71]
	v_mfma_f32_16x16x128_f8f6f4 v[56:59], v[8:15], v[222:229], v[56:59]
	v_mfma_f32_16x16x128_f8f6f4 v[44:47], v[0:7], v[230:237], v[44:47]
	v_mfma_f32_16x16x128_f8f6f4 v[36:39], v[8:15], v[230:237], v[36:39]
	s_setprio 0
	v_lshl_add_u64 v[174:175], v[180:181], 0, s[8:9]
	s_mov_b32 m0, s54
	s_nop 0
	global_load_lds_dwordx4 v[174:175], off
	v_lshl_add_u64 v[174:175], v[182:183], 0, s[8:9]
	s_mov_b32 m0, s55
	s_nop 0
	global_load_lds_dwordx4 v[174:175], off
	s_setprio 1
	v_mfma_f32_16x16x128_f8f6f4 v[100:103], v[16:23], v[206:213], v[100:103]
	v_mfma_f32_16x16x128_f8f6f4 v[92:95], v[24:31], v[206:213], v[92:95]
	v_mfma_f32_16x16x128_f8f6f4 v[80:83], v[16:23], v[214:221], v[80:83]
	v_mfma_f32_16x16x128_f8f6f4 v[72:75], v[24:31], v[214:221], v[72:75]
	v_mfma_f32_16x16x128_f8f6f4 v[64:67], v[16:23], v[222:229], v[64:67]
	v_mfma_f32_16x16x128_f8f6f4 v[52:55], v[24:31], v[222:229], v[52:55]
	v_mfma_f32_16x16x128_f8f6f4 v[40:43], v[16:23], v[230:237], v[40:43]
	v_mfma_f32_16x16x128_f8f6f4 v[32:35], v[24:31], v[230:237], v[32:35]
	s_setprio 0
	s_barrier
	s_andn2_b64 vcc, exec, s[38:39]
	s_mov_b64 s[40:41], -1
	s_mov_b64 s[38:39], 0
	s_mov_b64 s[42:43], 0x100
	s_cbranch_vccz .LBB0_1790
	s_nop 15
	s_nop 7
	s_and_b64 vcc, exec, s[12:13]
	s_cbranch_vccz .LBB0_1793
	s_barrier

.LBB0_2052:
	ds_read_b128 v[20:23], v188
	ds_read_b128 v[24:27], v189
	ds_read_b128 v[16:19], v183
	ds_read_b128 v[0:3], v184
	ds_read_b128 v[28:31], v190
	ds_read_b128 v[4:7], v191
	ds_read_b128 v[8:11], v192
	ds_read_b128 v[12:15], v193
	s_add_u32 s26, s24, 0xfffe0080
	s_addc_u32 s27, s25, -1
	s_cmp_eq_u32 s50, 4
	s_cselect_b32 s29, s9, s27
	s_cselect_b32 s28, s46, s26
	s_cselect_b32 s27, s7, s49
	s_cselect_b32 s26, s47, s48
	v_lshl_add_u64 v[228:229], s[24:25], 0, v[168:169]
	s_add_i32 m0, s17, 0xc000
	ds_read_b128 v[174:177], v200
	ds_read_b128 v[178:181], v200 offset:1024
	ds_read_b128 v[204:207], v200 offset:2048
	ds_read_b128 v[208:211], v200 offset:3072
	ds_read_b128 v[212:215], v200 offset:4096
	ds_read_b128 v[216:219], v200 offset:5120
	ds_read_b128 v[220:223], v200 offset:6144
	ds_read_b128 v[224:227], v200 offset:7168
	global_load_lds_dwordx4 v[228:229], off
	v_lshl_add_u64 v[228:229], s[24:25], 0, v[170:171]
	s_add_i32 m0, s17, 0xe000
	s_nop 0
	global_load_lds_dwordx4 v[228:229], off
	s_waitcnt vmcnt(8)
	s_waitcnt lgkmcnt(0)
	s_barrier
	s_setprio 1
	s_waitcnt lgkmcnt(0)
	v_mfma_f32_16x16x128_f8f6f4 v[156:159], v[16:23], v[174:181], v[156:159]
	v_mfma_f32_16x16x128_f8f6f4 v[152:155], v[24:31], v[174:181], v[152:155]
	v_mfma_f32_16x16x128_f8f6f4 v[144:147], v[16:23], v[204:211], v[144:147]
	v_mfma_f32_16x16x128_f8f6f4 v[136:139], v[24:31], v[204:211], v[136:139]
	v_mfma_f32_16x16x128_f8f6f4 v[128:131], v[16:23], v[212:219], v[128:131]
	v_mfma_f32_16x16x128_f8f6f4 v[120:123], v[24:31], v[212:219], v[120:123]
	v_mfma_f32_16x16x128_f8f6f4 v[112:115], v[16:23], v[220:227], v[112:115]
	v_mfma_f32_16x16x128_f8f6f4 v[104:107], v[24:31], v[220:227], v[104:107]
	s_setprio 0
	s_setprio 1
	v_mfma_f32_16x16x128_f8f6f4 v[148:151], v[0:7], v[174:181], v[148:151]
	v_mfma_f32_16x16x128_f8f6f4 v[140:143], v[8:15], v[174:181], v[140:143]
	v_mfma_f32_16x16x128_f8f6f4 v[132:135], v[0:7], v[204:211], v[132:135]
	v_mfma_f32_16x16x128_f8f6f4 v[124:127], v[8:15], v[204:211], v[124:127]
	v_mfma_f32_16x16x128_f8f6f4 v[116:119], v[0:7], v[212:219], v[116:119]
	v_mfma_f32_16x16x128_f8f6f4 v[108:111], v[8:15], v[212:219], v[108:111]
	v_mfma_f32_16x16x128_f8f6f4 v[92:95], v[0:7], v[220:227], v[92:95]
	v_mfma_f32_16x16x128_f8f6f4 v[88:91], v[8:15], v[220:227], v[88:91]
	s_setprio 0
	s_barrier
	s_mov_b32 m0, s22
	v_lshl_add_u64 v[174:175], s[26:27], 0, v[162:163]
	s_add_u32 s52, s26, 0x20000
	ds_read_b128 v[204:207], v200 offset:16384
	ds_read_b128 v[208:211], v200 offset:17408
	ds_read_b128 v[212:215], v200 offset:18432
	ds_read_b128 v[216:219], v200 offset:19456
	ds_read_b128 v[220:223], v200 offset:20480
	ds_read_b128 v[224:227], v200 offset:21504
	ds_read_b128 v[228:231], v200 offset:22528
	ds_read_b128 v[232:235], v200 offset:23552
	global_load_lds_dwordx4 v[174:175], off
	v_lshl_add_u64 v[176:177], s[26:27], 0, v[160:161]
	s_mov_b32 m0, s23
	s_addc_u32 s53, s27, 0
	global_load_lds_dwordx4 v[176:177], off
	v_lshl_add_u64 v[178:179], s[52:53], 0, v[162:163]
	s_mov_b32 m0, s30
	v_lshl_add_u64 v[180:181], s[28:29], 0, v[166:167]
	global_load_lds_dwordx4 v[178:179], off
	v_lshl_add_u64 v[178:179], s[52:53], 0, v[160:161]
	s_mov_b32 m0, s31
	s_nop 0
	global_load_lds_dwordx4 v[178:179], off
	s_waitcnt vmcnt(6)
	s_waitcnt lgkmcnt(0)
	s_barrier
	s_setprio 1
	s_waitcnt lgkmcnt(0)
	v_mfma_f32_16x16x128_f8f6f4 v[76:79], v[16:23], v[204:211], v[76:79]
	v_mfma_f32_16x16x128_f8f6f4 v[72:75], v[24:31], v[204:211], v[72:75]
	v_mfma_f32_16x16x128_f8f6f4 v[52:55], v[16:23], v[212:219], v[52:55]
	v_mfma_f32_16x16x128_f8f6f4 v[48:51], v[24:31], v[212:219], v[48:51]
	v_mfma_f32_16x16x128_f8f6f4 v[60:63], v[16:23], v[220:227], v[60:63]
	v_mfma_f32_16x16x128_f8f6f4 v[56:59], v[24:31], v[220:227], v[56:59]
	v_mfma_f32_16x16x128_f8f6f4 v[36:39], v[16:23], v[228:235], v[36:39]
	v_mfma_f32_16x16x128_f8f6f4 v[32:35], v[24:31], v[228:235], v[32:35]
	s_setprio 0
	v_lshl_add_u64 v[178:179], s[28:29], 0, v[164:165]
	s_mov_b32 m0, s17
	s_nop 0
	global_load_lds_dwordx4 v[178:179], off
	s_mov_b32 m0, s33
	s_nop 0
	global_load_lds_dwordx4 v[180:181], off
	s_setprio 1
	v_mfma_f32_16x16x128_f8f6f4 v[100:103], v[0:7], v[204:211], v[100:103]
	v_mfma_f32_16x16x128_f8f6f4 v[96:99], v[8:15], v[204:211], v[96:99]
	v_mfma_f32_16x16x128_f8f6f4 v[84:87], v[0:7], v[212:219], v[84:87]
	v_mfma_f32_16x16x128_f8f6f4 v[80:83], v[8:15], v[212:219], v[80:83]
	v_mfma_f32_16x16x128_f8f6f4 v[68:71], v[0:7], v[220:227], v[68:71]
	v_mfma_f32_16x16x128_f8f6f4 v[64:67], v[8:15], v[220:227], v[64:67]
	v_mfma_f32_16x16x128_f8f6f4 v[44:47], v[0:7], v[228:235], v[44:47]
	v_mfma_f32_16x16x128_f8f6f4 v[40:43], v[8:15], v[228:235], v[40:43]
	s_setprio 0
	s_barrier
	ds_read_b128 v[4:7], v194
	ds_read_b128 v[8:11], v195
	ds_read_b128 v[0:3], v185
	ds_read_b128 v[16:19], v186
	ds_read_b128 v[12:15], v196
	ds_read_b128 v[20:23], v197
	ds_read_b128 v[24:27], v198
	ds_read_b128 v[28:31], v199
	s_add_u32 s28, s28, 0x20000
	s_addc_u32 s29, s29, 0
	s_mov_b32 m0, s34
	v_lshl_add_u64 v[236:237], s[28:29], 0, v[164:165]
	ds_read_b128 v[204:207], v200 offset:32768
	ds_read_b128 v[208:211], v200 offset:33792
	ds_read_b128 v[212:215], v200 offset:34816
	ds_read_b128 v[216:219], v200 offset:35840
	ds_read_b128 v[220:223], v200 offset:36864
	ds_read_b128 v[224:227], v200 offset:37888
	ds_read_b128 v[228:231], v200 offset:38912
	ds_read_b128 v[232:235], v200 offset:39936
	global_load_lds_dwordx4 v[236:237], off
	v_lshl_add_u64 v[236:237], s[28:29], 0, v[166:167]
	s_mov_b32 m0, s35
	s_nop 0
	global_load_lds_dwordx4 v[236:237], off
	s_waitcnt vmcnt(8)
	s_waitcnt lgkmcnt(0)
	s_barrier
	s_setprio 1
	s_waitcnt lgkmcnt(0)
	v_mfma_f32_16x16x128_f8f6f4 v[156:159], v[0:7], v[204:211], v[156:159]
	v_mfma_f32_16x16x128_f8f6f4 v[152:155], v[8:15], v[204:211], v[152:155]
	v_mfma_f32_16x16x128_f8f6f4 v[144:147], v[0:7], v[212:219], v[144:147]
	v_mfma_f32_16x16x128_f8f6f4 v[136:139], v[8:15], v[212:219], v[136:139]
	v_mfma_f32_16x16x128_f8f6f4 v[128:131], v[0:7], v[220:227], v[128:131]
	v_mfma_f32_16x16x128_f8f6f4 v[120:123], v[8:15], v[220:227], v[120:123]
	v_mfma_f32_16x16x128_f8f6f4 v[112:115], v[0:7], v[228:235], v[112:115]
	v_mfma_f32_16x16x128_f8f6f4 v[104:107], v[8:15], v[228:235], v[104:107]
	s_setprio 0
	s_setprio 1
	v_mfma_f32_16x16x128_f8f6f4 v[148:151], v[16:23], v[204:211], v[148:151]
	v_mfma_f32_16x16x128_f8f6f4 v[140:143], v[24:31], v[204:211], v[140:143]
	v_mfma_f32_16x16x128_f8f6f4 v[132:135], v[16:23], v[212:219], v[132:135]
	v_mfma_f32_16x16x128_f8f6f4 v[124:127], v[24:31], v[212:219], v[124:127]
	v_mfma_f32_16x16x128_f8f6f4 v[116:119], v[16:23], v[220:227], v[116:119]
	v_mfma_f32_16x16x128_f8f6f4 v[108:111], v[24:31], v[220:227], v[108:111]
	v_mfma_f32_16x16x128_f8f6f4 v[92:95], v[16:23], v[228:235], v[92:95]
	v_mfma_f32_16x16x128_f8f6f4 v[88:91], v[24:31], v[228:235], v[88:91]
	s_setprio 0
	s_barrier
	s_mov_b32 m0, s37
	v_lshl_add_u64 v[174:175], v[174:175], 0, s[2:3]
	s_add_u32 s26, s26, 0x20080
	ds_read_b128 v[204:207], v200 offset:49152
	ds_read_b128 v[208:211], v200 offset:50176
	ds_read_b128 v[212:215], v200 offset:51200
	ds_read_b128 v[216:219], v200 offset:52224
	ds_read_b128 v[220:223], v200 offset:53248
	ds_read_b128 v[224:227], v200 offset:54272
	ds_read_b128 v[228:231], v200 offset:55296
	ds_read_b128 v[232:235], v200 offset:56320
	global_load_lds_dwordx4 v[174:175], off
	v_lshl_add_u64 v[174:175], v[176:177], 0, s[2:3]
	s_mov_b32 m0, s38
	s_addc_u32 s27, s27, 0
	global_load_lds_dwordx4 v[174:175], off
	v_lshl_add_u64 v[174:175], s[26:27], 0, v[162:163]
	s_mov_b32 m0, s41
	s_nop 0
	global_load_lds_dwordx4 v[174:175], off
	v_lshl_add_u64 v[174:175], s[26:27], 0, v[160:161]
	s_mov_b32 m0, s42
	s_nop 0
	global_load_lds_dwordx4 v[174:175], off
	s_waitcnt vmcnt(6)
	s_waitcnt lgkmcnt(0)
	s_barrier
	s_setprio 1
	s_waitcnt lgkmcnt(0)
	v_mfma_f32_16x16x128_f8f6f4 v[76:79], v[0:7], v[204:211], v[76:79]
	v_mfma_f32_16x16x128_f8f6f4 v[72:75], v[8:15], v[204:211], v[72:75]
	v_mfma_f32_16x16x128_f8f6f4 v[52:55], v[0:7], v[212:219], v[52:55]
	v_mfma_f32_16x16x128_f8f6f4 v[48:51], v[8:15], v[212:219], v[48:51]
	v_mfma_f32_16x16x128_f8f6f4 v[60:63], v[0:7], v[220:227], v[60:63]
	v_mfma_f32_16x16x128_f8f6f4 v[56:59], v[8:15], v[220:227], v[56:59]
	v_mfma_f32_16x16x128_f8f6f4 v[36:39], v[0:7], v[228:235], v[36:39]
	v_mfma_f32_16x16x128_f8f6f4 v[32:35], v[8:15], v[228:235], v[32:35]
	s_setprio 0
	v_lshl_add_u64 v[174:175], v[178:179], 0, s[2:3]
	s_mov_b32 m0, s39
	s_nop 0
	global_load_lds_dwordx4 v[174:175], off
	v_lshl_add_u64 v[174:175], v[180:181], 0, s[2:3]
	s_mov_b32 m0, s40
	s_nop 0
	global_load_lds_dwordx4 v[174:175], off
	s_setprio 1
	v_mfma_f32_16x16x128_f8f6f4 v[100:103], v[16:23], v[204:211], v[100:103]
	v_mfma_f32_16x16x128_f8f6f4 v[96:99], v[24:31], v[204:211], v[96:99]
	v_mfma_f32_16x16x128_f8f6f4 v[84:87], v[16:23], v[212:219], v[84:87]
	v_mfma_f32_16x16x128_f8f6f4 v[80:83], v[24:31], v[212:219], v[80:83]
	v_mfma_f32_16x16x128_f8f6f4 v[68:71], v[16:23], v[220:227], v[68:71]
	v_mfma_f32_16x16x128_f8f6f4 v[64:67], v[24:31], v[220:227], v[64:67]
	v_mfma_f32_16x16x128_f8f6f4 v[44:47], v[16:23], v[228:235], v[44:47]
	v_mfma_f32_16x16x128_f8f6f4 v[40:43], v[24:31], v[228:235], v[40:43]
	s_setprio 0
	s_barrier
	s_add_i32 s50, s50, 2
	s_add_u32 s24, s24, 0x100
	s_addc_u32 s25, s25, 0
	s_add_u32 s48, s48, 0x100
	s_addc_u32 s49, s49, 0
	s_cmp_gt_u32 s50, 5
	s_cbranch_scc0 .LBB0_2052
	s_nop 15
	s_nop 7
	s_and_b64 vcc, exec, s[4:5]
	s_cbranch_vccz .LBB0_2055
	s_barrier

.LBB0_2380:
	ds_read_b128 v[20:23], v217
	ds_read_b128 v[24:27], v218
	ds_read_b128 v[16:19], v213
	ds_read_b128 v[0:3], v214
	ds_read_b128 v[28:31], v219
	ds_read_b128 v[4:7], v220
	ds_read_b128 v[8:11], v221
	ds_read_b128 v[12:15], v222
	s_add_u32 s6, s2, 0xfffe0080
	s_addc_u32 s7, s3, -1
	s_cmp_eq_u32 s49, 4
	s_cselect_b32 s47, s1, s7
	s_cselect_b32 s46, s5, s6
	s_cselect_b32 s7, s33, s48
	s_cselect_b32 s6, s37, s39
	v_lshl_add_u64 v[210:211], s[2:3], 0, v[194:195]
	s_add_i32 m0, s55, 0xc000
	ds_read_b128 v[160:163], v229
	ds_read_b128 v[164:167], v229 offset:1024
	ds_read_b128 v[168:171], v229 offset:2048
	ds_read_b128 v[172:175], v229 offset:3072
	ds_read_b128 v[176:179], v229 offset:4096
	ds_read_b128 v[180:183], v229 offset:5120
	ds_read_b128 v[202:205], v229 offset:6144
	ds_read_b128 v[206:209], v229 offset:7168
	global_load_lds_dwordx4 v[210:211], off
	v_lshl_add_u64 v[210:211], s[2:3], 0, v[196:197]
	s_add_i32 m0, s55, 0xe000
	s_nop 0
	global_load_lds_dwordx4 v[210:211], off
	s_waitcnt vmcnt(8)
	s_waitcnt lgkmcnt(0)
	s_barrier
	s_setprio 1
	s_waitcnt lgkmcnt(0)
	v_mfma_f32_16x16x128_f8f6f4 v[156:159], v[16:23], v[160:167], v[156:159]
	v_mfma_f32_16x16x128_f8f6f4 v[152:155], v[24:31], v[160:167], v[152:155]
	v_mfma_f32_16x16x128_f8f6f4 v[140:143], v[16:23], v[168:175], v[140:143]
	v_mfma_f32_16x16x128_f8f6f4 v[136:139], v[24:31], v[168:175], v[136:139]
	v_mfma_f32_16x16x128_f8f6f4 v[124:127], v[16:23], v[176:183], v[124:127]
	v_mfma_f32_16x16x128_f8f6f4 v[120:123], v[24:31], v[176:183], v[120:123]
	v_mfma_f32_16x16x128_f8f6f4 v[108:111], v[16:23], v[202:209], v[108:111]
	v_mfma_f32_16x16x128_f8f6f4 v[104:107], v[24:31], v[202:209], v[104:107]
	s_setprio 0
	s_setprio 1
	v_mfma_f32_16x16x128_f8f6f4 v[148:151], v[0:7], v[160:167], v[148:151]
	v_mfma_f32_16x16x128_f8f6f4 v[144:147], v[8:15], v[160:167], v[144:147]
	v_mfma_f32_16x16x128_f8f6f4 v[132:135], v[0:7], v[168:175], v[132:135]
	v_mfma_f32_16x16x128_f8f6f4 v[128:131], v[8:15], v[168:175], v[128:131]
	v_mfma_f32_16x16x128_f8f6f4 v[116:119], v[0:7], v[176:183], v[116:119]
	v_mfma_f32_16x16x128_f8f6f4 v[112:115], v[8:15], v[176:183], v[112:115]
	v_mfma_f32_16x16x128_f8f6f4 v[100:103], v[0:7], v[202:209], v[100:103]
	v_mfma_f32_16x16x128_f8f6f4 v[96:99], v[8:15], v[202:209], v[96:99]
	s_setprio 0
	s_barrier
	s_mov_b32 m0, s56
	v_lshl_add_u64 v[160:161], s[6:7], 0, v[184:185]
	s_add_u32 s50, s6, 0x20000
	ds_read_b128 v[168:171], v229 offset:16384
	ds_read_b128 v[172:175], v229 offset:17408
	ds_read_b128 v[176:179], v229 offset:18432
	ds_read_b128 v[180:183], v229 offset:19456
	ds_read_b128 v[202:205], v229 offset:20480
	ds_read_b128 v[206:209], v229 offset:21504
	ds_read_b128 v[236:239], v229 offset:22528
	ds_read_b128 v[240:243], v229 offset:23552
	global_load_lds_dwordx4 v[160:161], off
	v_lshl_add_u64 v[162:163], s[6:7], 0, v[186:187]
	s_mov_b32 m0, s57
	s_addc_u32 s51, s7, 0
	global_load_lds_dwordx4 v[162:163], off
	v_lshl_add_u64 v[164:165], s[50:51], 0, v[184:185]
	s_mov_b32 m0, s58
	v_lshl_add_u64 v[166:167], s[46:47], 0, v[190:191]
	global_load_lds_dwordx4 v[164:165], off
	v_lshl_add_u64 v[164:165], s[50:51], 0, v[186:187]
	s_mov_b32 m0, s59
	s_nop 0
	global_load_lds_dwordx4 v[164:165], off
	s_waitcnt vmcnt(6)
	s_waitcnt lgkmcnt(0)
	s_barrier
	s_setprio 1
	s_waitcnt lgkmcnt(0)
	v_mfma_f32_16x16x128_f8f6f4 v[84:87], v[16:23], v[168:175], v[84:87]
	v_mfma_f32_16x16x128_f8f6f4 v[80:83], v[24:31], v[168:175], v[80:83]
	v_mfma_f32_16x16x128_f8f6f4 v[68:71], v[16:23], v[176:183], v[68:71]
	v_mfma_f32_16x16x128_f8f6f4 v[64:67], v[24:31], v[176:183], v[64:67]
	v_mfma_f32_16x16x128_f8f6f4 v[56:59], v[16:23], v[202:209], v[56:59]
	v_mfma_f32_16x16x128_f8f6f4 v[48:51], v[24:31], v[202:209], v[48:51]
	v_mfma_f32_16x16x128_f8f6f4 v[40:43], v[16:23], v[236:243], v[40:43]
	v_mfma_f32_16x16x128_f8f6f4 v[32:35], v[24:31], v[236:243], v[32:35]
	s_setprio 0
	v_lshl_add_u64 v[164:165], s[46:47], 0, v[188:189]
	s_mov_b32 m0, s55
	s_nop 0
	global_load_lds_dwordx4 v[164:165], off
	s_mov_b32 m0, s60
	s_nop 0
	global_load_lds_dwordx4 v[166:167], off
	s_setprio 1
	v_mfma_f32_16x16x128_f8f6f4 v[92:95], v[0:7], v[168:175], v[92:95]
	v_mfma_f32_16x16x128_f8f6f4 v[88:91], v[8:15], v[168:175], v[88:91]
	v_mfma_f32_16x16x128_f8f6f4 v[76:79], v[0:7], v[176:183], v[76:79]
	v_mfma_f32_16x16x128_f8f6f4 v[72:75], v[8:15], v[176:183], v[72:75]
	v_mfma_f32_16x16x128_f8f6f4 v[60:63], v[0:7], v[202:209], v[60:63]
	v_mfma_f32_16x16x128_f8f6f4 v[52:55], v[8:15], v[202:209], v[52:55]
	v_mfma_f32_16x16x128_f8f6f4 v[44:47], v[0:7], v[236:243], v[44:47]
	v_mfma_f32_16x16x128_f8f6f4 v[36:39], v[8:15], v[236:243], v[36:39]
	s_setprio 0
	s_barrier
	ds_read_b128 v[4:7], v223
	ds_read_b128 v[8:11], v224
	ds_read_b128 v[0:3], v215
	ds_read_b128 v[16:19], v216
	ds_read_b128 v[12:15], v225
	ds_read_b128 v[20:23], v226
	ds_read_b128 v[24:27], v227
	ds_read_b128 v[28:31], v228
	s_add_u32 s46, s46, 0x20000
	s_addc_u32 s47, s47, 0
	s_mov_b32 m0, s61
	v_lshl_add_u64 v[210:211], s[46:47], 0, v[188:189]
	ds_read_b128 v[168:171], v229 offset:32768
	ds_read_b128 v[172:175], v229 offset:33792
	ds_read_b128 v[176:179], v229 offset:34816
	ds_read_b128 v[180:183], v229 offset:35840
	ds_read_b128 v[202:205], v229 offset:36864
	ds_read_b128 v[206:209], v229 offset:37888
	ds_read_b128 v[236:239], v229 offset:38912
	ds_read_b128 v[240:243], v229 offset:39936
	global_load_lds_dwordx4 v[210:211], off
	v_lshl_add_u64 v[210:211], s[46:47], 0, v[190:191]
	s_mov_b32 m0, s62
	s_nop 0
	global_load_lds_dwordx4 v[210:211], off
	s_waitcnt vmcnt(8)
	s_waitcnt lgkmcnt(0)
	s_barrier
	s_setprio 1
	s_waitcnt lgkmcnt(0)
	v_mfma_f32_16x16x128_f8f6f4 v[156:159], v[0:7], v[168:175], v[156:159]
	v_mfma_f32_16x16x128_f8f6f4 v[152:155], v[8:15], v[168:175], v[152:155]
	v_mfma_f32_16x16x128_f8f6f4 v[140:143], v[0:7], v[176:183], v[140:143]
	v_mfma_f32_16x16x128_f8f6f4 v[136:139], v[8:15], v[176:183], v[136:139]
	v_mfma_f32_16x16x128_f8f6f4 v[124:127], v[0:7], v[202:209], v[124:127]
	v_mfma_f32_16x16x128_f8f6f4 v[120:123], v[8:15], v[202:209], v[120:123]
	v_mfma_f32_16x16x128_f8f6f4 v[108:111], v[0:7], v[236:243], v[108:111]
	v_mfma_f32_16x16x128_f8f6f4 v[104:107], v[8:15], v[236:243], v[104:107]
	s_setprio 0
	s_setprio 1
	v_mfma_f32_16x16x128_f8f6f4 v[148:151], v[16:23], v[168:175], v[148:151]
	v_mfma_f32_16x16x128_f8f6f4 v[144:147], v[24:31], v[168:175], v[144:147]
	v_mfma_f32_16x16x128_f8f6f4 v[132:135], v[16:23], v[176:183], v[132:135]
	v_mfma_f32_16x16x128_f8f6f4 v[128:131], v[24:31], v[176:183], v[128:131]
	v_mfma_f32_16x16x128_f8f6f4 v[116:119], v[16:23], v[202:209], v[116:119]
	v_mfma_f32_16x16x128_f8f6f4 v[112:115], v[24:31], v[202:209], v[112:115]
	v_mfma_f32_16x16x128_f8f6f4 v[100:103], v[16:23], v[236:243], v[100:103]
	v_mfma_f32_16x16x128_f8f6f4 v[96:99], v[24:31], v[236:243], v[96:99]
	s_setprio 0
	s_barrier
	s_mov_b32 m0, s67
	v_lshl_add_u64 v[160:161], v[160:161], 0, s[24:25]
	s_add_u32 s6, s6, 0x20080
	ds_read_b128 v[168:171], v229 offset:49152
	ds_read_b128 v[172:175], v229 offset:50176
	ds_read_b128 v[176:179], v229 offset:51200
	ds_read_b128 v[180:183], v229 offset:52224
	ds_read_b128 v[202:205], v229 offset:53248
	ds_read_b128 v[206:209], v229 offset:54272
	ds_read_b128 v[236:239], v229 offset:55296
	ds_read_b128 v[240:243], v229 offset:56320
	global_load_lds_dwordx4 v[160:161], off
	v_lshl_add_u64 v[160:161], v[162:163], 0, s[24:25]
	s_mov_b32 m0, s68
	s_addc_u32 s7, s7, 0
	global_load_lds_dwordx4 v[160:161], off
	v_lshl_add_u64 v[160:161], s[6:7], 0, v[184:185]
	s_mov_b32 m0, s71
	s_nop 0
	global_load_lds_dwordx4 v[160:161], off
	v_lshl_add_u64 v[160:161], s[6:7], 0, v[186:187]
	s_mov_b32 m0, s78
	s_nop 0
	global_load_lds_dwordx4 v[160:161], off
	s_waitcnt vmcnt(6)
	s_waitcnt lgkmcnt(0)
	s_barrier
	s_setprio 1
	s_waitcnt lgkmcnt(0)
	v_mfma_f32_16x16x128_f8f6f4 v[84:87], v[0:7], v[168:175], v[84:87]
	v_mfma_f32_16x16x128_f8f6f4 v[80:83], v[8:15], v[168:175], v[80:83]
	v_mfma_f32_16x16x128_f8f6f4 v[68:71], v[0:7], v[176:183], v[68:71]
	v_mfma_f32_16x16x128_f8f6f4 v[64:67], v[8:15], v[176:183], v[64:67]
	v_mfma_f32_16x16x128_f8f6f4 v[56:59], v[0:7], v[202:209], v[56:59]
	v_mfma_f32_16x16x128_f8f6f4 v[48:51], v[8:15], v[202:209], v[48:51]
	v_mfma_f32_16x16x128_f8f6f4 v[40:43], v[0:7], v[236:243], v[40:43]
	v_mfma_f32_16x16x128_f8f6f4 v[32:35], v[8:15], v[236:243], v[32:35]
	s_setprio 0
	v_lshl_add_u64 v[160:161], v[164:165], 0, s[24:25]
	s_mov_b32 m0, s69
	s_nop 0
	global_load_lds_dwordx4 v[160:161], off
	v_lshl_add_u64 v[160:161], v[166:167], 0, s[24:25]
	s_mov_b32 m0, s70
	s_nop 0
	global_load_lds_dwordx4 v[160:161], off
	s_setprio 1
	v_mfma_f32_16x16x128_f8f6f4 v[92:95], v[16:23], v[168:175], v[92:95]
	v_mfma_f32_16x16x128_f8f6f4 v[88:91], v[24:31], v[168:175], v[88:91]
	v_mfma_f32_16x16x128_f8f6f4 v[76:79], v[16:23], v[176:183], v[76:79]
	v_mfma_f32_16x16x128_f8f6f4 v[72:75], v[24:31], v[176:183], v[72:75]
	v_mfma_f32_16x16x128_f8f6f4 v[60:63], v[16:23], v[202:209], v[60:63]
	v_mfma_f32_16x16x128_f8f6f4 v[52:55], v[24:31], v[202:209], v[52:55]
	v_mfma_f32_16x16x128_f8f6f4 v[44:47], v[16:23], v[236:243], v[44:47]
	v_mfma_f32_16x16x128_f8f6f4 v[36:39], v[24:31], v[236:243], v[36:39]
	s_setprio 0
	s_barrier
	s_add_i32 s49, s49, 2
	s_add_u32 s2, s2, 0x100
	s_addc_u32 s3, s3, 0
	s_add_u32 s39, s39, 0x100
	s_addc_u32 s48, s48, 0
	s_cmp_gt_u32 s49, 5
	s_cbranch_scc0 .LBB0_2380
	s_nop 15
	s_nop 7
	s_and_b64 vcc, exec, s[26:27]
	s_cbranch_vccz .LBB0_2383
	s_barrier

.LBB0_2571:
	s_add_u32 s36, s90, s4
	s_addc_u32 s37, s91, s5
	s_add_u32 s73, s36, 0x21c00100
	s_addc_u32 s74, s37, 0
	s_cmpk_eq_i32 s4, 0x300
	v_lshl_add_u64 v[0:1], v[180:181], 0, s[4:5]
	s_cselect_b64 vcc, -1, 0
	v_cndmask_b32_e32 v183, v1, v167, vcc
	v_cndmask_b32_e32 v182, v0, v220, vcc
	ds_read_b128 v[8:11], v194
	ds_read_b128 v[12:15], v198
	ds_read_b128 v[24:27], v199
	ds_read_b128 v[28:31], v200
	ds_read_b128 v[0:3], v195
	ds_read_b128 v[4:7], v201
	ds_read_b128 v[16:19], v202
	ds_read_b128 v[20:23], v203
	s_and_b64 s[36:37], vcc, exec
	s_cselect_b32 s37, s9, s74
	s_cselect_b32 s36, s8, s73
	v_cndmask_b32_e32 v160, v219, v215, vcc
	v_cndmask_b32_e32 v184, v170, v216, vcc
	v_cndmask_b32_e32 v175, v172, v217, vcc
	v_cndmask_b32_e32 v173, v174, v218, vcc
	v_lshl_add_u64 v[186:187], v[178:179], 0, s[4:5]
	s_add_i32 m0, s0, 0xc000
	ds_read_b128 v[222:225], v212
	ds_read_b128 v[226:229], v212 offset:1024
	ds_read_b128 v[230:233], v212 offset:2048
	ds_read_b128 v[234:237], v212 offset:3072
	ds_read_b128 v[238:241], v212 offset:4096
	ds_read_b128 v[242:245], v212 offset:5120
	ds_read_b128 v[246:249], v212 offset:6144
	ds_read_b128 v[250:253], v212 offset:7168
	global_load_lds_dwordx4 v[186:187], off
	v_lshl_add_u64 v[186:187], v[176:177], 0, s[4:5]
	s_add_i32 m0, s0, 0xe000
	s_nop 0
	global_load_lds_dwordx4 v[186:187], off
	s_waitcnt vmcnt(8)
	s_waitcnt lgkmcnt(0)
	s_barrier
	s_setprio 1
	s_waitcnt lgkmcnt(0)
	v_mfma_f32_16x16x128_f8f6f4 v[156:159], v[8:15], v[222:229], v[156:159]
	v_mfma_f32_16x16x128_f8f6f4 v[152:155], v[24:31], v[222:229], v[152:155]
	v_mfma_f32_16x16x128_f8f6f4 v[140:143], v[8:15], v[230:237], v[140:143]
	v_mfma_f32_16x16x128_f8f6f4 v[136:139], v[24:31], v[230:237], v[136:139]
	v_mfma_f32_16x16x128_f8f6f4 v[124:127], v[8:15], v[238:245], v[124:127]
	v_mfma_f32_16x16x128_f8f6f4 v[120:123], v[24:31], v[238:245], v[120:123]
	v_mfma_f32_16x16x128_f8f6f4 v[108:111], v[8:15], v[246:253], v[108:111]
	v_mfma_f32_16x16x128_f8f6f4 v[104:107], v[24:31], v[246:253], v[104:107]
	s_setprio 0
	s_setprio 1
	v_mfma_f32_16x16x128_f8f6f4 v[148:151], v[0:7], v[222:229], v[148:151]
	v_mfma_f32_16x16x128_f8f6f4 v[144:147], v[16:23], v[222:229], v[144:147]
	v_mfma_f32_16x16x128_f8f6f4 v[132:135], v[0:7], v[230:237], v[132:135]
	v_mfma_f32_16x16x128_f8f6f4 v[128:131], v[16:23], v[230:237], v[128:131]
	v_mfma_f32_16x16x128_f8f6f4 v[116:119], v[0:7], v[238:245], v[116:119]
	v_mfma_f32_16x16x128_f8f6f4 v[112:115], v[16:23], v[238:245], v[112:115]
	v_mfma_f32_16x16x128_f8f6f4 v[100:103], v[0:7], v[246:253], v[100:103]
	v_mfma_f32_16x16x128_f8f6f4 v[96:99], v[16:23], v[246:253], v[96:99]
	s_setprio 0
	s_barrier
	s_mov_b32 m0, s40
	v_lshl_add_u64 v[186:187], v[182:183], 0, v[164:165]
	ds_read_b128 v[222:225], v212 offset:16384
	ds_read_b128 v[226:229], v212 offset:17408
	ds_read_b128 v[230:233], v212 offset:18432
	ds_read_b128 v[234:237], v212 offset:19456
	ds_read_b128 v[238:241], v212 offset:20480
	ds_read_b128 v[242:245], v212 offset:21504
	ds_read_b128 v[246:249], v212 offset:22528
	ds_read_b128 v[250:253], v212 offset:23552
	global_load_lds_dwordx4 v[186:187], off
	v_lshl_add_u64 v[188:189], v[182:183], 0, v[162:163]
	s_mov_b32 m0, s41
	v_lshl_add_u64 v[190:191], v[182:183], 0, s[12:13]
	global_load_lds_dwordx4 v[188:189], off
	v_lshl_add_u64 v[192:193], v[190:191], 0, v[164:165]
	s_mov_b32 m0, s42
	v_lshl_add_u64 v[190:191], v[190:191], 0, v[162:163]
	global_load_lds_dwordx4 v[192:193], off
	s_mov_b32 m0, s43
	v_mov_b32_e32 v185, v161
	global_load_lds_dwordx4 v[190:191], off
	s_mov_b32 m0, s0
	v_lshl_add_u64 v[190:191], s[36:37], 0, v[160:161]
	global_load_lds_dwordx4 v160, s[36:37]
	s_mov_b32 m0, s44
	s_nop 0
	global_load_lds_dwordx4 v184, s[36:37]
	s_waitcnt vmcnt(8)
	s_waitcnt lgkmcnt(0)
	v_lshl_add_u64 v[184:185], s[36:37], 0, v[184:185]
	s_barrier
	s_setprio 1
	s_waitcnt lgkmcnt(0)
	v_mfma_f32_16x16x128_f8f6f4 v[84:87], v[8:15], v[222:229], v[84:87]
	v_mfma_f32_16x16x128_f8f6f4 v[80:83], v[24:31], v[222:229], v[80:83]
	v_mfma_f32_16x16x128_f8f6f4 v[68:71], v[8:15], v[230:237], v[68:71]
	v_mfma_f32_16x16x128_f8f6f4 v[64:67], v[24:31], v[230:237], v[64:67]
	v_mfma_f32_16x16x128_f8f6f4 v[52:55], v[8:15], v[238:245], v[52:55]
	v_mfma_f32_16x16x128_f8f6f4 v[48:51], v[24:31], v[238:245], v[48:51]
	v_mfma_f32_16x16x128_f8f6f4 v[36:39], v[8:15], v[246:253], v[36:39]
	v_mfma_f32_16x16x128_f8f6f4 v[32:35], v[24:31], v[246:253], v[32:35]
	s_setprio 0
	s_setprio 1
	v_mfma_f32_16x16x128_f8f6f4 v[92:95], v[0:7], v[222:229], v[92:95]
	v_mfma_f32_16x16x128_f8f6f4 v[88:91], v[16:23], v[222:229], v[88:91]
	v_mfma_f32_16x16x128_f8f6f4 v[76:79], v[0:7], v[230:237], v[76:79]
	v_mfma_f32_16x16x128_f8f6f4 v[72:75], v[16:23], v[230:237], v[72:75]
	v_mfma_f32_16x16x128_f8f6f4 v[60:63], v[0:7], v[238:245], v[60:63]
	v_mfma_f32_16x16x128_f8f6f4 v[56:59], v[16:23], v[238:245], v[56:59]
	v_mfma_f32_16x16x128_f8f6f4 v[44:47], v[0:7], v[246:253], v[44:47]
	v_mfma_f32_16x16x128_f8f6f4 v[40:43], v[16:23], v[246:253], v[40:43]
	s_setprio 0
	s_barrier
	ds_read_b128 v[4:7], v204
	ds_read_b128 v[8:11], v205
	ds_read_b128 v[0:3], v196
	ds_read_b128 v[16:19], v197
	ds_read_b128 v[12:15], v206
	ds_read_b128 v[20:23], v207
	ds_read_b128 v[24:27], v208
	ds_read_b128 v[28:31], v209
	s_mov_b32 m0, s45
	ds_read_b128 v[222:225], v212 offset:32768
	ds_read_b128 v[226:229], v212 offset:33792
	ds_read_b128 v[230:233], v212 offset:34816
	ds_read_b128 v[234:237], v212 offset:35840
	ds_read_b128 v[238:241], v212 offset:36864
	ds_read_b128 v[242:245], v212 offset:37888
	ds_read_b128 v[246:249], v212 offset:38912
	ds_read_b128 v[250:253], v212 offset:39936
	global_load_lds_dwordx4 v175, s[36:37]
	s_mov_b32 m0, s46
	s_nop 0
	global_load_lds_dwordx4 v173, s[36:37]
	s_waitcnt vmcnt(8)
	s_waitcnt lgkmcnt(0)
	s_barrier
	s_setprio 1
	s_waitcnt lgkmcnt(0)
	v_mfma_f32_16x16x128_f8f6f4 v[156:159], v[0:7], v[222:229], v[156:159]
	v_mfma_f32_16x16x128_f8f6f4 v[152:155], v[8:15], v[222:229], v[152:155]
	v_mfma_f32_16x16x128_f8f6f4 v[140:143], v[0:7], v[230:237], v[140:143]
	v_mfma_f32_16x16x128_f8f6f4 v[136:139], v[8:15], v[230:237], v[136:139]
	v_mfma_f32_16x16x128_f8f6f4 v[124:127], v[0:7], v[238:245], v[124:127]
	v_mfma_f32_16x16x128_f8f6f4 v[120:123], v[8:15], v[238:245], v[120:123]
	v_mfma_f32_16x16x128_f8f6f4 v[108:111], v[0:7], v[246:253], v[108:111]
	v_mfma_f32_16x16x128_f8f6f4 v[104:107], v[8:15], v[246:253], v[104:107]
	s_setprio 0
	s_setprio 1
	v_mfma_f32_16x16x128_f8f6f4 v[148:151], v[16:23], v[222:229], v[148:151]
	v_mfma_f32_16x16x128_f8f6f4 v[144:147], v[24:31], v[222:229], v[144:147]
	v_mfma_f32_16x16x128_f8f6f4 v[132:135], v[16:23], v[230:237], v[132:135]
	v_mfma_f32_16x16x128_f8f6f4 v[128:131], v[24:31], v[230:237], v[128:131]
	v_mfma_f32_16x16x128_f8f6f4 v[116:119], v[16:23], v[238:245], v[116:119]
	v_mfma_f32_16x16x128_f8f6f4 v[112:115], v[24:31], v[238:245], v[112:115]
	v_mfma_f32_16x16x128_f8f6f4 v[100:103], v[16:23], v[246:253], v[100:103]
	v_mfma_f32_16x16x128_f8f6f4 v[96:99], v[24:31], v[246:253], v[96:99]
	s_setprio 0
	s_barrier
	s_mov_b32 m0, s47
	v_lshl_add_u64 v[186:187], v[186:187], 0, s[16:17]
	ds_read_b128 v[222:225], v212 offset:49152
	ds_read_b128 v[226:229], v212 offset:50176
	ds_read_b128 v[230:233], v212 offset:51200
	ds_read_b128 v[234:237], v212 offset:52224
	ds_read_b128 v[238:241], v212 offset:53248
	ds_read_b128 v[242:245], v212 offset:54272
	ds_read_b128 v[246:249], v212 offset:55296
	ds_read_b128 v[250:253], v212 offset:56320
	global_load_lds_dwordx4 v[186:187], off
	v_lshl_add_u64 v[186:187], v[188:189], 0, s[16:17]
	s_mov_b32 m0, s48
	v_lshl_add_u64 v[182:183], v[182:183], 0, s[26:27]
	global_load_lds_dwordx4 v[186:187], off
	v_lshl_add_u64 v[186:187], v[182:183], 0, v[164:165]
	s_mov_b32 m0, s51
	v_lshl_add_u64 v[182:183], v[182:183], 0, v[162:163]
	global_load_lds_dwordx4 v[186:187], off
	s_mov_b32 m0, s52
	s_nop 0
	global_load_lds_dwordx4 v[182:183], off
	s_waitcnt vmcnt(6)
	s_waitcnt lgkmcnt(0)
	s_barrier
	s_setprio 1
	s_waitcnt lgkmcnt(0)
	v_mfma_f32_16x16x128_f8f6f4 v[84:87], v[0:7], v[222:229], v[84:87]
	v_mfma_f32_16x16x128_f8f6f4 v[80:83], v[8:15], v[222:229], v[80:83]
	v_mfma_f32_16x16x128_f8f6f4 v[68:71], v[0:7], v[230:237], v[68:71]
	v_mfma_f32_16x16x128_f8f6f4 v[64:67], v[8:15], v[230:237], v[64:67]
	v_mfma_f32_16x16x128_f8f6f4 v[52:55], v[0:7], v[238:245], v[52:55]
	v_mfma_f32_16x16x128_f8f6f4 v[48:51], v[8:15], v[238:245], v[48:51]
	v_mfma_f32_16x16x128_f8f6f4 v[36:39], v[0:7], v[246:253], v[36:39]
	v_mfma_f32_16x16x128_f8f6f4 v[32:35], v[8:15], v[246:253], v[32:35]
	s_setprio 0
	v_lshl_add_u64 v[182:183], v[190:191], 0, s[16:17]
	s_mov_b32 m0, s49
	s_nop 0
	global_load_lds_dwordx4 v[182:183], off
	v_lshl_add_u64 v[182:183], v[184:185], 0, s[16:17]
	s_mov_b32 m0, s50
	s_nop 0
	global_load_lds_dwordx4 v[182:183], off
	s_setprio 1
	v_mfma_f32_16x16x128_f8f6f4 v[92:95], v[16:23], v[222:229], v[92:95]
	v_mfma_f32_16x16x128_f8f6f4 v[88:91], v[24:31], v[222:229], v[88:91]
	v_mfma_f32_16x16x128_f8f6f4 v[76:79], v[16:23], v[230:237], v[76:79]
	v_mfma_f32_16x16x128_f8f6f4 v[72:75], v[24:31], v[230:237], v[72:75]
	v_mfma_f32_16x16x128_f8f6f4 v[60:63], v[16:23], v[238:245], v[60:63]
	v_mfma_f32_16x16x128_f8f6f4 v[56:59], v[24:31], v[238:245], v[56:59]
	v_mfma_f32_16x16x128_f8f6f4 v[44:47], v[16:23], v[246:253], v[44:47]
	v_mfma_f32_16x16x128_f8f6f4 v[40:43], v[24:31], v[246:253], v[40:43]
	s_setprio 0
	s_barrier
	s_add_i32 s35, s35, 2
	s_add_u32 s4, s4, 0x100
	s_addc_u32 s5, s5, 0
	s_cmp_gt_u32 s35, 5
	s_cbranch_scc0 .LBB0_2571
	s_nop 15
	s_nop 7
	s_and_b64 vcc, exec, s[28:29]
	s_cbranch_vccz .LBB0_2574
	s_barrier

.LBB0_2669:
	s_mov_b64 s[80:81], 0x100
	v_lshl_add_u64 v[0:1], v[168:169], 0, s[36:37]
	v_lshl_add_u64 v[0:1], v[0:1], 0, s[80:81]
	v_cndmask_b32_e64 v179, v1, v171, s[34:35]
	v_cndmask_b32_e64 v178, v0, v205, s[34:35]
	ds_read_b128 v[8:11], v185
	ds_read_b128 v[12:15], v189
	ds_read_b128 v[24:27], v190
	ds_read_b128 v[28:31], v191
	ds_read_b128 v[0:3], v186
	ds_read_b128 v[4:7], v192
	ds_read_b128 v[16:19], v193
	ds_read_b128 v[20:23], v194
	s_add_u32 s15, s24, s36
	s_addc_u32 s79, s25, s37
	s_add_u32 s82, s15, 0x100
	s_addc_u32 s83, s79, 0
	s_and_b64 s[38:39], s[34:35], exec
	s_cselect_b32 s39, s27, s83
	s_cselect_b32 s38, s78, s82
	s_add_u32 s36, s15, 0x10080
	s_addc_u32 s37, s79, 0
	s_add_i32 m0, s43, 0xc000
	s_add_i32 s15, s43, 0xe000
	s_add_u32 s34, s38, 0x10000
	s_addc_u32 s35, s39, 0
	v_lshl_add_u64 v[180:181], v[178:179], 0, s[0:1]
	v_lshl_add_u64 v[174:175], v[178:179], 0, s[10:11]
	v_lshl_add_u64 v[176:177], s[36:37], 0, v[164:165]
	ds_read_b128 v[206:209], v203
	ds_read_b128 v[210:213], v203 offset:1024
	ds_read_b128 v[214:217], v203 offset:2048
	ds_read_b128 v[218:221], v203 offset:3072
	ds_read_b128 v[222:225], v203 offset:4096
	ds_read_b128 v[226:229], v203 offset:5120
	ds_read_b128 v[230:233], v203 offset:6144
	ds_read_b128 v[234:237], v203 offset:7168
	global_load_lds_dwordx4 v[176:177], off
	v_lshl_add_u64 v[176:177], s[36:37], 0, v[166:167]
	s_mov_b32 m0, s15
	s_nop 0
	global_load_lds_dwordx4 v[176:177], off
	s_waitcnt vmcnt(8)
	s_waitcnt lgkmcnt(0)
	s_barrier
	s_setprio 1
	s_waitcnt lgkmcnt(0)
	v_mfma_f32_16x16x128_f8f6f4 v[156:159], v[8:15], v[206:213], v[156:159]
	v_mfma_f32_16x16x128_f8f6f4 v[152:155], v[24:31], v[206:213], v[152:155]
	v_mfma_f32_16x16x128_f8f6f4 v[140:143], v[8:15], v[214:221], v[140:143]
	v_mfma_f32_16x16x128_f8f6f4 v[136:139], v[24:31], v[214:221], v[136:139]
	v_mfma_f32_16x16x128_f8f6f4 v[124:127], v[8:15], v[222:229], v[124:127]
	v_mfma_f32_16x16x128_f8f6f4 v[120:123], v[24:31], v[222:229], v[120:123]
	v_mfma_f32_16x16x128_f8f6f4 v[108:111], v[8:15], v[230:237], v[108:111]
	v_mfma_f32_16x16x128_f8f6f4 v[104:107], v[24:31], v[230:237], v[104:107]
	s_setprio 0
	s_setprio 1
	v_mfma_f32_16x16x128_f8f6f4 v[148:151], v[0:7], v[206:213], v[148:151]
	v_mfma_f32_16x16x128_f8f6f4 v[144:147], v[16:23], v[206:213], v[144:147]
	v_mfma_f32_16x16x128_f8f6f4 v[132:135], v[0:7], v[214:221], v[132:135]
	v_mfma_f32_16x16x128_f8f6f4 v[128:131], v[16:23], v[214:221], v[128:131]
	v_mfma_f32_16x16x128_f8f6f4 v[116:119], v[0:7], v[222:229], v[116:119]
	v_mfma_f32_16x16x128_f8f6f4 v[112:115], v[16:23], v[222:229], v[112:115]
	v_mfma_f32_16x16x128_f8f6f4 v[96:99], v[0:7], v[230:237], v[96:99]
	v_mfma_f32_16x16x128_f8f6f4 v[88:91], v[16:23], v[230:237], v[88:91]
	s_setprio 0
	s_barrier
	s_mov_b32 m0, s44
	v_lshl_add_u64 v[176:177], v[178:179], 0, v[162:163]
	ds_read_b128 v[206:209], v203 offset:16384
	ds_read_b128 v[210:213], v203 offset:17408
	ds_read_b128 v[214:217], v203 offset:18432
	ds_read_b128 v[218:221], v203 offset:19456
	ds_read_b128 v[222:225], v203 offset:20480
	ds_read_b128 v[226:229], v203 offset:21504
	ds_read_b128 v[230:233], v203 offset:22528
	ds_read_b128 v[234:237], v203 offset:23552
	global_load_lds_dwordx4 v[176:177], off
	v_lshl_add_u64 v[178:179], v[178:179], 0, v[160:161]
	s_mov_b32 m0, s45
	v_lshl_add_u64 v[182:183], v[180:181], 0, v[162:163]
	global_load_lds_dwordx4 v[178:179], off
	s_mov_b32 m0, s46
	v_lshl_add_u64 v[180:181], v[180:181], 0, v[160:161]
	global_load_lds_dwordx4 v[182:183], off
	s_mov_b32 m0, s47
	v_lshl_add_u64 v[182:183], s[38:39], 0, v[166:167]
	global_load_lds_dwordx4 v[180:181], off
	s_waitcnt vmcnt(6)
	s_waitcnt lgkmcnt(0)
	s_barrier
	s_setprio 1
	s_waitcnt lgkmcnt(0)
	v_mfma_f32_16x16x128_f8f6f4 v[84:87], v[8:15], v[206:213], v[84:87]
	v_mfma_f32_16x16x128_f8f6f4 v[76:79], v[24:31], v[206:213], v[76:79]
	v_mfma_f32_16x16x128_f8f6f4 v[60:63], v[8:15], v[214:221], v[60:63]
	v_mfma_f32_16x16x128_f8f6f4 v[48:51], v[24:31], v[214:221], v[48:51]
	v_mfma_f32_16x16x128_f8f6f4 v[68:71], v[8:15], v[222:229], v[68:71]
	v_mfma_f32_16x16x128_f8f6f4 v[56:59], v[24:31], v[222:229], v[56:59]
	v_mfma_f32_16x16x128_f8f6f4 v[44:47], v[8:15], v[230:237], v[44:47]
	v_mfma_f32_16x16x128_f8f6f4 v[36:39], v[24:31], v[230:237], v[36:39]
	s_setprio 0
	v_lshl_add_u64 v[180:181], s[38:39], 0, v[164:165]
	s_mov_b32 m0, s43
	s_nop 0
	global_load_lds_dwordx4 v[180:181], off
	s_mov_b32 m0, s48
	s_nop 0
	global_load_lds_dwordx4 v[182:183], off
	s_setprio 1
	v_mfma_f32_16x16x128_f8f6f4 v[100:103], v[0:7], v[206:213], v[100:103]
	v_mfma_f32_16x16x128_f8f6f4 v[92:95], v[16:23], v[206:213], v[92:95]
	v_mfma_f32_16x16x128_f8f6f4 v[80:83], v[0:7], v[214:221], v[80:83]
	v_mfma_f32_16x16x128_f8f6f4 v[72:75], v[16:23], v[214:221], v[72:75]
	v_mfma_f32_16x16x128_f8f6f4 v[64:67], v[0:7], v[222:229], v[64:67]
	v_mfma_f32_16x16x128_f8f6f4 v[52:55], v[16:23], v[222:229], v[52:55]
	v_mfma_f32_16x16x128_f8f6f4 v[40:43], v[0:7], v[230:237], v[40:43]
	v_mfma_f32_16x16x128_f8f6f4 v[32:35], v[16:23], v[230:237], v[32:35]
	s_setprio 0
	s_barrier
	ds_read_b128 v[4:7], v195
	ds_read_b128 v[8:11], v196
	ds_read_b128 v[0:3], v187
	ds_read_b128 v[16:19], v188
	ds_read_b128 v[12:15], v197
	ds_read_b128 v[20:23], v198
	ds_read_b128 v[24:27], v199
	ds_read_b128 v[28:31], v200
	s_mov_b32 m0, s49
	v_lshl_add_u64 v[238:239], s[34:35], 0, v[164:165]
	ds_read_b128 v[206:209], v203 offset:32768
	ds_read_b128 v[210:213], v203 offset:33792
	ds_read_b128 v[214:217], v203 offset:34816
	ds_read_b128 v[218:221], v203 offset:35840
	ds_read_b128 v[222:225], v203 offset:36864
	ds_read_b128 v[226:229], v203 offset:37888
	ds_read_b128 v[230:233], v203 offset:38912
	ds_read_b128 v[234:237], v203 offset:39936
	global_load_lds_dwordx4 v[238:239], off
	v_lshl_add_u64 v[238:239], s[34:35], 0, v[166:167]
	s_mov_b32 m0, s50
	s_nop 0
	global_load_lds_dwordx4 v[238:239], off
	s_waitcnt vmcnt(8)
	s_waitcnt lgkmcnt(0)
	s_barrier
	s_setprio 1
	s_waitcnt lgkmcnt(0)
	v_mfma_f32_16x16x128_f8f6f4 v[156:159], v[0:7], v[206:213], v[156:159]
	v_mfma_f32_16x16x128_f8f6f4 v[152:155], v[8:15], v[206:213], v[152:155]
	v_mfma_f32_16x16x128_f8f6f4 v[140:143], v[0:7], v[214:221], v[140:143]
	v_mfma_f32_16x16x128_f8f6f4 v[136:139], v[8:15], v[214:221], v[136:139]
	v_mfma_f32_16x16x128_f8f6f4 v[124:127], v[0:7], v[222:229], v[124:127]
	v_mfma_f32_16x16x128_f8f6f4 v[120:123], v[8:15], v[222:229], v[120:123]
	v_mfma_f32_16x16x128_f8f6f4 v[108:111], v[0:7], v[230:237], v[108:111]
	v_mfma_f32_16x16x128_f8f6f4 v[104:107], v[8:15], v[230:237], v[104:107]
	s_setprio 0
	s_setprio 1
	v_mfma_f32_16x16x128_f8f6f4 v[148:151], v[16:23], v[206:213], v[148:151]
	v_mfma_f32_16x16x128_f8f6f4 v[144:147], v[24:31], v[206:213], v[144:147]
	v_mfma_f32_16x16x128_f8f6f4 v[132:135], v[16:23], v[214:221], v[132:135]
	v_mfma_f32_16x16x128_f8f6f4 v[128:131], v[24:31], v[214:221], v[128:131]
	v_mfma_f32_16x16x128_f8f6f4 v[116:119], v[16:23], v[222:229], v[116:119]
	v_mfma_f32_16x16x128_f8f6f4 v[112:115], v[24:31], v[222:229], v[112:115]
	v_mfma_f32_16x16x128_f8f6f4 v[96:99], v[16:23], v[230:237], v[96:99]
	v_mfma_f32_16x16x128_f8f6f4 v[88:91], v[24:31], v[230:237], v[88:91]
	s_setprio 0
	s_barrier
	s_mov_b32 m0, s52
	v_lshl_add_u64 v[176:177], v[176:177], 0, s[8:9]
	ds_read_b128 v[206:209], v203 offset:49152
	ds_read_b128 v[210:213], v203 offset:50176
	ds_read_b128 v[214:217], v203 offset:51200
	ds_read_b128 v[218:221], v203 offset:52224
	ds_read_b128 v[222:225], v203 offset:53248
	ds_read_b128 v[226:229], v203 offset:54272
	ds_read_b128 v[230:233], v203 offset:55296
	ds_read_b128 v[234:237], v203 offset:56320
	global_load_lds_dwordx4 v[176:177], off
	v_lshl_add_u64 v[176:177], v[178:179], 0, s[8:9]
	s_mov_b32 m0, s53
	s_nop 0
	global_load_lds_dwordx4 v[176:177], off
	v_lshl_add_u64 v[176:177], v[174:175], 0, v[162:163]
	s_mov_b32 m0, s56
	v_lshl_add_u64 v[174:175], v[174:175], 0, v[160:161]
	global_load_lds_dwordx4 v[176:177], off
	s_mov_b32 m0, s57
	s_nop 0
	global_load_lds_dwordx4 v[174:175], off
	s_waitcnt vmcnt(6)
	s_waitcnt lgkmcnt(0)
	s_barrier
	s_setprio 1
	s_waitcnt lgkmcnt(0)
	v_mfma_f32_16x16x128_f8f6f4 v[84:87], v[0:7], v[206:213], v[84:87]
	v_mfma_f32_16x16x128_f8f6f4 v[76:79], v[8:15], v[206:213], v[76:79]
	v_mfma_f32_16x16x128_f8f6f4 v[60:63], v[0:7], v[214:221], v[60:63]
	v_mfma_f32_16x16x128_f8f6f4 v[48:51], v[8:15], v[214:221], v[48:51]
	v_mfma_f32_16x16x128_f8f6f4 v[68:71], v[0:7], v[222:229], v[68:71]
	v_mfma_f32_16x16x128_f8f6f4 v[56:59], v[8:15], v[222:229], v[56:59]
	v_mfma_f32_16x16x128_f8f6f4 v[44:47], v[0:7], v[230:237], v[44:47]
	v_mfma_f32_16x16x128_f8f6f4 v[36:39], v[8:15], v[230:237], v[36:39]
	s_setprio 0
	v_lshl_add_u64 v[174:175], v[180:181], 0, s[8:9]
	s_mov_b32 m0, s54
	s_nop 0
	global_load_lds_dwordx4 v[174:175], off
	v_lshl_add_u64 v[174:175], v[182:183], 0, s[8:9]
	s_mov_b32 m0, s55
	s_nop 0
	global_load_lds_dwordx4 v[174:175], off
	s_setprio 1
	v_mfma_f32_16x16x128_f8f6f4 v[100:103], v[16:23], v[206:213], v[100:103]
	v_mfma_f32_16x16x128_f8f6f4 v[92:95], v[24:31], v[206:213], v[92:95]
	v_mfma_f32_16x16x128_f8f6f4 v[80:83], v[16:23], v[214:221], v[80:83]
	v_mfma_f32_16x16x128_f8f6f4 v[72:75], v[24:31], v[214:221], v[72:75]
	v_mfma_f32_16x16x128_f8f6f4 v[64:67], v[16:23], v[222:229], v[64:67]
	v_mfma_f32_16x16x128_f8f6f4 v[52:55], v[24:31], v[222:229], v[52:55]
	v_mfma_f32_16x16x128_f8f6f4 v[40:43], v[16:23], v[230:237], v[40:43]
	v_mfma_f32_16x16x128_f8f6f4 v[32:35], v[24:31], v[230:237], v[32:35]
	s_setprio 0
	s_barrier
	s_andn2_b64 vcc, exec, s[30:31]
	s_mov_b64 s[34:35], -1
	s_mov_b64 s[30:31], 0
	s_mov_b64 s[36:37], 0x100
	s_cbranch_vccz .LBB0_2669
	s_nop 15
	s_nop 7
	s_and_b64 vcc, exec, s[12:13]
	s_cbranch_vccz .LBB0_2672
	s_barrier

.LBB0_2932:
	s_waitcnt lgkmcnt(0)
	ds_read_b128 v[20:23], v188
	ds_read_b128 v[24:27], v189
	ds_read_b128 v[16:19], v183
	ds_read_b128 v[0:3], v184
	ds_read_b128 v[28:31], v190
	ds_read_b128 v[4:7], v191
	ds_read_b128 v[8:11], v192
	ds_read_b128 v[12:15], v193
	s_add_u32 s24, s22, 0xfffe0080
	s_addc_u32 s25, s23, -1
	s_cmp_eq_u32 s58, 4
	s_cselect_b32 s27, s15, s25
	s_cselect_b32 s26, s54, s24
	s_cselect_b32 s25, s13, s57
	s_cselect_b32 s24, s55, s56
	v_lshl_add_u64 v[232:233], s[22:23], 0, v[168:169]
	s_add_i32 m0, s33, 0xc000
	ds_read_b128 v[174:177], v200
	ds_read_b128 v[178:181], v200 offset:1024
	ds_read_b128 v[208:211], v200 offset:2048
	ds_read_b128 v[212:215], v200 offset:3072
	ds_read_b128 v[216:219], v200 offset:4096
	ds_read_b128 v[220:223], v200 offset:5120
	ds_read_b128 v[224:227], v200 offset:6144
	ds_read_b128 v[228:231], v200 offset:7168
	global_load_lds_dwordx4 v[232:233], off
	v_lshl_add_u64 v[232:233], s[22:23], 0, v[170:171]
	s_add_i32 m0, s33, 0xe000
	s_nop 0
	global_load_lds_dwordx4 v[232:233], off
	s_waitcnt vmcnt(8)
	s_waitcnt lgkmcnt(0)
	s_barrier
	s_setprio 1
	s_waitcnt lgkmcnt(0)
	v_mfma_f32_16x16x128_f8f6f4 v[156:159], v[16:23], v[174:181], v[156:159]
	v_mfma_f32_16x16x128_f8f6f4 v[124:127], v[24:31], v[174:181], v[124:127]
	v_mfma_f32_16x16x128_f8f6f4 v[144:147], v[16:23], v[208:215], v[144:147]
	v_mfma_f32_16x16x128_f8f6f4 v[112:115], v[24:31], v[208:215], v[112:115]
	v_mfma_f32_16x16x128_f8f6f4 v[140:143], v[16:23], v[216:223], v[140:143]
	v_mfma_f32_16x16x128_f8f6f4 v[108:111], v[24:31], v[216:223], v[108:111]
	v_mfma_f32_16x16x128_f8f6f4 v[136:139], v[16:23], v[224:231], v[136:139]
	v_mfma_f32_16x16x128_f8f6f4 v[96:99], v[24:31], v[224:231], v[96:99]
	s_setprio 0
	s_setprio 1
	v_mfma_f32_16x16x128_f8f6f4 v[72:75], v[0:7], v[174:181], v[72:75]
	v_mfma_f32_16x16x128_f8f6f4 v[44:47], v[8:15], v[174:181], v[44:47]
	v_mfma_f32_16x16x128_f8f6f4 v[56:59], v[0:7], v[208:215], v[56:59]
	v_mfma_f32_16x16x128_f8f6f4 v[40:43], v[8:15], v[208:215], v[40:43]
	v_mfma_f32_16x16x128_f8f6f4 v[52:55], v[0:7], v[216:223], v[52:55]
	v_mfma_f32_16x16x128_f8f6f4 v[36:39], v[8:15], v[216:223], v[36:39]
	v_mfma_f32_16x16x128_f8f6f4 v[48:51], v[0:7], v[224:231], v[48:51]
	v_mfma_f32_16x16x128_f8f6f4 v[32:35], v[8:15], v[224:231], v[32:35]
	s_setprio 0
	s_barrier
	s_mov_b32 m0, s34
	v_lshl_add_u64 v[174:175], s[24:25], 0, v[162:163]
	s_add_u32 s60, s24, 0x20000
	ds_read_b128 v[208:211], v200 offset:16384
	ds_read_b128 v[212:215], v200 offset:17408
	ds_read_b128 v[216:219], v200 offset:18432
	ds_read_b128 v[220:223], v200 offset:19456
	ds_read_b128 v[224:227], v200 offset:20480
	ds_read_b128 v[228:231], v200 offset:21504
	ds_read_b128 v[232:235], v200 offset:22528
	ds_read_b128 v[236:239], v200 offset:23552
	global_load_lds_dwordx4 v[174:175], off
	v_lshl_add_u64 v[176:177], s[24:25], 0, v[160:161]
	s_mov_b32 m0, s35
	s_addc_u32 s61, s25, 0
	global_load_lds_dwordx4 v[176:177], off
	v_lshl_add_u64 v[178:179], s[60:61], 0, v[162:163]
	s_mov_b32 m0, s36
	v_lshl_add_u64 v[180:181], s[26:27], 0, v[166:167]
	global_load_lds_dwordx4 v[178:179], off
	v_lshl_add_u64 v[178:179], s[60:61], 0, v[160:161]
	s_mov_b32 m0, s37
	s_nop 0
	global_load_lds_dwordx4 v[178:179], off
	s_waitcnt vmcnt(6)
	s_waitcnt lgkmcnt(0)
	s_barrier
	s_setprio 1
	s_waitcnt lgkmcnt(0)
	v_mfma_f32_16x16x128_f8f6f4 v[128:131], v[16:23], v[208:215], v[128:131]
	v_mfma_f32_16x16x128_f8f6f4 v[84:87], v[24:31], v[208:215], v[84:87]
	v_mfma_f32_16x16x128_f8f6f4 v[116:119], v[16:23], v[216:223], v[116:119]
	v_mfma_f32_16x16x128_f8f6f4 v[64:67], v[24:31], v[216:223], v[64:67]
	v_mfma_f32_16x16x128_f8f6f4 v[148:151], v[16:23], v[224:231], v[148:151]
	v_mfma_f32_16x16x128_f8f6f4 v[120:123], v[24:31], v[224:231], v[120:123]
	v_mfma_f32_16x16x128_f8f6f4 v[152:155], v[16:23], v[232:239], v[152:155]
	v_mfma_f32_16x16x128_f8f6f4 v[132:135], v[24:31], v[232:239], v[132:135]
	s_setprio 0
	v_lshl_add_u64 v[178:179], s[26:27], 0, v[164:165]
	s_mov_b32 m0, s33
	s_nop 0
	global_load_lds_dwordx4 v[178:179], off
	s_mov_b32 m0, s38
	s_nop 0
	global_load_lds_dwordx4 v[180:181], off
	s_setprio 1
	v_mfma_f32_16x16x128_f8f6f4 v[88:91], v[0:7], v[208:215], v[88:91]
	v_mfma_f32_16x16x128_f8f6f4 v[60:63], v[8:15], v[208:215], v[60:63]
	v_mfma_f32_16x16x128_f8f6f4 v[92:95], v[0:7], v[216:223], v[92:95]
	v_mfma_f32_16x16x128_f8f6f4 v[68:71], v[8:15], v[216:223], v[68:71]
	v_mfma_f32_16x16x128_f8f6f4 v[100:103], v[0:7], v[224:231], v[100:103]
	v_mfma_f32_16x16x128_f8f6f4 v[76:79], v[8:15], v[224:231], v[76:79]
	v_mfma_f32_16x16x128_f8f6f4 v[104:107], v[0:7], v[232:239], v[104:107]
	v_mfma_f32_16x16x128_f8f6f4 v[80:83], v[8:15], v[232:239], v[80:83]
	s_setprio 0
	s_barrier
	ds_read_b128 v[4:7], v194
	ds_read_b128 v[8:11], v195
	ds_read_b128 v[0:3], v185
	ds_read_b128 v[16:19], v186
	ds_read_b128 v[12:15], v196
	ds_read_b128 v[20:23], v197
	ds_read_b128 v[24:27], v198
	ds_read_b128 v[28:31], v199
	s_add_u32 s26, s26, 0x20000
	s_addc_u32 s27, s27, 0
	s_mov_b32 m0, s39
	v_lshl_add_u64 v[240:241], s[26:27], 0, v[164:165]
	ds_read_b128 v[208:211], v200 offset:32768
	ds_read_b128 v[212:215], v200 offset:33792
	ds_read_b128 v[216:219], v200 offset:34816
	ds_read_b128 v[220:223], v200 offset:35840
	ds_read_b128 v[224:227], v200 offset:36864
	ds_read_b128 v[228:231], v200 offset:37888
	ds_read_b128 v[232:235], v200 offset:38912
	ds_read_b128 v[236:239], v200 offset:39936
	global_load_lds_dwordx4 v[240:241], off
	v_lshl_add_u64 v[240:241], s[26:27], 0, v[166:167]
	s_mov_b32 m0, s40
	s_nop 0
	global_load_lds_dwordx4 v[240:241], off
	s_waitcnt vmcnt(8)
	s_waitcnt lgkmcnt(0)
	s_barrier
	s_setprio 1
	s_waitcnt lgkmcnt(0)
	v_mfma_f32_16x16x128_f8f6f4 v[156:159], v[0:7], v[208:215], v[156:159]
	v_mfma_f32_16x16x128_f8f6f4 v[124:127], v[8:15], v[208:215], v[124:127]
	v_mfma_f32_16x16x128_f8f6f4 v[144:147], v[0:7], v[216:223], v[144:147]
	v_mfma_f32_16x16x128_f8f6f4 v[112:115], v[8:15], v[216:223], v[112:115]
	v_mfma_f32_16x16x128_f8f6f4 v[140:143], v[0:7], v[224:231], v[140:143]
	v_mfma_f32_16x16x128_f8f6f4 v[108:111], v[8:15], v[224:231], v[108:111]
	v_mfma_f32_16x16x128_f8f6f4 v[136:139], v[0:7], v[232:239], v[136:139]
	v_mfma_f32_16x16x128_f8f6f4 v[96:99], v[8:15], v[232:239], v[96:99]
	s_setprio 0
	s_setprio 1
	v_mfma_f32_16x16x128_f8f6f4 v[72:75], v[16:23], v[208:215], v[72:75]
	v_mfma_f32_16x16x128_f8f6f4 v[44:47], v[24:31], v[208:215], v[44:47]
	v_mfma_f32_16x16x128_f8f6f4 v[56:59], v[16:23], v[216:223], v[56:59]
	v_mfma_f32_16x16x128_f8f6f4 v[40:43], v[24:31], v[216:223], v[40:43]
	v_mfma_f32_16x16x128_f8f6f4 v[52:55], v[16:23], v[224:231], v[52:55]
	v_mfma_f32_16x16x128_f8f6f4 v[36:39], v[24:31], v[224:231], v[36:39]
	v_mfma_f32_16x16x128_f8f6f4 v[48:51], v[16:23], v[232:239], v[48:51]
	v_mfma_f32_16x16x128_f8f6f4 v[32:35], v[24:31], v[232:239], v[32:35]
	s_setprio 0
	s_barrier
	s_mov_b32 m0, s42
	v_lshl_add_u64 v[174:175], v[174:175], 0, s[8:9]
	s_add_u32 s24, s24, 0x20080
	ds_read_b128 v[208:211], v200 offset:49152
	ds_read_b128 v[212:215], v200 offset:50176
	ds_read_b128 v[216:219], v200 offset:51200
	ds_read_b128 v[220:223], v200 offset:52224
	ds_read_b128 v[224:227], v200 offset:53248
	ds_read_b128 v[228:231], v200 offset:54272
	ds_read_b128 v[232:235], v200 offset:55296
	ds_read_b128 v[236:239], v200 offset:56320
	global_load_lds_dwordx4 v[174:175], off
	v_lshl_add_u64 v[174:175], v[176:177], 0, s[8:9]
	s_mov_b32 m0, s43
	s_addc_u32 s25, s25, 0
	global_load_lds_dwordx4 v[174:175], off
	v_lshl_add_u64 v[174:175], s[24:25], 0, v[162:163]
	s_mov_b32 m0, s46
	s_nop 0
	global_load_lds_dwordx4 v[174:175], off
	v_lshl_add_u64 v[174:175], s[24:25], 0, v[160:161]
	s_mov_b32 m0, s47
	s_nop 0
	global_load_lds_dwordx4 v[174:175], off
	s_waitcnt vmcnt(6)
	s_waitcnt lgkmcnt(0)
	s_barrier
	s_setprio 1
	s_waitcnt lgkmcnt(0)
	v_mfma_f32_16x16x128_f8f6f4 v[128:131], v[0:7], v[208:215], v[128:131]
	v_mfma_f32_16x16x128_f8f6f4 v[84:87], v[8:15], v[208:215], v[84:87]
	v_mfma_f32_16x16x128_f8f6f4 v[116:119], v[0:7], v[216:223], v[116:119]
	v_mfma_f32_16x16x128_f8f6f4 v[64:67], v[8:15], v[216:223], v[64:67]
	v_mfma_f32_16x16x128_f8f6f4 v[148:151], v[0:7], v[224:231], v[148:151]
	v_mfma_f32_16x16x128_f8f6f4 v[120:123], v[8:15], v[224:231], v[120:123]
	v_mfma_f32_16x16x128_f8f6f4 v[152:155], v[0:7], v[232:239], v[152:155]
	v_mfma_f32_16x16x128_f8f6f4 v[132:135], v[8:15], v[232:239], v[132:135]
	s_setprio 0
	v_lshl_add_u64 v[174:175], v[178:179], 0, s[8:9]
	s_mov_b32 m0, s44
	s_nop 0
	global_load_lds_dwordx4 v[174:175], off
	v_lshl_add_u64 v[174:175], v[180:181], 0, s[8:9]
	s_mov_b32 m0, s45
	s_nop 0
	global_load_lds_dwordx4 v[174:175], off
	s_setprio 1
	v_mfma_f32_16x16x128_f8f6f4 v[88:91], v[16:23], v[208:215], v[88:91]
	v_mfma_f32_16x16x128_f8f6f4 v[60:63], v[24:31], v[208:215], v[60:63]
	v_mfma_f32_16x16x128_f8f6f4 v[92:95], v[16:23], v[216:223], v[92:95]
	v_mfma_f32_16x16x128_f8f6f4 v[68:71], v[24:31], v[216:223], v[68:71]
	v_mfma_f32_16x16x128_f8f6f4 v[100:103], v[16:23], v[224:231], v[100:103]
	v_mfma_f32_16x16x128_f8f6f4 v[76:79], v[24:31], v[224:231], v[76:79]
	v_mfma_f32_16x16x128_f8f6f4 v[104:107], v[16:23], v[232:239], v[104:107]
	v_mfma_f32_16x16x128_f8f6f4 v[80:83], v[24:31], v[232:239], v[80:83]
	s_setprio 0
	s_barrier
	s_add_i32 s58, s58, 2
	s_add_u32 s22, s22, 0x100
	s_addc_u32 s23, s23, 0
	s_add_u32 s56, s56, 0x100
	s_addc_u32 s57, s57, 0
	s_cmp_gt_u32 s58, 5
	s_cbranch_scc0 .LBB0_2932
	s_nop 15
	s_nop 7
	s_and_b64 vcc, exec, s[10:11]
	s_cbranch_vccz .LBB0_2935
	s_barrier

.LBB0_3128:
	ds_read_b128 v[20:23], v213
	ds_read_b128 v[24:27], v214
	ds_read_b128 v[16:19], v209
	ds_read_b128 v[0:3], v210
	ds_read_b128 v[28:31], v215
	ds_read_b128 v[4:7], v216
	ds_read_b128 v[8:11], v217
	ds_read_b128 v[12:15], v218
	s_add_u32 s6, s2, 0xfffe0080
	s_addc_u32 s7, s3, -1
	s_cmp_eq_u32 s49, 4
	s_cselect_b32 s47, s1, s7
	s_cselect_b32 s46, s5, s6
	s_cselect_b32 s7, s33, s48
	s_cselect_b32 s6, s37, s39
	v_lshl_add_u64 v[202:203], s[2:3], 0, v[194:195]
	s_add_i32 m0, s55, 0xc000
	ds_read_b128 v[160:163], v225
	ds_read_b128 v[164:167], v225 offset:1024
	ds_read_b128 v[168:171], v225 offset:2048
	ds_read_b128 v[172:175], v225 offset:3072
	ds_read_b128 v[176:179], v225 offset:4096
	ds_read_b128 v[180:183], v225 offset:5120
	ds_read_b128 v[232:235], v225 offset:6144
	ds_read_b128 v[236:239], v225 offset:7168
	global_load_lds_dwordx4 v[202:203], off
	v_lshl_add_u64 v[202:203], s[2:3], 0, v[196:197]
	s_add_i32 m0, s55, 0xe000
	s_nop 0
	global_load_lds_dwordx4 v[202:203], off
	s_waitcnt vmcnt(8)
	s_waitcnt lgkmcnt(0)
	s_barrier
	s_setprio 1
	s_waitcnt lgkmcnt(0)
	v_mfma_f32_16x16x128_f8f6f4 v[156:159], v[16:23], v[160:167], v[156:159]
	v_mfma_f32_16x16x128_f8f6f4 v[152:155], v[24:31], v[160:167], v[152:155]
	v_mfma_f32_16x16x128_f8f6f4 v[140:143], v[16:23], v[168:175], v[140:143]
	v_mfma_f32_16x16x128_f8f6f4 v[136:139], v[24:31], v[168:175], v[136:139]
	v_mfma_f32_16x16x128_f8f6f4 v[124:127], v[16:23], v[176:183], v[124:127]
	v_mfma_f32_16x16x128_f8f6f4 v[120:123], v[24:31], v[176:183], v[120:123]
	v_mfma_f32_16x16x128_f8f6f4 v[108:111], v[16:23], v[232:239], v[108:111]
	v_mfma_f32_16x16x128_f8f6f4 v[104:107], v[24:31], v[232:239], v[104:107]
	s_setprio 0
	s_setprio 1
	v_mfma_f32_16x16x128_f8f6f4 v[148:151], v[0:7], v[160:167], v[148:151]
	v_mfma_f32_16x16x128_f8f6f4 v[144:147], v[8:15], v[160:167], v[144:147]
	v_mfma_f32_16x16x128_f8f6f4 v[132:135], v[0:7], v[168:175], v[132:135]
	v_mfma_f32_16x16x128_f8f6f4 v[128:131], v[8:15], v[168:175], v[128:131]
	v_mfma_f32_16x16x128_f8f6f4 v[116:119], v[0:7], v[176:183], v[116:119]
	v_mfma_f32_16x16x128_f8f6f4 v[112:115], v[8:15], v[176:183], v[112:115]
	v_mfma_f32_16x16x128_f8f6f4 v[100:103], v[0:7], v[232:239], v[100:103]
	v_mfma_f32_16x16x128_f8f6f4 v[96:99], v[8:15], v[232:239], v[96:99]
	s_setprio 0
	s_barrier
	s_mov_b32 m0, s56
	v_lshl_add_u64 v[160:161], s[6:7], 0, v[184:185]
	s_add_u32 s50, s6, 0x20000
	ds_read_b128 v[168:171], v225 offset:16384
	ds_read_b128 v[172:175], v225 offset:17408
	ds_read_b128 v[176:179], v225 offset:18432
	ds_read_b128 v[180:183], v225 offset:19456
	ds_read_b128 v[232:235], v225 offset:20480
	ds_read_b128 v[236:239], v225 offset:21504
	ds_read_b128 v[240:243], v225 offset:22528
	ds_read_b128 v[244:247], v225 offset:23552
	global_load_lds_dwordx4 v[160:161], off
	v_lshl_add_u64 v[162:163], s[6:7], 0, v[186:187]
	s_mov_b32 m0, s57
	s_addc_u32 s51, s7, 0
	global_load_lds_dwordx4 v[162:163], off
	v_lshl_add_u64 v[164:165], s[50:51], 0, v[184:185]
	s_mov_b32 m0, s58
	v_lshl_add_u64 v[166:167], s[46:47], 0, v[190:191]
	global_load_lds_dwordx4 v[164:165], off
	v_lshl_add_u64 v[164:165], s[50:51], 0, v[186:187]
	s_mov_b32 m0, s59
	s_nop 0
	global_load_lds_dwordx4 v[164:165], off
	s_waitcnt vmcnt(6)
	s_waitcnt lgkmcnt(0)
	s_barrier
	s_setprio 1
	s_waitcnt lgkmcnt(0)
	v_mfma_f32_16x16x128_f8f6f4 v[84:87], v[16:23], v[168:175], v[84:87]
	v_mfma_f32_16x16x128_f8f6f4 v[80:83], v[24:31], v[168:175], v[80:83]
	v_mfma_f32_16x16x128_f8f6f4 v[68:71], v[16:23], v[176:183], v[68:71]
	v_mfma_f32_16x16x128_f8f6f4 v[64:67], v[24:31], v[176:183], v[64:67]
	v_mfma_f32_16x16x128_f8f6f4 v[56:59], v[16:23], v[232:239], v[56:59]
	v_mfma_f32_16x16x128_f8f6f4 v[48:51], v[24:31], v[232:239], v[48:51]
	v_mfma_f32_16x16x128_f8f6f4 v[40:43], v[16:23], v[240:247], v[40:43]
	v_mfma_f32_16x16x128_f8f6f4 v[32:35], v[24:31], v[240:247], v[32:35]
	s_setprio 0
	v_lshl_add_u64 v[164:165], s[46:47], 0, v[188:189]
	s_mov_b32 m0, s55
	s_nop 0
	global_load_lds_dwordx4 v[164:165], off
	s_mov_b32 m0, s60
	s_nop 0
	global_load_lds_dwordx4 v[166:167], off
	s_setprio 1
	v_mfma_f32_16x16x128_f8f6f4 v[92:95], v[0:7], v[168:175], v[92:95]
	v_mfma_f32_16x16x128_f8f6f4 v[88:91], v[8:15], v[168:175], v[88:91]
	v_mfma_f32_16x16x128_f8f6f4 v[76:79], v[0:7], v[176:183], v[76:79]
	v_mfma_f32_16x16x128_f8f6f4 v[72:75], v[8:15], v[176:183], v[72:75]
	v_mfma_f32_16x16x128_f8f6f4 v[60:63], v[0:7], v[232:239], v[60:63]
	v_mfma_f32_16x16x128_f8f6f4 v[52:55], v[8:15], v[232:239], v[52:55]
	v_mfma_f32_16x16x128_f8f6f4 v[44:47], v[0:7], v[240:247], v[44:47]
	v_mfma_f32_16x16x128_f8f6f4 v[36:39], v[8:15], v[240:247], v[36:39]
	s_setprio 0
	s_barrier
	ds_read_b128 v[4:7], v219
	ds_read_b128 v[8:11], v220
	ds_read_b128 v[0:3], v211
	ds_read_b128 v[16:19], v212
	ds_read_b128 v[12:15], v221
	ds_read_b128 v[20:23], v222
	ds_read_b128 v[24:27], v223
	ds_read_b128 v[28:31], v224
	s_add_u32 s46, s46, 0x20000
	s_addc_u32 s47, s47, 0
	s_mov_b32 m0, s61
	v_lshl_add_u64 v[202:203], s[46:47], 0, v[188:189]
	ds_read_b128 v[168:171], v225 offset:32768
	ds_read_b128 v[172:175], v225 offset:33792
	ds_read_b128 v[176:179], v225 offset:34816
	ds_read_b128 v[180:183], v225 offset:35840
	ds_read_b128 v[232:235], v225 offset:36864
	ds_read_b128 v[236:239], v225 offset:37888
	ds_read_b128 v[240:243], v225 offset:38912
	ds_read_b128 v[244:247], v225 offset:39936
	global_load_lds_dwordx4 v[202:203], off
	v_lshl_add_u64 v[202:203], s[46:47], 0, v[190:191]
	s_mov_b32 m0, s62
	s_nop 0
	global_load_lds_dwordx4 v[202:203], off
	s_waitcnt vmcnt(8)
	s_waitcnt lgkmcnt(0)
	s_barrier
	s_setprio 1
	s_waitcnt lgkmcnt(0)
	v_mfma_f32_16x16x128_f8f6f4 v[156:159], v[0:7], v[168:175], v[156:159]
	v_mfma_f32_16x16x128_f8f6f4 v[152:155], v[8:15], v[168:175], v[152:155]
	v_mfma_f32_16x16x128_f8f6f4 v[140:143], v[0:7], v[176:183], v[140:143]
	v_mfma_f32_16x16x128_f8f6f4 v[136:139], v[8:15], v[176:183], v[136:139]
	v_mfma_f32_16x16x128_f8f6f4 v[124:127], v[0:7], v[232:239], v[124:127]
	v_mfma_f32_16x16x128_f8f6f4 v[120:123], v[8:15], v[232:239], v[120:123]
	v_mfma_f32_16x16x128_f8f6f4 v[108:111], v[0:7], v[240:247], v[108:111]
	v_mfma_f32_16x16x128_f8f6f4 v[104:107], v[8:15], v[240:247], v[104:107]
	s_setprio 0
	s_setprio 1
	v_mfma_f32_16x16x128_f8f6f4 v[148:151], v[16:23], v[168:175], v[148:151]
	v_mfma_f32_16x16x128_f8f6f4 v[144:147], v[24:31], v[168:175], v[144:147]
	v_mfma_f32_16x16x128_f8f6f4 v[132:135], v[16:23], v[176:183], v[132:135]
	v_mfma_f32_16x16x128_f8f6f4 v[128:131], v[24:31], v[176:183], v[128:131]
	v_mfma_f32_16x16x128_f8f6f4 v[116:119], v[16:23], v[232:239], v[116:119]
	v_mfma_f32_16x16x128_f8f6f4 v[112:115], v[24:31], v[232:239], v[112:115]
	v_mfma_f32_16x16x128_f8f6f4 v[100:103], v[16:23], v[240:247], v[100:103]
	v_mfma_f32_16x16x128_f8f6f4 v[96:99], v[24:31], v[240:247], v[96:99]
	s_setprio 0
	s_barrier
	s_mov_b32 m0, s67
	v_lshl_add_u64 v[160:161], v[160:161], 0, s[24:25]
	s_add_u32 s6, s6, 0x20080
	ds_read_b128 v[168:171], v225 offset:49152
	ds_read_b128 v[172:175], v225 offset:50176
	ds_read_b128 v[176:179], v225 offset:51200
	ds_read_b128 v[180:183], v225 offset:52224
	ds_read_b128 v[232:235], v225 offset:53248
	ds_read_b128 v[236:239], v225 offset:54272
	ds_read_b128 v[240:243], v225 offset:55296
	ds_read_b128 v[244:247], v225 offset:56320
	global_load_lds_dwordx4 v[160:161], off
	v_lshl_add_u64 v[160:161], v[162:163], 0, s[24:25]
	s_mov_b32 m0, s68
	s_addc_u32 s7, s7, 0
	global_load_lds_dwordx4 v[160:161], off
	v_lshl_add_u64 v[160:161], s[6:7], 0, v[184:185]
	s_mov_b32 m0, s71
	s_nop 0
	global_load_lds_dwordx4 v[160:161], off
	v_lshl_add_u64 v[160:161], s[6:7], 0, v[186:187]
	s_mov_b32 m0, s78
	s_nop 0
	global_load_lds_dwordx4 v[160:161], off
	s_waitcnt vmcnt(6)
	s_waitcnt lgkmcnt(0)
	s_barrier
	s_setprio 1
	s_waitcnt lgkmcnt(0)
	v_mfma_f32_16x16x128_f8f6f4 v[84:87], v[0:7], v[168:175], v[84:87]
	v_mfma_f32_16x16x128_f8f6f4 v[80:83], v[8:15], v[168:175], v[80:83]
	v_mfma_f32_16x16x128_f8f6f4 v[68:71], v[0:7], v[176:183], v[68:71]
	v_mfma_f32_16x16x128_f8f6f4 v[64:67], v[8:15], v[176:183], v[64:67]
	v_mfma_f32_16x16x128_f8f6f4 v[56:59], v[0:7], v[232:239], v[56:59]
	v_mfma_f32_16x16x128_f8f6f4 v[48:51], v[8:15], v[232:239], v[48:51]
	v_mfma_f32_16x16x128_f8f6f4 v[40:43], v[0:7], v[240:247], v[40:43]
	v_mfma_f32_16x16x128_f8f6f4 v[32:35], v[8:15], v[240:247], v[32:35]
	s_setprio 0
	v_lshl_add_u64 v[160:161], v[164:165], 0, s[24:25]
	s_mov_b32 m0, s69
	s_nop 0
	global_load_lds_dwordx4 v[160:161], off
	v_lshl_add_u64 v[160:161], v[166:167], 0, s[24:25]
	s_mov_b32 m0, s70
	s_nop 0
	global_load_lds_dwordx4 v[160:161], off
	s_setprio 1
	v_mfma_f32_16x16x128_f8f6f4 v[92:95], v[16:23], v[168:175], v[92:95]
	v_mfma_f32_16x16x128_f8f6f4 v[88:91], v[24:31], v[168:175], v[88:91]
	v_mfma_f32_16x16x128_f8f6f4 v[76:79], v[16:23], v[176:183], v[76:79]
	v_mfma_f32_16x16x128_f8f6f4 v[72:75], v[24:31], v[176:183], v[72:75]
	v_mfma_f32_16x16x128_f8f6f4 v[60:63], v[16:23], v[232:239], v[60:63]
	v_mfma_f32_16x16x128_f8f6f4 v[52:55], v[24:31], v[232:239], v[52:55]
	v_mfma_f32_16x16x128_f8f6f4 v[44:47], v[16:23], v[240:247], v[44:47]
	v_mfma_f32_16x16x128_f8f6f4 v[36:39], v[24:31], v[240:247], v[36:39]
	s_setprio 0
	s_barrier
	s_add_i32 s49, s49, 2
	s_add_u32 s2, s2, 0x100
	s_addc_u32 s3, s3, 0
	s_add_u32 s39, s39, 0x100
	s_addc_u32 s48, s48, 0
	s_cmp_gt_u32 s49, 5
	s_cbranch_scc0 .LBB0_3128
	s_nop 15
	s_nop 7
	s_and_b64 vcc, exec, s[26:27]
	s_cbranch_vccz .LBB0_3131
	s_barrier

.LBB0_3319:
	s_add_u32 s34, s90, s4
	s_addc_u32 s35, s91, s5
	s_add_u32 s71, s34, 0x21c00100
	s_addc_u32 s72, s35, 0
	s_cmpk_eq_i32 s4, 0x300
	v_lshl_add_u64 v[0:1], v[180:181], 0, s[4:5]
	s_cselect_b64 vcc, -1, 0
	v_cndmask_b32_e32 v183, v1, v167, vcc
	v_cndmask_b32_e32 v182, v0, v220, vcc
	ds_read_b128 v[8:11], v194
	ds_read_b128 v[12:15], v198
	ds_read_b128 v[24:27], v199
	ds_read_b128 v[28:31], v200
	ds_read_b128 v[0:3], v195
	ds_read_b128 v[4:7], v201
	ds_read_b128 v[16:19], v202
	ds_read_b128 v[20:23], v203
	s_and_b64 s[34:35], vcc, exec
	s_cselect_b32 s35, s9, s72
	s_cselect_b32 s34, s8, s71
	v_cndmask_b32_e32 v160, v219, v215, vcc
	v_cndmask_b32_e32 v184, v170, v216, vcc
	v_cndmask_b32_e32 v175, v172, v217, vcc
	v_cndmask_b32_e32 v173, v174, v218, vcc
	v_lshl_add_u64 v[186:187], v[178:179], 0, s[4:5]
	s_add_i32 m0, s0, 0xc000
	ds_read_b128 v[222:225], v212
	ds_read_b128 v[226:229], v212 offset:1024
	ds_read_b128 v[230:233], v212 offset:2048
	ds_read_b128 v[234:237], v212 offset:3072
	ds_read_b128 v[238:241], v212 offset:4096
	ds_read_b128 v[242:245], v212 offset:5120
	ds_read_b128 v[246:249], v212 offset:6144
	ds_read_b128 v[250:253], v212 offset:7168
	global_load_lds_dwordx4 v[186:187], off
	v_lshl_add_u64 v[186:187], v[176:177], 0, s[4:5]
	s_add_i32 m0, s0, 0xe000
	s_nop 0
	global_load_lds_dwordx4 v[186:187], off
	s_waitcnt vmcnt(8)
	s_waitcnt lgkmcnt(0)
	s_barrier
	s_setprio 1
	s_waitcnt lgkmcnt(0)
	v_mfma_f32_16x16x128_f8f6f4 v[156:159], v[8:15], v[222:229], v[156:159]
	v_mfma_f32_16x16x128_f8f6f4 v[152:155], v[24:31], v[222:229], v[152:155]
	v_mfma_f32_16x16x128_f8f6f4 v[140:143], v[8:15], v[230:237], v[140:143]
	v_mfma_f32_16x16x128_f8f6f4 v[136:139], v[24:31], v[230:237], v[136:139]
	v_mfma_f32_16x16x128_f8f6f4 v[124:127], v[8:15], v[238:245], v[124:127]
	v_mfma_f32_16x16x128_f8f6f4 v[120:123], v[24:31], v[238:245], v[120:123]
	v_mfma_f32_16x16x128_f8f6f4 v[108:111], v[8:15], v[246:253], v[108:111]
	v_mfma_f32_16x16x128_f8f6f4 v[104:107], v[24:31], v[246:253], v[104:107]
	s_setprio 0
	s_setprio 1
	v_mfma_f32_16x16x128_f8f6f4 v[148:151], v[0:7], v[222:229], v[148:151]
	v_mfma_f32_16x16x128_f8f6f4 v[144:147], v[16:23], v[222:229], v[144:147]
	v_mfma_f32_16x16x128_f8f6f4 v[132:135], v[0:7], v[230:237], v[132:135]
	v_mfma_f32_16x16x128_f8f6f4 v[128:131], v[16:23], v[230:237], v[128:131]
	v_mfma_f32_16x16x128_f8f6f4 v[116:119], v[0:7], v[238:245], v[116:119]
	v_mfma_f32_16x16x128_f8f6f4 v[112:115], v[16:23], v[238:245], v[112:115]
	v_mfma_f32_16x16x128_f8f6f4 v[100:103], v[0:7], v[246:253], v[100:103]
	v_mfma_f32_16x16x128_f8f6f4 v[96:99], v[16:23], v[246:253], v[96:99]
	s_setprio 0
	s_barrier
	s_mov_b32 m0, s38
	v_lshl_add_u64 v[186:187], v[182:183], 0, v[164:165]
	ds_read_b128 v[222:225], v212 offset:16384
	ds_read_b128 v[226:229], v212 offset:17408
	ds_read_b128 v[230:233], v212 offset:18432
	ds_read_b128 v[234:237], v212 offset:19456
	ds_read_b128 v[238:241], v212 offset:20480
	ds_read_b128 v[242:245], v212 offset:21504
	ds_read_b128 v[246:249], v212 offset:22528
	ds_read_b128 v[250:253], v212 offset:23552
	global_load_lds_dwordx4 v[186:187], off
	v_lshl_add_u64 v[188:189], v[182:183], 0, v[162:163]
	s_mov_b32 m0, s39
	v_lshl_add_u64 v[190:191], v[182:183], 0, s[12:13]
	global_load_lds_dwordx4 v[188:189], off
	v_lshl_add_u64 v[192:193], v[190:191], 0, v[164:165]
	s_mov_b32 m0, s40
	v_lshl_add_u64 v[190:191], v[190:191], 0, v[162:163]
	global_load_lds_dwordx4 v[192:193], off
	s_mov_b32 m0, s41
	v_mov_b32_e32 v185, v161
	global_load_lds_dwordx4 v[190:191], off
	s_mov_b32 m0, s0
	v_lshl_add_u64 v[190:191], s[34:35], 0, v[160:161]
	global_load_lds_dwordx4 v160, s[34:35]
	s_mov_b32 m0, s42
	s_nop 0
	global_load_lds_dwordx4 v184, s[34:35]
	s_waitcnt vmcnt(8)
	s_waitcnt lgkmcnt(0)
	v_lshl_add_u64 v[184:185], s[34:35], 0, v[184:185]
	s_barrier
	s_setprio 1
	s_waitcnt lgkmcnt(0)
	v_mfma_f32_16x16x128_f8f6f4 v[84:87], v[8:15], v[222:229], v[84:87]
	v_mfma_f32_16x16x128_f8f6f4 v[80:83], v[24:31], v[222:229], v[80:83]
	v_mfma_f32_16x16x128_f8f6f4 v[68:71], v[8:15], v[230:237], v[68:71]
	v_mfma_f32_16x16x128_f8f6f4 v[64:67], v[24:31], v[230:237], v[64:67]
	v_mfma_f32_16x16x128_f8f6f4 v[52:55], v[8:15], v[238:245], v[52:55]
	v_mfma_f32_16x16x128_f8f6f4 v[48:51], v[24:31], v[238:245], v[48:51]
	v_mfma_f32_16x16x128_f8f6f4 v[36:39], v[8:15], v[246:253], v[36:39]
	v_mfma_f32_16x16x128_f8f6f4 v[32:35], v[24:31], v[246:253], v[32:35]
	s_setprio 0
	s_setprio 1
	v_mfma_f32_16x16x128_f8f6f4 v[92:95], v[0:7], v[222:229], v[92:95]
	v_mfma_f32_16x16x128_f8f6f4 v[88:91], v[16:23], v[222:229], v[88:91]
	v_mfma_f32_16x16x128_f8f6f4 v[76:79], v[0:7], v[230:237], v[76:79]
	v_mfma_f32_16x16x128_f8f6f4 v[72:75], v[16:23], v[230:237], v[72:75]
	v_mfma_f32_16x16x128_f8f6f4 v[60:63], v[0:7], v[238:245], v[60:63]
	v_mfma_f32_16x16x128_f8f6f4 v[56:59], v[16:23], v[238:245], v[56:59]
	v_mfma_f32_16x16x128_f8f6f4 v[44:47], v[0:7], v[246:253], v[44:47]
	v_mfma_f32_16x16x128_f8f6f4 v[40:43], v[16:23], v[246:253], v[40:43]
	s_setprio 0
	s_barrier
	ds_read_b128 v[4:7], v204
	ds_read_b128 v[8:11], v205
	ds_read_b128 v[0:3], v196
	ds_read_b128 v[16:19], v197
	ds_read_b128 v[12:15], v206
	ds_read_b128 v[20:23], v207
	ds_read_b128 v[24:27], v208
	ds_read_b128 v[28:31], v209
	s_mov_b32 m0, s43
	ds_read_b128 v[222:225], v212 offset:32768
	ds_read_b128 v[226:229], v212 offset:33792
	ds_read_b128 v[230:233], v212 offset:34816
	ds_read_b128 v[234:237], v212 offset:35840
	ds_read_b128 v[238:241], v212 offset:36864
	ds_read_b128 v[242:245], v212 offset:37888
	ds_read_b128 v[246:249], v212 offset:38912
	ds_read_b128 v[250:253], v212 offset:39936
	global_load_lds_dwordx4 v175, s[34:35]
	s_mov_b32 m0, s44
	s_nop 0
	global_load_lds_dwordx4 v173, s[34:35]
	s_waitcnt vmcnt(8)
	s_waitcnt lgkmcnt(0)
	s_barrier
	s_setprio 1
	s_waitcnt lgkmcnt(0)
	v_mfma_f32_16x16x128_f8f6f4 v[156:159], v[0:7], v[222:229], v[156:159]
	v_mfma_f32_16x16x128_f8f6f4 v[152:155], v[8:15], v[222:229], v[152:155]
	v_mfma_f32_16x16x128_f8f6f4 v[140:143], v[0:7], v[230:237], v[140:143]
	v_mfma_f32_16x16x128_f8f6f4 v[136:139], v[8:15], v[230:237], v[136:139]
	v_mfma_f32_16x16x128_f8f6f4 v[124:127], v[0:7], v[238:245], v[124:127]
	v_mfma_f32_16x16x128_f8f6f4 v[120:123], v[8:15], v[238:245], v[120:123]
	v_mfma_f32_16x16x128_f8f6f4 v[108:111], v[0:7], v[246:253], v[108:111]
	v_mfma_f32_16x16x128_f8f6f4 v[104:107], v[8:15], v[246:253], v[104:107]
	s_setprio 0
	s_setprio 1
	v_mfma_f32_16x16x128_f8f6f4 v[148:151], v[16:23], v[222:229], v[148:151]
	v_mfma_f32_16x16x128_f8f6f4 v[144:147], v[24:31], v[222:229], v[144:147]
	v_mfma_f32_16x16x128_f8f6f4 v[132:135], v[16:23], v[230:237], v[132:135]
	v_mfma_f32_16x16x128_f8f6f4 v[128:131], v[24:31], v[230:237], v[128:131]
	v_mfma_f32_16x16x128_f8f6f4 v[116:119], v[16:23], v[238:245], v[116:119]
	v_mfma_f32_16x16x128_f8f6f4 v[112:115], v[24:31], v[238:245], v[112:115]
	v_mfma_f32_16x16x128_f8f6f4 v[100:103], v[16:23], v[246:253], v[100:103]
	v_mfma_f32_16x16x128_f8f6f4 v[96:99], v[24:31], v[246:253], v[96:99]
	s_setprio 0
	s_barrier
	s_mov_b32 m0, s45
	v_lshl_add_u64 v[186:187], v[186:187], 0, s[16:17]
	ds_read_b128 v[222:225], v212 offset:49152
	ds_read_b128 v[226:229], v212 offset:50176
	ds_read_b128 v[230:233], v212 offset:51200
	ds_read_b128 v[234:237], v212 offset:52224
	ds_read_b128 v[238:241], v212 offset:53248
	ds_read_b128 v[242:245], v212 offset:54272
	ds_read_b128 v[246:249], v212 offset:55296
	ds_read_b128 v[250:253], v212 offset:56320
	global_load_lds_dwordx4 v[186:187], off
	v_lshl_add_u64 v[186:187], v[188:189], 0, s[16:17]
	s_mov_b32 m0, s46
	v_lshl_add_u64 v[182:183], v[182:183], 0, s[24:25]
	global_load_lds_dwordx4 v[186:187], off
	v_lshl_add_u64 v[186:187], v[182:183], 0, v[164:165]
	s_mov_b32 m0, s49
	v_lshl_add_u64 v[182:183], v[182:183], 0, v[162:163]
	global_load_lds_dwordx4 v[186:187], off
	s_mov_b32 m0, s50
	s_nop 0
	global_load_lds_dwordx4 v[182:183], off
	s_waitcnt vmcnt(6)
	s_waitcnt lgkmcnt(0)
	s_barrier
	s_setprio 1
	s_waitcnt lgkmcnt(0)
	v_mfma_f32_16x16x128_f8f6f4 v[84:87], v[0:7], v[222:229], v[84:87]
	v_mfma_f32_16x16x128_f8f6f4 v[80:83], v[8:15], v[222:229], v[80:83]
	v_mfma_f32_16x16x128_f8f6f4 v[68:71], v[0:7], v[230:237], v[68:71]
	v_mfma_f32_16x16x128_f8f6f4 v[64:67], v[8:15], v[230:237], v[64:67]
	v_mfma_f32_16x16x128_f8f6f4 v[52:55], v[0:7], v[238:245], v[52:55]
	v_mfma_f32_16x16x128_f8f6f4 v[48:51], v[8:15], v[238:245], v[48:51]
	v_mfma_f32_16x16x128_f8f6f4 v[36:39], v[0:7], v[246:253], v[36:39]
	v_mfma_f32_16x16x128_f8f6f4 v[32:35], v[8:15], v[246:253], v[32:35]
	s_setprio 0
	v_lshl_add_u64 v[182:183], v[190:191], 0, s[16:17]
	s_mov_b32 m0, s47
	s_nop 0
	global_load_lds_dwordx4 v[182:183], off
	v_lshl_add_u64 v[182:183], v[184:185], 0, s[16:17]
	s_mov_b32 m0, s48
	s_nop 0
	global_load_lds_dwordx4 v[182:183], off
	s_setprio 1
	v_mfma_f32_16x16x128_f8f6f4 v[92:95], v[16:23], v[222:229], v[92:95]
	v_mfma_f32_16x16x128_f8f6f4 v[88:91], v[24:31], v[222:229], v[88:91]
	v_mfma_f32_16x16x128_f8f6f4 v[76:79], v[16:23], v[230:237], v[76:79]
	v_mfma_f32_16x16x128_f8f6f4 v[72:75], v[24:31], v[230:237], v[72:75]
	v_mfma_f32_16x16x128_f8f6f4 v[60:63], v[16:23], v[238:245], v[60:63]
	v_mfma_f32_16x16x128_f8f6f4 v[56:59], v[24:31], v[238:245], v[56:59]
	v_mfma_f32_16x16x128_f8f6f4 v[44:47], v[16:23], v[246:253], v[44:47]
	v_mfma_f32_16x16x128_f8f6f4 v[40:43], v[24:31], v[246:253], v[40:43]
	s_setprio 0
	s_barrier
	s_add_i32 s31, s31, 2
	s_add_u32 s4, s4, 0x100
	s_addc_u32 s5, s5, 0
	s_cmp_gt_u32 s31, 5
	s_cbranch_scc0 .LBB0_3319
	s_nop 15
	s_nop 7
	s_and_b64 vcc, exec, s[26:27]
	s_cbranch_vccz .LBB0_3322
	s_barrier

.LBB0_3417:
	s_mov_b64 s[76:77], 0x100
	v_lshl_add_u64 v[0:1], v[168:169], 0, s[34:35]
	v_lshl_add_u64 v[0:1], v[0:1], 0, s[76:77]
	v_cndmask_b32_e64 v179, v1, v171, s[30:31]
	v_cndmask_b32_e64 v178, v0, v205, s[30:31]
	ds_read_b128 v[8:11], v185
	ds_read_b128 v[12:15], v189
	ds_read_b128 v[24:27], v190
	ds_read_b128 v[28:31], v191
	ds_read_b128 v[0:3], v186
	ds_read_b128 v[4:7], v192
	ds_read_b128 v[16:19], v193
	ds_read_b128 v[20:23], v194
	s_add_u32 s15, s22, s34
	s_addc_u32 s75, s23, s35
	s_add_u32 s78, s15, 0x100
	s_addc_u32 s79, s75, 0
	s_and_b64 s[36:37], s[30:31], exec
	s_cselect_b32 s37, s25, s79
	s_cselect_b32 s36, s74, s78
	s_add_u32 s34, s15, 0x10080
	s_addc_u32 s35, s75, 0
	s_add_i32 m0, s41, 0xc000
	s_add_i32 s15, s41, 0xe000
	s_add_u32 s30, s36, 0x10000
	s_addc_u32 s31, s37, 0
	v_lshl_add_u64 v[180:181], v[178:179], 0, s[0:1]
	v_lshl_add_u64 v[174:175], v[178:179], 0, s[10:11]
	v_lshl_add_u64 v[176:177], s[34:35], 0, v[164:165]
	ds_read_b128 v[206:209], v203
	ds_read_b128 v[210:213], v203 offset:1024
	ds_read_b128 v[214:217], v203 offset:2048
	ds_read_b128 v[218:221], v203 offset:3072
	ds_read_b128 v[222:225], v203 offset:4096
	ds_read_b128 v[226:229], v203 offset:5120
	ds_read_b128 v[230:233], v203 offset:6144
	ds_read_b128 v[234:237], v203 offset:7168
	global_load_lds_dwordx4 v[176:177], off
	v_lshl_add_u64 v[176:177], s[34:35], 0, v[166:167]
	s_mov_b32 m0, s15
	s_nop 0
	global_load_lds_dwordx4 v[176:177], off
	s_waitcnt vmcnt(8)
	s_waitcnt lgkmcnt(0)
	s_barrier
	s_setprio 1
	s_waitcnt lgkmcnt(0)
	v_mfma_f32_16x16x128_f8f6f4 v[156:159], v[8:15], v[206:213], v[156:159]
	v_mfma_f32_16x16x128_f8f6f4 v[152:155], v[24:31], v[206:213], v[152:155]
	v_mfma_f32_16x16x128_f8f6f4 v[140:143], v[8:15], v[214:221], v[140:143]
	v_mfma_f32_16x16x128_f8f6f4 v[136:139], v[24:31], v[214:221], v[136:139]
	v_mfma_f32_16x16x128_f8f6f4 v[124:127], v[8:15], v[222:229], v[124:127]
	v_mfma_f32_16x16x128_f8f6f4 v[120:123], v[24:31], v[222:229], v[120:123]
	v_mfma_f32_16x16x128_f8f6f4 v[108:111], v[8:15], v[230:237], v[108:111]
	v_mfma_f32_16x16x128_f8f6f4 v[104:107], v[24:31], v[230:237], v[104:107]
	s_setprio 0
	s_setprio 1
	v_mfma_f32_16x16x128_f8f6f4 v[148:151], v[0:7], v[206:213], v[148:151]
	v_mfma_f32_16x16x128_f8f6f4 v[144:147], v[16:23], v[206:213], v[144:147]
	v_mfma_f32_16x16x128_f8f6f4 v[132:135], v[0:7], v[214:221], v[132:135]
	v_mfma_f32_16x16x128_f8f6f4 v[128:131], v[16:23], v[214:221], v[128:131]
	v_mfma_f32_16x16x128_f8f6f4 v[116:119], v[0:7], v[222:229], v[116:119]
	v_mfma_f32_16x16x128_f8f6f4 v[112:115], v[16:23], v[222:229], v[112:115]
	v_mfma_f32_16x16x128_f8f6f4 v[92:95], v[0:7], v[230:237], v[92:95]
	v_mfma_f32_16x16x128_f8f6f4 v[88:91], v[16:23], v[230:237], v[88:91]
	s_setprio 0
	s_barrier
	s_mov_b32 m0, s42
	v_lshl_add_u64 v[176:177], v[178:179], 0, v[162:163]
	ds_read_b128 v[206:209], v203 offset:16384
	ds_read_b128 v[210:213], v203 offset:17408
	ds_read_b128 v[214:217], v203 offset:18432
	ds_read_b128 v[218:221], v203 offset:19456
	ds_read_b128 v[222:225], v203 offset:20480
	ds_read_b128 v[226:229], v203 offset:21504
	ds_read_b128 v[230:233], v203 offset:22528
	ds_read_b128 v[234:237], v203 offset:23552
	global_load_lds_dwordx4 v[176:177], off
	v_lshl_add_u64 v[178:179], v[178:179], 0, v[160:161]
	s_mov_b32 m0, s43
	v_lshl_add_u64 v[182:183], v[180:181], 0, v[162:163]
	global_load_lds_dwordx4 v[178:179], off
	s_mov_b32 m0, s44
	v_lshl_add_u64 v[180:181], v[180:181], 0, v[160:161]
	global_load_lds_dwordx4 v[182:183], off
	s_mov_b32 m0, s45
	v_lshl_add_u64 v[182:183], s[36:37], 0, v[166:167]
	global_load_lds_dwordx4 v[180:181], off
	s_waitcnt vmcnt(6)
	s_waitcnt lgkmcnt(0)
	s_barrier
	s_setprio 1
	s_waitcnt lgkmcnt(0)
	v_mfma_f32_16x16x128_f8f6f4 v[84:87], v[8:15], v[206:213], v[84:87]
	v_mfma_f32_16x16x128_f8f6f4 v[76:79], v[24:31], v[206:213], v[76:79]
	v_mfma_f32_16x16x128_f8f6f4 v[60:63], v[8:15], v[214:221], v[60:63]
	v_mfma_f32_16x16x128_f8f6f4 v[48:51], v[24:31], v[214:221], v[48:51]
	v_mfma_f32_16x16x128_f8f6f4 v[68:71], v[8:15], v[222:229], v[68:71]
	v_mfma_f32_16x16x128_f8f6f4 v[56:59], v[24:31], v[222:229], v[56:59]
	v_mfma_f32_16x16x128_f8f6f4 v[44:47], v[8:15], v[230:237], v[44:47]
	v_mfma_f32_16x16x128_f8f6f4 v[36:39], v[24:31], v[230:237], v[36:39]
	s_setprio 0
	v_lshl_add_u64 v[180:181], s[36:37], 0, v[164:165]
	s_mov_b32 m0, s41
	s_nop 0
	global_load_lds_dwordx4 v[180:181], off
	s_mov_b32 m0, s46
	s_nop 0
	global_load_lds_dwordx4 v[182:183], off
	s_setprio 1
	v_mfma_f32_16x16x128_f8f6f4 v[100:103], v[0:7], v[206:213], v[100:103]
	v_mfma_f32_16x16x128_f8f6f4 v[96:99], v[16:23], v[206:213], v[96:99]
	v_mfma_f32_16x16x128_f8f6f4 v[80:83], v[0:7], v[214:221], v[80:83]
	v_mfma_f32_16x16x128_f8f6f4 v[72:75], v[16:23], v[214:221], v[72:75]
	v_mfma_f32_16x16x128_f8f6f4 v[64:67], v[0:7], v[222:229], v[64:67]
	v_mfma_f32_16x16x128_f8f6f4 v[52:55], v[16:23], v[222:229], v[52:55]
	v_mfma_f32_16x16x128_f8f6f4 v[40:43], v[0:7], v[230:237], v[40:43]
	v_mfma_f32_16x16x128_f8f6f4 v[32:35], v[16:23], v[230:237], v[32:35]
	s_setprio 0
	s_barrier
	ds_read_b128 v[4:7], v195
	ds_read_b128 v[8:11], v196
	ds_read_b128 v[0:3], v187
	ds_read_b128 v[16:19], v188
	ds_read_b128 v[12:15], v197
	ds_read_b128 v[20:23], v198
	ds_read_b128 v[24:27], v199
	ds_read_b128 v[28:31], v200
	s_mov_b32 m0, s47
	v_lshl_add_u64 v[238:239], s[30:31], 0, v[164:165]
	ds_read_b128 v[206:209], v203 offset:32768
	ds_read_b128 v[210:213], v203 offset:33792
	ds_read_b128 v[214:217], v203 offset:34816
	ds_read_b128 v[218:221], v203 offset:35840
	ds_read_b128 v[222:225], v203 offset:36864
	ds_read_b128 v[226:229], v203 offset:37888
	ds_read_b128 v[230:233], v203 offset:38912
	ds_read_b128 v[234:237], v203 offset:39936
	global_load_lds_dwordx4 v[238:239], off
	v_lshl_add_u64 v[238:239], s[30:31], 0, v[166:167]
	s_mov_b32 m0, s48
	s_nop 0
	global_load_lds_dwordx4 v[238:239], off
	s_waitcnt vmcnt(8)
	s_waitcnt lgkmcnt(0)
	s_barrier
	s_setprio 1
	s_waitcnt lgkmcnt(0)
	v_mfma_f32_16x16x128_f8f6f4 v[156:159], v[0:7], v[206:213], v[156:159]
	v_mfma_f32_16x16x128_f8f6f4 v[152:155], v[8:15], v[206:213], v[152:155]
	v_mfma_f32_16x16x128_f8f6f4 v[140:143], v[0:7], v[214:221], v[140:143]
	v_mfma_f32_16x16x128_f8f6f4 v[136:139], v[8:15], v[214:221], v[136:139]
	v_mfma_f32_16x16x128_f8f6f4 v[124:127], v[0:7], v[222:229], v[124:127]
	v_mfma_f32_16x16x128_f8f6f4 v[120:123], v[8:15], v[222:229], v[120:123]
	v_mfma_f32_16x16x128_f8f6f4 v[108:111], v[0:7], v[230:237], v[108:111]
	v_mfma_f32_16x16x128_f8f6f4 v[104:107], v[8:15], v[230:237], v[104:107]
	s_setprio 0
	s_setprio 1
	v_mfma_f32_16x16x128_f8f6f4 v[148:151], v[16:23], v[206:213], v[148:151]
	v_mfma_f32_16x16x128_f8f6f4 v[144:147], v[24:31], v[206:213], v[144:147]
	v_mfma_f32_16x16x128_f8f6f4 v[132:135], v[16:23], v[214:221], v[132:135]
	v_mfma_f32_16x16x128_f8f6f4 v[128:131], v[24:31], v[214:221], v[128:131]
	v_mfma_f32_16x16x128_f8f6f4 v[116:119], v[16:23], v[222:229], v[116:119]
	v_mfma_f32_16x16x128_f8f6f4 v[112:115], v[24:31], v[222:229], v[112:115]
	v_mfma_f32_16x16x128_f8f6f4 v[92:95], v[16:23], v[230:237], v[92:95]
	v_mfma_f32_16x16x128_f8f6f4 v[88:91], v[24:31], v[230:237], v[88:91]
	s_setprio 0
	s_barrier
	s_mov_b32 m0, s50
	v_lshl_add_u64 v[176:177], v[176:177], 0, s[8:9]
	ds_read_b128 v[206:209], v203 offset:49152
	ds_read_b128 v[210:213], v203 offset:50176
	ds_read_b128 v[214:217], v203 offset:51200
	ds_read_b128 v[218:221], v203 offset:52224
	ds_read_b128 v[222:225], v203 offset:53248
	ds_read_b128 v[226:229], v203 offset:54272
	ds_read_b128 v[230:233], v203 offset:55296
	ds_read_b128 v[234:237], v203 offset:56320
	global_load_lds_dwordx4 v[176:177], off
	v_lshl_add_u64 v[176:177], v[178:179], 0, s[8:9]
	s_mov_b32 m0, s51
	s_nop 0
	global_load_lds_dwordx4 v[176:177], off
	v_lshl_add_u64 v[176:177], v[174:175], 0, v[162:163]
	s_mov_b32 m0, s54
	v_lshl_add_u64 v[174:175], v[174:175], 0, v[160:161]
	global_load_lds_dwordx4 v[176:177], off
	s_mov_b32 m0, s55
	s_nop 0
	global_load_lds_dwordx4 v[174:175], off
	s_waitcnt vmcnt(6)
	s_waitcnt lgkmcnt(0)
	s_barrier
	s_setprio 1
	s_waitcnt lgkmcnt(0)
	v_mfma_f32_16x16x128_f8f6f4 v[84:87], v[0:7], v[206:213], v[84:87]
	v_mfma_f32_16x16x128_f8f6f4 v[76:79], v[8:15], v[206:213], v[76:79]
	v_mfma_f32_16x16x128_f8f6f4 v[60:63], v[0:7], v[214:221], v[60:63]
	v_mfma_f32_16x16x128_f8f6f4 v[48:51], v[8:15], v[214:221], v[48:51]
	v_mfma_f32_16x16x128_f8f6f4 v[68:71], v[0:7], v[222:229], v[68:71]
	v_mfma_f32_16x16x128_f8f6f4 v[56:59], v[8:15], v[222:229], v[56:59]
	v_mfma_f32_16x16x128_f8f6f4 v[44:47], v[0:7], v[230:237], v[44:47]
	v_mfma_f32_16x16x128_f8f6f4 v[36:39], v[8:15], v[230:237], v[36:39]
	s_setprio 0
	v_lshl_add_u64 v[174:175], v[180:181], 0, s[8:9]
	s_mov_b32 m0, s52
	s_nop 0
	global_load_lds_dwordx4 v[174:175], off
	v_lshl_add_u64 v[174:175], v[182:183], 0, s[8:9]
	s_mov_b32 m0, s53
	s_nop 0
	global_load_lds_dwordx4 v[174:175], off
	s_setprio 1
	v_mfma_f32_16x16x128_f8f6f4 v[100:103], v[16:23], v[206:213], v[100:103]
	v_mfma_f32_16x16x128_f8f6f4 v[96:99], v[24:31], v[206:213], v[96:99]
	v_mfma_f32_16x16x128_f8f6f4 v[80:83], v[16:23], v[214:221], v[80:83]
	v_mfma_f32_16x16x128_f8f6f4 v[72:75], v[24:31], v[214:221], v[72:75]
	v_mfma_f32_16x16x128_f8f6f4 v[64:67], v[16:23], v[222:229], v[64:67]
	v_mfma_f32_16x16x128_f8f6f4 v[52:55], v[24:31], v[222:229], v[52:55]
	v_mfma_f32_16x16x128_f8f6f4 v[40:43], v[16:23], v[230:237], v[40:43]
	v_mfma_f32_16x16x128_f8f6f4 v[32:35], v[24:31], v[230:237], v[32:35]
	s_setprio 0
	s_barrier
	s_andn2_b64 vcc, exec, s[28:29]
	s_mov_b64 s[30:31], -1
	s_mov_b64 s[28:29], 0
	s_mov_b64 s[34:35], 0x100
	s_cbranch_vccz .LBB0_3417
	s_nop 15
	s_nop 7
	s_and_b64 vcc, exec, s[12:13]
	s_cbranch_vccz .LBB0_3420
	s_barrier
